# stacked: MoE gate/up half-unit epilogues rewritten like the full ones, barrier leader arrival atomic made no-return (division and generation bump skipped), arrive-side division replaced by barrier cou
# speedup vs baseline: 1.0327x; 1.0039x over previous
.LBB0_107:
	s_add_i32 s3, 0, 0x24808
	v_mov_b32_e32 v3, s3
	ds_read_b32 v4, v3
	s_mov_b64 s[0:1], exec
	v_mbcnt_lo_u32_b32 v2, s0, 0
	v_mbcnt_hi_u32_b32 v2, s1, v2
	v_cmp_eq_u32_e32 vcc, 0, v2
	s_waitcnt lgkmcnt(0)
	v_add_u32_e32 v4, 1, v4
	v_mov_b32_e32 v7, v4
	ds_write_b32 v3, v4
	s_and_saveexec_b64 s[8:9], vcc
	s_cbranch_execz .LBB0_109
	v_readlane_b32 s3, v249, 34
	s_lshl_b32 s3, s3, 8
	s_add_u32 s10, s94, s3
	s_addc_u32 s11, s95, 0
	s_bcnt1_i32_b64 s0, s[0:1]
	v_mov_b32_e32 v3, 0x1000
	v_mov_b32_e32 v4, s0
	global_atomic_add v3, v3, v4, s[10:11] offset:1024 sc0
.LBB0_109:
	s_or_b64 exec, exec, s[8:9]
	s_waitcnt vmcnt(0)
	v_readfirstlane_b32 s0, v3
	s_nop 1
	v_add_u32_e32 v2, s0, v2
	v_add_u32_e32 v5, 1, v2
	v_mul_lo_u32 v1, v1, v7
	v_add_u32_e32 v2, -1, v7
	v_cmp_eq_u32_e64 s[0:1], v5, v1
	v_cmp_ne_u32_e32 vcc, v5, v1
	s_nop 0
	v_cndmask_b32_e64 v1, 0, 1, s[0:1]
	s_add_i32 s0, 0, 0x2480c
	v_mov_b32_e32 v3, s0
	s_add_i32 s0, 0, 0x24810
	ds_write_b32 v3, v1
	v_mov_b32_e32 v1, s0
	ds_write_b32 v1, v2
	s_and_saveexec_b64 s[0:1], vcc
	s_xor_b64 s[0:1], exec, s[0:1]
	s_cbranch_execz .LBB0_112
	s_add_i32 s3, 0, 0x24808
	v_mov_b32_e32 v0, s3
	ds_read_b32 v0, v0
	s_waitcnt lgkmcnt(0)
	v_and_b32_e32 v0, 1, v0
	v_cmp_eq_u32_e32 vcc, 0, v0
	s_cbranch_vccnz .LBB0_112
	buffer_inv sc1
	s_waitcnt vmcnt(0)
.LBB0_112:
	s_andn2_saveexec_b64 s[0:1], s[0:1]
	s_cbranch_execz .LBB0_119
	s_mov_b64 s[0:1], exec
	buffer_wbl2 sc1
	s_waitcnt lgkmcnt(0)
	s_waitcnt vmcnt(0)
	v_mbcnt_lo_u32_b32 v1, s0, 0
	v_mbcnt_hi_u32_b32 v1, s1, v1
	v_cmp_eq_u32_e32 vcc, 0, v1
	s_and_saveexec_b64 s[8:9], vcc
	s_cbranch_execz .LBB0_115
	s_bcnt1_i32_b64 s0, s[0:1]
	v_mov_b32_e32 v2, 0x3000
	v_mov_b32_e32 v3, s0
	global_atomic_add v2, v3, s[94:95] offset:1024
.LBB0_115:
	s_or_b64 exec, exec, s[8:9]
	s_branch .LBB0_119
	v_cvt_f32_u32_e32 v3, v0
	s_waitcnt vmcnt(0)
	v_readfirstlane_b32 s0, v2
	v_sub_u32_e32 v2, 0, v0
	v_rcp_iflag_f32_e32 v3, v3
	v_add_u32_e32 v1, s0, v1
	v_mul_f32_e32 v3, 0x4f7ffffe, v3
	v_cvt_u32_f32_e32 v3, v3
	v_mul_lo_u32 v2, v2, v3
	v_mul_hi_u32 v2, v3, v2
	v_add_u32_e32 v2, v3, v2
	v_mul_hi_u32 v2, v1, v2
	v_mul_lo_u32 v3, v2, v0
	v_sub_u32_e32 v3, v1, v3
	v_add_u32_e32 v4, 1, v2
	v_cmp_ge_u32_e32 vcc, v3, v0
	v_add_u32_e32 v1, 1, v1
	s_nop 0
	v_cndmask_b32_e32 v2, v2, v4, vcc
	v_sub_u32_e32 v4, v3, v0
	v_cndmask_b32_e32 v3, v3, v4, vcc
	v_add_u32_e32 v4, 1, v2
	v_cmp_ge_u32_e32 vcc, v3, v0
	s_nop 1
	v_cndmask_b32_e32 v2, v2, v4, vcc
	v_mul_lo_u32 v2, v0, v2
	v_add_u32_e32 v0, v2, v0
	v_cmp_eq_u32_e32 vcc, v1, v0
	s_and_saveexec_b64 s[0:1], vcc
	s_cbranch_execz .LBB0_118
	s_mov_b64 s[8:9], exec
	v_mbcnt_lo_u32_b32 v0, s8, 0
	v_mbcnt_hi_u32_b32 v0, s9, v0
	v_cmp_eq_u32_e32 vcc, 0, v0
	s_and_b64 s[10:11], exec, vcc
	s_mov_b64 exec, s[10:11]
	s_cbranch_execz .LBB0_118
	s_bcnt1_i32_b64 s3, s[8:9]
	v_mov_b32_e32 v0, 0x3000
	v_mov_b32_e32 v1, s3
	global_atomic_add v0, v1, s[94:95] offset:1280

.LBB0_243:
	s_add_u32 s49, s78, 0x1400000
	s_addc_u32 s50, s79, 0
	s_add_u32 s8, s78, 0x100000
	s_addc_u32 s9, s79, 0
	s_add_u32 s10, s78, 0x300000
	s_addc_u32 s11, s79, 0
	s_add_u32 s3, s78, 0x12500000
	s_addc_u32 s42, s79, 0
	s_add_u32 s43, s78, 0x14500000
	s_addc_u32 s44, s79, 0
	s_add_u32 s45, s78, 0x14d00000
	s_addc_u32 s48, s79, 0
	s_cmpk_gt_i32 s33, 0x17f
	s_cselect_b64 s[12:13], -1, 0
	s_lshl_b32 s5, s33, 1
	s_sub_i32 s5, 0x300, s5
	s_cmp_gt_i32 s5, s33
	s_cselect_b64 s[14:15], -1, 0
	s_or_b64 s[14:15], s[12:13], s[14:15]
	s_andn2_b64 vcc, exec, s[0:1]
	s_xor_b64 s[12:13], s[14:15], -1
	s_cbranch_vccnz .LBB0_328
	v_bfe_i32 v3, v0, 27, 1
	v_lshlrev_b32_e32 v1, 4, v0
	v_lshrrev_b32_e32 v3, 22, v3
	v_add_u32_e32 v3, v1, v3
	v_and_b32_e32 v3, 0xfffffc00, v3
	v_ashrrev_i32_e32 v2, 31, v0
	v_sub_u32_e32 v1, v1, v3
	v_lshrrev_b32_e32 v2, 26, v2
	v_lshrrev_b32_e32 v3, 4, v1
	v_add_u32_e32 v2, v0, v2
	v_bitop3_b32 v3, v3, v1, 32 bitop3:0x6c
	v_ashrrev_i32_e32 v1, 31, v1
	v_ashrrev_i32_e32 v2, 6, v2
	v_lshrrev_b32_e32 v1, 26, v1
	v_lshlrev_b32_e32 v4, 3, v2
	v_add_u32_e32 v1, v3, v1
	v_and_b32_e32 v4, -16, v4
	v_ashrrev_i32_e32 v1, 6, v1
	v_add_u32_e32 v4, v1, v4
	v_mul_i32_i24_e32 v5, 64, v1
	v_and_b32_e32 v1, 3, v1
	s_mov_b32 s5, 0x1fffe0
	s_ashr_i32 s1, s18, 6
	v_and_or_b32 v1, v4, s5, v1
	s_ashr_i32 s5, s4, 31
	s_ashr_i32 s0, s18, 8
	s_lshl_b32 s51, s1, 10
	s_lshl_b64 s[16:17], s[4:5], 19
	v_sub_u32_e32 v3, v3, v5
	v_mov_b32_e32 v5, 1
	s_add_u32 s30, s90, s16
	v_lshlrev_b32_e32 v2, 5, v2
	v_ashrrev_i16_sdwa v3, v5, sext(v3) dst_sel:DWORD dst_unused:UNUSED_PAD src0_sel:DWORD src1_sel:BYTE_0
	v_lshlrev_b32_e32 v5, 1, v4
	v_lshrrev_b32_e32 v6, 2, v4
	s_addc_u32 s31, s91, s17
	s_ashr_i32 s37, s36, 31
	v_and_b32_e32 v2, 32, v2
	v_bfe_i32 v3, v3, 0, 16
	v_and_b32_e32 v5, 24, v5
	v_and_b32_e32 v6, 4, v6
	s_lshl_b64 s[16:17], s[36:37], 19
	v_or3_b32 v1, v1, v6, v5
	v_add_lshl_u32 v2, v2, v3, 1
	s_add_u32 s34, s49, s16
	v_lshl_add_u32 v158, v1, 11, v2
	s_addc_u32 s35, s50, s17
	s_add_i32 s52, s51, 0
	s_mov_b64 s[16:17], s[34:35]
	s_add_i32 m0, s52, 0x10000
	v_lshl_add_u32 v159, v4, 11, v2
	global_load_lds_dwordx4 v158, s[16:17]
	s_add_u32 s16, s34, 0x20000
	s_addc_u32 s17, s35, 0
	s_add_i32 m0, s52, 0x12000
	s_mov_b32 s19, 0
	global_load_lds_dwordx4 v158, s[16:17]
	s_add_i32 m0, s52, 0x14000
	s_add_u32 s16, s34, 0x40000
	s_addc_u32 s17, s35, 0
	s_nop 0
	global_load_lds_dwordx4 v158, s[16:17]
	s_add_u32 s16, s34, 0x60000
	s_addc_u32 s17, s35, 0
	s_add_i32 m0, s52, 0x16000
	s_nop 0
	global_load_lds_dwordx4 v158, s[16:17]
	s_mov_b64 s[16:17], s[30:31]
	s_mov_b32 m0, s52
	s_nop 0
	global_load_lds_dwordx4 v159, s[16:17]
	s_add_u32 s16, s30, 0x20000
	s_addc_u32 s17, s31, 0
	s_add_i32 s53, s52, 0x2000
	s_mov_b32 m0, s53
	s_add_i32 s60, s52, 0x4000
	global_load_lds_dwordx4 v159, s[16:17]
	s_add_u32 s16, s30, 0x40000
	s_addc_u32 s17, s31, 0
	s_mov_b32 m0, s60
	s_nop 0
	global_load_lds_dwordx4 v159, s[16:17]
	s_add_u32 s16, s30, 0x60000
	s_addc_u32 s17, s31, 0
	s_add_i32 s61, s52, 0x6000
	s_mov_b32 m0, s61
	s_cmp_eq_u32 s0, 1
	global_load_lds_dwordx4 v159, s[16:17]
	s_cselect_b64 s[16:17], -1, 0
	s_cmp_lg_u32 s0, 1
	s_cbranch_scc1 .LBB0_246
	s_barrier
.LBB0_246:
	s_and_b32 s5, s1, 3
	s_ashr_i32 s64, s33, 31
	s_ashr_i32 s65, s2, 31
	s_lshl_b32 s68, s0, 6
	s_lshl_b32 s20, s0, 13
	s_lshl_b32 s21, s5, 12
	s_add_u32 s0, s34, 0x80
	s_addc_u32 s1, s35, 0
	s_waitcnt vmcnt(2)
	s_barrier
	s_add_i32 m0, s52, 0x18000
	v_lshlrev_b32_e32 v2, 6, v0
	global_load_lds_dwordx4 v158, s[0:1]
	s_add_u32 s0, s34, 0x20080
	s_addc_u32 s1, s35, 0
	s_add_i32 m0, s52, 0x1a000
	v_mov_b64_e32 v[144:145], 0x180
	global_load_lds_dwordx4 v158, s[0:1]
	s_add_u32 s0, s30, 0x80
	s_addc_u32 s1, s31, 0
	s_add_i32 s69, s52, 0x8000
	s_mov_b32 m0, s69
	v_mov_b32_e32 v147, 0
	global_load_lds_dwordx4 v159, s[0:1]
	s_add_u32 s0, s30, 0x20080
	s_addc_u32 s1, s31, 0
	s_add_i32 s70, s52, 0xa000
	s_mov_b32 m0, s70
	s_mov_b32 s74, 0
	global_load_lds_dwordx4 v159, s[0:1]
	s_add_i32 m0, s52, 0x1c000
	s_add_u32 s0, s34, 0x40080
	s_addc_u32 s1, s35, 0
	s_nop 0
	global_load_lds_dwordx4 v158, s[0:1]
	s_add_u32 s0, s34, 0x60080
	s_addc_u32 s1, s35, 0
	s_add_i32 m0, s52, 0x1e000
	s_cmpk_lt_u32 s18, 0x100
	global_load_lds_dwordx4 v158, s[0:1]
	v_and_b32_e32 v1, 48, v0
	s_movk_i32 s0, 0x3c0
	v_lshlrev_b32_e32 v0, 2, v0
	v_and_or_b32 v1, v2, s0, v1
	v_and_b32_e32 v0, 32, v0
	s_waitcnt vmcnt(6)
	v_bitop3_b32 v2, v1, s20, v0 bitop3:0xde
	v_bitop3_b32 v160, v1, s21, v0 bitop3:0xde
	s_cselect_b64 s[20:21], -1, 0
	s_add_i32 s72, 0, 0x10000
	s_add_i32 s73, 0, 0x14000
	s_lshl_b32 s71, s5, 6
	v_add_u32_e32 v161, s72, v160
	v_add_u32_e32 v162, s73, v160
	v_add_u32_e32 v163, 0, v2
	s_barrier
	s_branch .LBB0_249

.LBB0_252:
	ds_read_b128 v[40:43], v161
	ds_read_b128 v[44:47], v161 offset:1024
	ds_read_b128 v[56:59], v161 offset:2048
	ds_read_b128 v[60:63], v161 offset:3072
	ds_read_b128 v[148:151], v162
	ds_read_b128 v[152:155], v162 offset:1024
	ds_read_b128 v[164:167], v162 offset:2048
	ds_read_b128 v[168:171], v162 offset:3072
	s_add_u32 s25, s30, 0xfffa0080
	s_addc_u32 s34, s31, -1
	s_cmp_eq_u32 s23, 12
	s_cselect_b32 s35, s27, s34
	s_cselect_b32 s34, s26, s25
	s_cselect_b32 s40, s28, s5
	s_cselect_b32 s41, s29, s18
	s_add_u32 s38, s34, 0x80
	s_addc_u32 s39, s35, 0
	s_add_u32 s78, s30, 0xfffe0000
	v_mov_b32_e32 v146, v159
	s_addc_u32 s79, s31, -1
	ds_read_b128 v[172:175], v163
	ds_read_b128 v[176:179], v163 offset:1024
	ds_read_b128 v[180:183], v163 offset:2048
	ds_read_b128 v[184:187], v163 offset:3072
	ds_read_b128 v[188:191], v163 offset:4096
	ds_read_b128 v[192:195], v163 offset:5120
	ds_read_b128 v[196:199], v163 offset:6144
	ds_read_b128 v[200:203], v163 offset:7168
	s_add_i32 m0, s52, 0xc000
	s_nop 0
	global_load_lds_dwordx4 v146, s[78:79]
	s_mov_b64 s[78:79], s[30:31]
	s_add_i32 m0, s52, 0xe000
	s_nop 0
	global_load_lds_dwordx4 v159, s[78:79]
	s_waitcnt vmcnt(8)
	s_waitcnt lgkmcnt(0)
	s_barrier
	s_setprio 3
	v_mfma_f32_16x16x32_bf16 v[140:143], v[40:43], v[172:175], v[140:143]
	v_mfma_f32_16x16x32_bf16 v[132:135], v[56:59], v[172:175], v[132:135]
	v_mfma_f32_16x16x32_bf16 v[124:127], v[40:43], v[180:183], v[124:127]
	v_mfma_f32_16x16x32_bf16 v[116:119], v[56:59], v[180:183], v[116:119]
	v_mfma_f32_16x16x32_bf16 v[108:111], v[40:43], v[188:191], v[108:111]
	v_mfma_f32_16x16x32_bf16 v[100:103], v[56:59], v[188:191], v[100:103]
	v_mfma_f32_16x16x32_bf16 v[92:95], v[40:43], v[196:199], v[92:95]
	v_mfma_f32_16x16x32_bf16 v[84:87], v[56:59], v[196:199], v[84:87]
	v_mfma_f32_16x16x32_bf16 v[140:143], v[44:47], v[176:179], v[140:143]
	v_mfma_f32_16x16x32_bf16 v[132:135], v[60:63], v[176:179], v[132:135]
	v_mfma_f32_16x16x32_bf16 v[124:127], v[44:47], v[184:187], v[124:127]
	v_mfma_f32_16x16x32_bf16 v[116:119], v[60:63], v[184:187], v[116:119]
	v_mfma_f32_16x16x32_bf16 v[108:111], v[44:47], v[192:195], v[108:111]
	v_mfma_f32_16x16x32_bf16 v[100:103], v[60:63], v[192:195], v[100:103]
	v_mfma_f32_16x16x32_bf16 v[92:95], v[44:47], v[200:203], v[92:95]
	v_mfma_f32_16x16x32_bf16 v[84:87], v[60:63], v[200:203], v[84:87]
	v_mfma_f32_16x16x32_bf16 v[136:139], v[148:151], v[172:175], v[136:139]
	v_mfma_f32_16x16x32_bf16 v[128:131], v[164:167], v[172:175], v[128:131]
	v_mfma_f32_16x16x32_bf16 v[120:123], v[148:151], v[180:183], v[120:123]
	v_mfma_f32_16x16x32_bf16 v[112:115], v[164:167], v[180:183], v[112:115]
	v_mfma_f32_16x16x32_bf16 v[104:107], v[148:151], v[188:191], v[104:107]
	v_mfma_f32_16x16x32_bf16 v[96:99], v[164:167], v[188:191], v[96:99]
	v_mfma_f32_16x16x32_bf16 v[88:91], v[148:151], v[196:199], v[88:91]
	v_mfma_f32_16x16x32_bf16 v[80:83], v[164:167], v[196:199], v[80:83]
	v_mfma_f32_16x16x32_bf16 v[136:139], v[152:155], v[176:179], v[136:139]
	v_mfma_f32_16x16x32_bf16 v[128:131], v[168:171], v[176:179], v[128:131]
	v_mfma_f32_16x16x32_bf16 v[120:123], v[152:155], v[184:187], v[120:123]
	v_mfma_f32_16x16x32_bf16 v[112:115], v[168:171], v[184:187], v[112:115]
	v_mfma_f32_16x16x32_bf16 v[104:107], v[152:155], v[192:195], v[104:107]
	v_mfma_f32_16x16x32_bf16 v[96:99], v[168:171], v[192:195], v[96:99]
	v_mfma_f32_16x16x32_bf16 v[88:91], v[152:155], v[200:203], v[88:91]
	v_mfma_f32_16x16x32_bf16 v[80:83], v[168:171], v[200:203], v[80:83]
	s_setprio 0
	s_barrier
	v_mov_b32_e32 v146, v158
	s_mov_b64 s[78:79], s[40:41]
	s_add_i32 s25, s72, s51
	ds_read_b128 v[172:175], v163 offset:16384
	ds_read_b128 v[176:179], v163 offset:17408
	ds_read_b128 v[180:183], v163 offset:18432
	ds_read_b128 v[184:187], v163 offset:19456
	ds_read_b128 v[188:191], v163 offset:20480
	ds_read_b128 v[192:195], v163 offset:21504
	ds_read_b128 v[196:199], v163 offset:22528
	ds_read_b128 v[200:203], v163 offset:23552
	s_mov_b32 m0, s25
	s_nop 0
	global_load_lds_dwordx4 v146, s[78:79]
	s_add_u32 s78, s40, 0x20000
	s_addc_u32 s79, s41, 0
	s_add_i32 m0, s25, 0x2000
	s_nop 0
	global_load_lds_dwordx4 v158, s[78:79]
	s_add_u32 s78, s40, 0x40000
	s_addc_u32 s79, s41, 0
	s_add_i32 s25, s73, s51
	s_mov_b32 m0, s25
	s_nop 0
	global_load_lds_dwordx4 v158, s[78:79]
	s_add_u32 s78, s40, 0x60000
	s_addc_u32 s79, s41, 0
	s_add_i32 m0, s25, 0x2000
	s_nop 0
	global_load_lds_dwordx4 v158, s[78:79]
	s_mov_b64 s[78:79], s[34:35]
	s_mov_b32 m0, s52
	s_nop 0
	global_load_lds_dwordx4 v159, s[78:79]
	s_add_u32 s78, s34, 0x20000
	s_addc_u32 s79, s35, 0
	s_mov_b32 m0, s53
	s_nop 0
	global_load_lds_dwordx4 v159, s[78:79]
	s_waitcnt vmcnt(8)
	s_waitcnt lgkmcnt(0)
	s_barrier
	s_setprio 3
	v_mfma_f32_16x16x32_bf16 v[76:79], v[40:43], v[172:175], v[76:79]
	v_mfma_f32_16x16x32_bf16 v[68:71], v[56:59], v[172:175], v[68:71]
	v_mfma_f32_16x16x32_bf16 v[52:55], v[40:43], v[180:183], v[52:55]
	v_mfma_f32_16x16x32_bf16 v[36:39], v[56:59], v[180:183], v[36:39]
	v_mfma_f32_16x16x32_bf16 v[28:31], v[40:43], v[188:191], v[28:31]
	v_mfma_f32_16x16x32_bf16 v[20:23], v[56:59], v[188:191], v[20:23]
	v_mfma_f32_16x16x32_bf16 v[12:15], v[40:43], v[196:199], v[12:15]
	v_mfma_f32_16x16x32_bf16 v[4:7], v[56:59], v[196:199], v[4:7]
	v_mfma_f32_16x16x32_bf16 v[76:79], v[44:47], v[176:179], v[76:79]
	v_mfma_f32_16x16x32_bf16 v[68:71], v[60:63], v[176:179], v[68:71]
	v_mfma_f32_16x16x32_bf16 v[52:55], v[44:47], v[184:187], v[52:55]
	v_mfma_f32_16x16x32_bf16 v[36:39], v[60:63], v[184:187], v[36:39]
	v_mfma_f32_16x16x32_bf16 v[28:31], v[44:47], v[192:195], v[28:31]
	v_mfma_f32_16x16x32_bf16 v[20:23], v[60:63], v[192:195], v[20:23]
	v_mfma_f32_16x16x32_bf16 v[12:15], v[44:47], v[200:203], v[12:15]
	v_mfma_f32_16x16x32_bf16 v[4:7], v[60:63], v[200:203], v[4:7]
	v_mfma_f32_16x16x32_bf16 v[48:51], v[148:151], v[180:183], v[48:51]
	v_mfma_f32_16x16x32_bf16 v[32:35], v[164:167], v[180:183], v[32:35]
	v_mfma_f32_16x16x32_bf16 v[24:27], v[148:151], v[188:191], v[24:27]
	v_mfma_f32_16x16x32_bf16 v[16:19], v[164:167], v[188:191], v[16:19]
	v_mfma_f32_16x16x32_bf16 v[8:11], v[148:151], v[196:199], v[8:11]
	v_mfma_f32_16x16x32_bf16 v[0:3], v[164:167], v[196:199], v[0:3]
	v_mfma_f32_16x16x32_bf16 v[40:43], v[148:151], v[172:175], v[72:75]
	v_mfma_f32_16x16x32_bf16 v[44:47], v[164:167], v[172:175], v[64:67]
	v_mfma_f32_16x16x32_bf16 v[48:51], v[152:155], v[184:187], v[48:51]
	v_mfma_f32_16x16x32_bf16 v[32:35], v[168:171], v[184:187], v[32:35]
	v_mfma_f32_16x16x32_bf16 v[24:27], v[152:155], v[192:195], v[24:27]
	v_mfma_f32_16x16x32_bf16 v[16:19], v[168:171], v[192:195], v[16:19]
	v_mfma_f32_16x16x32_bf16 v[8:11], v[152:155], v[200:203], v[8:11]
	v_mfma_f32_16x16x32_bf16 v[0:3], v[168:171], v[200:203], v[0:3]
	v_mfma_f32_16x16x32_bf16 v[40:43], v[152:155], v[176:179], v[40:43]
	v_mfma_f32_16x16x32_bf16 v[44:47], v[168:171], v[176:179], v[44:47]
	s_setprio 0
	s_barrier
	s_add_i32 s25, 0, 0x18000
	s_add_i32 s37, 0, 0x1c000
	v_add_u32_e32 v72, s25, v160
	v_add_u32_e32 v146, s37, v160
	ds_read_b128 v[56:59], v72
	ds_read_b128 v[60:63], v72 offset:1024
	ds_read_b128 v[64:67], v72 offset:2048
	ds_read_b128 v[72:75], v72 offset:3072
	ds_read_b128 v[148:151], v146
	ds_read_b128 v[152:155], v146 offset:1024
	ds_read_b128 v[164:167], v146 offset:2048
	ds_read_b128 v[168:171], v146 offset:3072
	s_add_u32 s78, s34, 0x40000
	v_mov_b32_e32 v146, v159
	s_addc_u32 s79, s35, 0
	s_mov_b32 m0, s60
	ds_read_b128 v[172:175], v163 offset:32768
	ds_read_b128 v[176:179], v163 offset:33792
	ds_read_b128 v[180:183], v163 offset:34816
	ds_read_b128 v[184:187], v163 offset:35840
	ds_read_b128 v[188:191], v163 offset:36864
	ds_read_b128 v[192:195], v163 offset:37888
	ds_read_b128 v[196:199], v163 offset:38912
	ds_read_b128 v[200:203], v163 offset:39936
	s_nop 0
	global_load_lds_dwordx4 v146, s[78:79]
	s_add_u32 s78, s34, 0x60000
	s_addc_u32 s79, s35, 0
	s_mov_b32 m0, s61
	s_nop 0
	global_load_lds_dwordx4 v159, s[78:79]
	s_waitcnt vmcnt(8)
	s_waitcnt lgkmcnt(0)
	s_barrier
	s_setprio 3
	v_mfma_f32_16x16x32_bf16 v[140:143], v[56:59], v[172:175], v[140:143]
	v_mfma_f32_16x16x32_bf16 v[132:135], v[64:67], v[172:175], v[132:135]
	v_mfma_f32_16x16x32_bf16 v[124:127], v[56:59], v[180:183], v[124:127]
	v_mfma_f32_16x16x32_bf16 v[116:119], v[64:67], v[180:183], v[116:119]
	v_mfma_f32_16x16x32_bf16 v[108:111], v[56:59], v[188:191], v[108:111]
	v_mfma_f32_16x16x32_bf16 v[100:103], v[64:67], v[188:191], v[100:103]
	v_mfma_f32_16x16x32_bf16 v[92:95], v[56:59], v[196:199], v[92:95]
	v_mfma_f32_16x16x32_bf16 v[84:87], v[64:67], v[196:199], v[84:87]
	v_mfma_f32_16x16x32_bf16 v[140:143], v[60:63], v[176:179], v[140:143]
	v_mfma_f32_16x16x32_bf16 v[132:135], v[72:75], v[176:179], v[132:135]
	v_mfma_f32_16x16x32_bf16 v[124:127], v[60:63], v[184:187], v[124:127]
	v_mfma_f32_16x16x32_bf16 v[116:119], v[72:75], v[184:187], v[116:119]
	v_mfma_f32_16x16x32_bf16 v[108:111], v[60:63], v[192:195], v[108:111]
	v_mfma_f32_16x16x32_bf16 v[100:103], v[72:75], v[192:195], v[100:103]
	v_mfma_f32_16x16x32_bf16 v[92:95], v[60:63], v[200:203], v[92:95]
	v_mfma_f32_16x16x32_bf16 v[84:87], v[72:75], v[200:203], v[84:87]
	v_mfma_f32_16x16x32_bf16 v[136:139], v[148:151], v[172:175], v[136:139]
	v_mfma_f32_16x16x32_bf16 v[128:131], v[164:167], v[172:175], v[128:131]
	v_mfma_f32_16x16x32_bf16 v[120:123], v[148:151], v[180:183], v[120:123]
	v_mfma_f32_16x16x32_bf16 v[112:115], v[164:167], v[180:183], v[112:115]
	v_mfma_f32_16x16x32_bf16 v[104:107], v[148:151], v[188:191], v[104:107]
	v_mfma_f32_16x16x32_bf16 v[96:99], v[164:167], v[188:191], v[96:99]
	v_mfma_f32_16x16x32_bf16 v[88:91], v[148:151], v[196:199], v[88:91]
	v_mfma_f32_16x16x32_bf16 v[80:83], v[164:167], v[196:199], v[80:83]
	v_mfma_f32_16x16x32_bf16 v[136:139], v[152:155], v[176:179], v[136:139]
	v_mfma_f32_16x16x32_bf16 v[128:131], v[168:171], v[176:179], v[128:131]
	v_mfma_f32_16x16x32_bf16 v[120:123], v[152:155], v[184:187], v[120:123]
	v_mfma_f32_16x16x32_bf16 v[112:115], v[168:171], v[184:187], v[112:115]
	v_mfma_f32_16x16x32_bf16 v[104:107], v[152:155], v[192:195], v[104:107]
	v_mfma_f32_16x16x32_bf16 v[96:99], v[168:171], v[192:195], v[96:99]
	v_mfma_f32_16x16x32_bf16 v[88:91], v[152:155], v[200:203], v[88:91]
	v_mfma_f32_16x16x32_bf16 v[80:83], v[168:171], v[200:203], v[80:83]
	s_setprio 0
	s_barrier
	s_add_u32 s78, s40, 0x80
	s_addc_u32 s79, s41, 0
	v_mov_b32_e32 v146, v158
	s_add_i32 s25, s25, s51
	ds_read_b128 v[172:175], v163 offset:49152
	ds_read_b128 v[176:179], v163 offset:50176
	ds_read_b128 v[180:183], v163 offset:51200
	ds_read_b128 v[184:187], v163 offset:52224
	ds_read_b128 v[188:191], v163 offset:53248
	ds_read_b128 v[192:195], v163 offset:54272
	ds_read_b128 v[196:199], v163 offset:55296
	ds_read_b128 v[200:203], v163 offset:56320
	s_mov_b32 m0, s25
	s_nop 0
	global_load_lds_dwordx4 v146, s[78:79]
	s_add_u32 s78, s40, 0x20080
	s_addc_u32 s79, s41, 0
	s_add_i32 m0, s25, 0x2000
	s_nop 0
	global_load_lds_dwordx4 v158, s[78:79]
	s_add_u32 s78, s40, 0x40080
	s_addc_u32 s79, s41, 0
	s_add_i32 s25, s37, s51
	s_mov_b32 m0, s25
	s_add_u32 s40, s40, 0x60080
	global_load_lds_dwordx4 v158, s[78:79]
	s_addc_u32 s41, s41, 0
	s_add_i32 m0, s25, 0x2000
	s_add_u32 s34, s34, 0x20080
	global_load_lds_dwordx4 v158, s[40:41]
	s_mov_b32 m0, s69
	s_addc_u32 s35, s35, 0
	global_load_lds_dwordx4 v159, s[38:39]
	s_mov_b32 m0, s70
	s_nop 0
	global_load_lds_dwordx4 v159, s[34:35]
	s_waitcnt vmcnt(8)
	s_waitcnt lgkmcnt(0)
	s_barrier
	s_setprio 3
	v_mfma_f32_16x16x32_bf16 v[76:79], v[56:59], v[172:175], v[76:79]
	v_mfma_f32_16x16x32_bf16 v[68:71], v[64:67], v[172:175], v[68:71]
	v_mfma_f32_16x16x32_bf16 v[52:55], v[56:59], v[180:183], v[52:55]
	v_mfma_f32_16x16x32_bf16 v[36:39], v[64:67], v[180:183], v[36:39]
	v_mfma_f32_16x16x32_bf16 v[28:31], v[56:59], v[188:191], v[28:31]
	v_mfma_f32_16x16x32_bf16 v[20:23], v[64:67], v[188:191], v[20:23]
	v_mfma_f32_16x16x32_bf16 v[12:15], v[56:59], v[196:199], v[12:15]
	v_mfma_f32_16x16x32_bf16 v[4:7], v[64:67], v[196:199], v[4:7]
	v_mfma_f32_16x16x32_bf16 v[76:79], v[60:63], v[176:179], v[76:79]
	v_mfma_f32_16x16x32_bf16 v[68:71], v[72:75], v[176:179], v[68:71]
	v_mfma_f32_16x16x32_bf16 v[52:55], v[60:63], v[184:187], v[52:55]
	v_mfma_f32_16x16x32_bf16 v[36:39], v[72:75], v[184:187], v[36:39]
	v_mfma_f32_16x16x32_bf16 v[28:31], v[60:63], v[192:195], v[28:31]
	v_mfma_f32_16x16x32_bf16 v[20:23], v[72:75], v[192:195], v[20:23]
	v_mfma_f32_16x16x32_bf16 v[12:15], v[60:63], v[200:203], v[12:15]
	v_mfma_f32_16x16x32_bf16 v[4:7], v[72:75], v[200:203], v[4:7]
	v_mfma_f32_16x16x32_bf16 v[40:43], v[148:151], v[172:175], v[40:43]
	v_mfma_f32_16x16x32_bf16 v[72:75], v[152:155], v[176:179], v[40:43]
	v_mfma_f32_16x16x32_bf16 v[40:43], v[164:167], v[172:175], v[44:47]
	v_mfma_f32_16x16x32_bf16 v[64:67], v[168:171], v[176:179], v[40:43]
	v_mfma_f32_16x16x32_bf16 v[40:43], v[148:151], v[180:183], v[48:51]
	v_mfma_f32_16x16x32_bf16 v[32:35], v[164:167], v[180:183], v[32:35]
	v_mfma_f32_16x16x32_bf16 v[24:27], v[148:151], v[188:191], v[24:27]
	v_mfma_f32_16x16x32_bf16 v[16:19], v[164:167], v[188:191], v[16:19]
	v_mfma_f32_16x16x32_bf16 v[8:11], v[148:151], v[196:199], v[8:11]
	v_mfma_f32_16x16x32_bf16 v[0:3], v[164:167], v[196:199], v[0:3]
	v_mfma_f32_16x16x32_bf16 v[48:51], v[152:155], v[184:187], v[40:43]
	v_mfma_f32_16x16x32_bf16 v[32:35], v[168:171], v[184:187], v[32:35]
	v_mfma_f32_16x16x32_bf16 v[24:27], v[152:155], v[192:195], v[24:27]
	v_mfma_f32_16x16x32_bf16 v[16:19], v[168:171], v[192:195], v[16:19]
	v_mfma_f32_16x16x32_bf16 v[8:11], v[152:155], v[200:203], v[8:11]
	v_mfma_f32_16x16x32_bf16 v[0:3], v[168:171], v[200:203], v[0:3]
	s_setprio 0
	s_barrier
	s_add_i32 s23, s23, 2
	s_add_u32 s5, s5, 0x100
	s_addc_u32 s18, s18, 0
	s_add_u32 s30, s30, 0x100
	s_addc_u32 s31, s31, 0
	s_cmp_gt_u32 s23, 13
	s_cbranch_scc0 .LBB0_252
	s_and_b64 vcc, exec, s[20:21]
	s_cbranch_vccz .LBB0_255
	s_barrier

.LBB0_328:
	s_andn2_b64 vcc, exec, s[12:13]
	s_cbranch_vccnz .LBB0_380
	s_getreg_b32 s0, hwreg(HW_REG_HW_ID, 0, 6)
	s_lshl_b32 s0, s0, 2
	s_and_b32 s0, s0, 0xfc
	s_add_i32 s0, s0, 0
	s_add_i32 s0, s0, 0x25c00
	v_mov_b32_e32 v0, s0
	ds_read_b32 v0, v0
	s_ashr_i32 s0, s2, 1
	s_add_i32 s0, s33, s0
	s_cmpk_gt_i32 s0, 0x17f
	s_waitcnt lgkmcnt(0)
	v_readfirstlane_b32 s1, v0
	v_mbcnt_lo_u32_b32 v0, -1, 0
	v_mbcnt_hi_u32_b32 v0, -1, v0
	s_nop 1
	v_lshl_add_u32 v0, s1, 6, v0
	s_nop 0
	v_readfirstlane_b32 s1, v0
	s_cbranch_scc1 .LBB0_380
	v_bfe_i32 v3, v0, 27, 1
	v_lshlrev_b32_e32 v1, 4, v0
	v_lshrrev_b32_e32 v3, 22, v3
	v_add_u32_e32 v3, v1, v3
	v_and_b32_e32 v3, 0xfffffc00, v3
	v_ashrrev_i32_e32 v2, 31, v0
	v_sub_u32_e32 v1, v1, v3
	v_lshrrev_b32_e32 v2, 26, v2
	v_lshrrev_b32_e32 v3, 4, v1
	v_add_u32_e32 v2, v0, v2
	v_bitop3_b32 v3, v3, v1, 32 bitop3:0x6c
	v_ashrrev_i32_e32 v1, 31, v1
	v_ashrrev_i32_e32 v2, 6, v2
	v_lshrrev_b32_e32 v1, 26, v1
	v_lshlrev_b32_e32 v4, 3, v2
	v_add_u32_e32 v1, v3, v1
	v_and_b32_e32 v4, -16, v4
	v_ashrrev_i32_e32 v1, 6, v1
	v_add_u32_e32 v4, v1, v4
	v_mul_i32_i24_e32 v5, 64, v1
	v_and_b32_e32 v1, 3, v1
	s_mov_b32 s4, 0x1fffe0
	v_and_or_b32 v1, v4, s4, v1
	s_ashr_i32 s4, s0, 31
	s_lshr_b32 s4, s4, 29
	s_add_i32 s4, s0, s4
	s_ashr_i32 s16, s1, 6
	s_ashr_i32 s5, s4, 3
	s_and_b32 s4, s4, -8
	s_and_b32 s20, s2, 1
	s_ashr_i32 s15, s1, 8
	s_lshl_b32 s14, s16, 10
	s_sub_i32 s0, s0, s4
	s_lshl_b32 s4, s20, 7
	s_cmp_lt_i32 s0, 0
	s_cselect_b32 s12, 49, 48
	s_mul_i32 s0, s0, s12
	s_add_i32 s0, s0, s5
	s_mul_hi_i32 s5, s0, 0x2aaaaaab
	s_lshr_b32 s12, s5, 31
	s_ashr_i32 s5, s5, 3
	s_add_i32 s5, s5, s12
	s_lshl_b32 s12, s5, 3
	s_mul_i32 s5, s5, 48
	s_sub_i32 s5, s0, s5
	s_bfe_i32 s0, s5, 0x80000
	s_bfe_u32 s0, s0, 0x3000c
	s_add_i32 s13, s5, s0
	s_bfe_i32 s0, s13, 0x80000
	s_and_b32 s13, s13, 0xf8
	s_sub_i32 s5, s5, s13
	s_sext_i32_i8 s5, s5
	s_add_i32 s21, s12, s5
	s_lshl_b32 s5, s21, 8
	s_or_b32 s4, s5, s4
	s_sext_i32_i16 s0, s0
	s_ashr_i32 s5, s4, 31
	s_lshr_b32 s0, s0, 3
	s_lshl_b64 s[4:5], s[4:5], 11
	v_sub_u32_e32 v3, v3, v5
	v_mov_b32_e32 v5, 1
	s_add_u32 s4, s90, s4
	v_lshlrev_b32_e32 v2, 5, v2
	v_ashrrev_i16_sdwa v3, v5, sext(v3) dst_sel:DWORD dst_unused:UNUSED_PAD src0_sel:DWORD src1_sel:BYTE_0
	v_lshlrev_b32_e32 v5, 1, v4
	v_lshrrev_b32_e32 v6, 2, v4
	s_addc_u32 s5, s91, s5
	s_bfe_i64 s[12:13], s[0:1], 0x100000
	v_and_b32_e32 v2, 32, v2
	v_bfe_i32 v3, v3, 0, 16
	v_and_b32_e32 v5, 24, v5
	v_and_b32_e32 v6, 4, v6
	s_lshl_b64 s[12:13], s[12:13], 19
	v_or3_b32 v1, v1, v6, v5
	v_add_lshl_u32 v2, v2, v3, 1
	s_add_u32 s12, s49, s12
	v_lshl_add_u32 v36, v1, 11, v2
	s_addc_u32 s13, s50, s13
	s_add_i32 s23, s14, 0
	s_mov_b64 s[18:19], s[12:13]
	s_add_i32 m0, s23, 0x10000
	v_lshl_add_u32 v37, v4, 11, v2
	global_load_lds_dwordx4 v36, s[18:19]
	s_add_u32 s18, s12, 0x20000
	s_addc_u32 s19, s13, 0
	s_add_i32 m0, s23, 0x12000
	s_nop 0
	global_load_lds_dwordx4 v36, s[18:19]
	s_add_i32 m0, s23, 0x14000
	s_add_u32 s18, s12, 0x40000
	s_addc_u32 s19, s13, 0
	s_nop 0
	global_load_lds_dwordx4 v36, s[18:19]
	s_add_u32 s18, s12, 0x60000
	s_addc_u32 s19, s13, 0
	s_add_i32 m0, s23, 0x16000
	s_nop 0
	global_load_lds_dwordx4 v36, s[18:19]
	s_mov_b64 s[18:19], s[4:5]
	s_mov_b32 m0, s23
	s_nop 0
	global_load_lds_dwordx4 v37, s[18:19]
	s_add_u32 s18, s4, 0x20000
	s_addc_u32 s19, s5, 0
	s_add_i32 s24, s23, 0x2000
	s_mov_b32 m0, s24
	s_cmp_lg_u32 s15, 1
	global_load_lds_dwordx4 v37, s[18:19]
	s_cbranch_scc1 .LBB0_332
	s_barrier
.LBB0_332:
	s_and_b32 s25, s16, 3
	v_and_b32_e32 v1, 48, v0
	v_lshlrev_b32_e32 v2, 6, v0
	s_movk_i32 s16, 0x3c0
	v_lshlrev_b32_e32 v0, 2, v0
	s_lshl_b32 s22, s15, 6
	s_lshl_b32 s15, s15, 13
	v_and_or_b32 v1, v2, s16, v1
	v_and_b32_e32 v0, 32, v0
	v_bitop3_b32 v2, v1, s15, v0 bitop3:0xde
	s_lshl_b32 s15, s25, 12
	s_add_u32 s16, s12, 0x80
	v_bitop3_b32 v1, v1, s15, v0 bitop3:0xde
	s_addc_u32 s17, s13, 0
	s_waitcnt vmcnt(0)
	s_barrier
	s_add_i32 m0, s23, 0x18000
	s_mov_b32 s34, -2
	global_load_lds_dwordx4 v36, s[16:17]
	s_add_u32 s16, s12, 0x20080
	s_addc_u32 s17, s13, 0
	s_add_i32 m0, s23, 0x1a000
	v_add_u32_e32 v40, 0, v2
	global_load_lds_dwordx4 v36, s[16:17]
	s_add_u32 s16, s4, 0x80
	s_addc_u32 s17, s5, 0
	s_add_i32 s26, s23, 0x8000
	s_mov_b32 m0, s26
	s_nop 0
	global_load_lds_dwordx4 v37, s[16:17]
	s_add_u32 s16, s4, 0x20080
	s_addc_u32 s17, s5, 0
	s_add_i32 s27, s23, 0xa000
	s_mov_b32 m0, s27
	s_nop 0
	global_load_lds_dwordx4 v37, s[16:17]
	s_add_i32 m0, s23, 0x1c000
	s_add_u32 s16, s12, 0x40080
	s_addc_u32 s17, s13, 0
	s_nop 0
	global_load_lds_dwordx4 v36, s[16:17]
	s_add_u32 s16, s12, 0x60080
	s_addc_u32 s17, s13, 0
	s_add_i32 m0, s23, 0x1e000
	s_add_u32 s28, s12, 0x100
	global_load_lds_dwordx4 v36, s[16:17]
	s_addc_u32 s29, s13, 0
	s_add_u32 s30, s4, 0x100
	s_waitcnt vmcnt(6)
	s_addc_u32 s31, s5, 0
	s_add_i32 s35, 0, 0x10000
	s_add_i32 s37, 0, 0x14000
	s_add_i32 s39, 0, 0x18000
	s_add_i32 s41, 0, 0x1c000
	v_mov_b32_e32 v0, 0
	v_add_u32_e32 v38, s35, v1
	v_add_u32_e32 v39, s37, v1
	s_add_i32 s35, s35, s14
	s_add_i32 s37, s37, s14
	v_add_u32_e32 v41, s39, v1
	v_add_u32_e32 v42, s41, v1
	s_add_i32 s39, s39, s14
	s_add_i32 s41, s41, s14
	s_add_i32 s36, s35, 0x2000
	s_add_i32 s38, s37, 0x2000
	s_add_i32 s40, s39, 0x2000
	s_add_i32 s49, s41, 0x2000
	v_mov_b32_e32 v1, v0
	v_mov_b32_e32 v2, v0
	v_mov_b32_e32 v3, v0
	v_mov_b32_e32 v8, v0
	v_mov_b32_e32 v9, v0
	v_mov_b32_e32 v10, v0
	v_mov_b32_e32 v11, v0
	v_mov_b32_e32 v16, v0
	v_mov_b32_e32 v17, v0
	v_mov_b32_e32 v18, v0
	v_mov_b32_e32 v19, v0
	v_mov_b32_e32 v24, v0
	v_mov_b32_e32 v25, v0
	v_mov_b32_e32 v26, v0
	v_mov_b32_e32 v27, v0
	v_mov_b32_e32 v32, v0
	v_mov_b32_e32 v33, v0
	v_mov_b32_e32 v34, v0
	v_mov_b32_e32 v35, v0
	v_mov_b32_e32 v48, v0
	v_mov_b32_e32 v49, v0
	v_mov_b32_e32 v50, v0
	v_mov_b32_e32 v51, v0
	v_mov_b32_e32 v64, v0
	v_mov_b32_e32 v65, v0
	v_mov_b32_e32 v66, v0
	v_mov_b32_e32 v67, v0
	v_mov_b32_e32 v72, v0
	v_mov_b32_e32 v73, v0
	v_mov_b32_e32 v74, v0
	v_mov_b32_e32 v75, v0
	v_mov_b32_e32 v4, v0
	v_mov_b32_e32 v5, v0
	v_mov_b32_e32 v6, v0
	v_mov_b32_e32 v7, v0
	v_mov_b32_e32 v12, v0
	v_mov_b32_e32 v13, v0
	v_mov_b32_e32 v14, v0
	v_mov_b32_e32 v15, v0
	v_mov_b32_e32 v20, v0
	v_mov_b32_e32 v21, v0
	v_mov_b32_e32 v22, v0
	v_mov_b32_e32 v23, v0
	v_mov_b32_e32 v28, v0
	v_mov_b32_e32 v29, v0
	v_mov_b32_e32 v30, v0
	v_mov_b32_e32 v31, v0
	v_mov_b32_e32 v44, v0
	v_mov_b32_e32 v45, v0
	v_mov_b32_e32 v46, v0
	v_mov_b32_e32 v47, v0
	v_mov_b32_e32 v60, v0
	v_mov_b32_e32 v61, v0
	v_mov_b32_e32 v62, v0
	v_mov_b32_e32 v63, v0
	v_mov_b32_e32 v68, v0
	v_mov_b32_e32 v69, v0
	v_mov_b32_e32 v70, v0
	v_mov_b32_e32 v71, v0
	v_mov_b32_e32 v76, v0
	v_mov_b32_e32 v77, v0
	v_mov_b32_e32 v78, v0
	v_mov_b32_e32 v79, v0
	s_barrier
.LBB0_333:
	ds_read_b128 v[52:55], v38
	ds_read_b128 v[56:59], v38 offset:1024
	ds_read_b128 v[80:83], v38 offset:2048
	ds_read_b128 v[84:87], v38 offset:3072
	ds_read_b128 v[88:91], v39
	ds_read_b128 v[92:95], v39 offset:1024
	ds_read_b128 v[96:99], v39 offset:2048
	ds_read_b128 v[100:103], v39 offset:3072
	s_cmp_eq_u32 s34, 12
	s_cselect_b32 s14, s4, s30
	s_cselect_b32 s15, s5, s31
	s_cselect_b32 s18, s12, s28
	s_cselect_b32 s19, s13, s29
	s_add_u32 s16, s14, 0x80
	s_addc_u32 s17, s15, 0
	ds_read_b128 v[104:107], v40
	ds_read_b128 v[108:111], v40 offset:1024
	ds_read_b128 v[112:115], v40 offset:2048
	ds_read_b128 v[116:119], v40 offset:3072
	ds_read_b128 v[120:123], v40 offset:4096
	ds_read_b128 v[124:127], v40 offset:5120
	ds_read_b128 v[128:131], v40 offset:6144
	ds_read_b128 v[132:135], v40 offset:7168
	s_waitcnt vmcnt(6)
	s_waitcnt lgkmcnt(0)
	s_barrier
	s_setprio 3
	v_mfma_f32_16x16x32_bf16 v[76:79], v[52:55], v[104:107], v[76:79]
	v_mfma_f32_16x16x32_bf16 v[68:71], v[80:83], v[104:107], v[68:71]
	v_mfma_f32_16x16x32_bf16 v[60:63], v[52:55], v[112:115], v[60:63]
	v_mfma_f32_16x16x32_bf16 v[44:47], v[80:83], v[112:115], v[44:47]
	v_mfma_f32_16x16x32_bf16 v[28:31], v[52:55], v[120:123], v[28:31]
	v_mfma_f32_16x16x32_bf16 v[20:23], v[80:83], v[120:123], v[20:23]
	v_mfma_f32_16x16x32_bf16 v[12:15], v[52:55], v[128:131], v[12:15]
	v_mfma_f32_16x16x32_bf16 v[4:7], v[80:83], v[128:131], v[4:7]
	v_mfma_f32_16x16x32_bf16 v[76:79], v[56:59], v[108:111], v[76:79]
	v_mfma_f32_16x16x32_bf16 v[68:71], v[84:87], v[108:111], v[68:71]
	v_mfma_f32_16x16x32_bf16 v[60:63], v[56:59], v[116:119], v[60:63]
	v_mfma_f32_16x16x32_bf16 v[44:47], v[84:87], v[116:119], v[44:47]
	v_mfma_f32_16x16x32_bf16 v[28:31], v[56:59], v[124:127], v[28:31]
	v_mfma_f32_16x16x32_bf16 v[20:23], v[84:87], v[124:127], v[20:23]
	v_mfma_f32_16x16x32_bf16 v[12:15], v[56:59], v[132:135], v[12:15]
	v_mfma_f32_16x16x32_bf16 v[4:7], v[84:87], v[132:135], v[4:7]
	v_mfma_f32_16x16x32_bf16 v[48:51], v[88:91], v[112:115], v[48:51]
	v_mfma_f32_16x16x32_bf16 v[32:35], v[96:99], v[112:115], v[32:35]
	v_mfma_f32_16x16x32_bf16 v[24:27], v[88:91], v[120:123], v[24:27]
	v_mfma_f32_16x16x32_bf16 v[16:19], v[96:99], v[120:123], v[16:19]
	v_mfma_f32_16x16x32_bf16 v[8:11], v[88:91], v[128:131], v[8:11]
	v_mfma_f32_16x16x32_bf16 v[0:3], v[96:99], v[128:131], v[0:3]
	v_mfma_f32_16x16x32_bf16 v[52:55], v[88:91], v[104:107], v[72:75]
	v_mfma_f32_16x16x32_bf16 v[56:59], v[96:99], v[104:107], v[64:67]
	v_mfma_f32_16x16x32_bf16 v[48:51], v[92:95], v[116:119], v[48:51]
	v_mfma_f32_16x16x32_bf16 v[32:35], v[100:103], v[116:119], v[32:35]
	v_mfma_f32_16x16x32_bf16 v[24:27], v[92:95], v[124:127], v[24:27]
	v_mfma_f32_16x16x32_bf16 v[16:19], v[100:103], v[124:127], v[16:19]
	v_mfma_f32_16x16x32_bf16 v[8:11], v[92:95], v[132:135], v[8:11]
	v_mfma_f32_16x16x32_bf16 v[0:3], v[100:103], v[132:135], v[0:3]
	v_mfma_f32_16x16x32_bf16 v[52:55], v[92:95], v[108:111], v[52:55]
	v_mfma_f32_16x16x32_bf16 v[56:59], v[100:103], v[108:111], v[56:59]
	s_setprio 0
	s_barrier
	s_mov_b64 s[50:51], s[18:19]
	s_mov_b32 m0, s35
	s_nop 0
	global_load_lds_dwordx4 v36, s[50:51]
	s_add_u32 s50, s18, 0x20000
	s_addc_u32 s51, s19, 0
	s_mov_b32 m0, s36
	s_nop 0
	global_load_lds_dwordx4 v36, s[50:51]
	s_add_u32 s50, s18, 0x40000
	s_addc_u32 s51, s19, 0
	s_mov_b32 m0, s37
	s_nop 0
	global_load_lds_dwordx4 v36, s[50:51]
	s_add_u32 s50, s18, 0x60000
	s_addc_u32 s51, s19, 0
	s_mov_b32 m0, s38
	s_nop 0
	global_load_lds_dwordx4 v36, s[50:51]
	s_mov_b64 s[50:51], s[14:15]
	s_mov_b32 m0, s23
	s_nop 0
	global_load_lds_dwordx4 v37, s[50:51]
	s_add_u32 s50, s14, 0x20000
	s_addc_u32 s51, s15, 0
	s_mov_b32 m0, s24
	s_nop 0
	global_load_lds_dwordx4 v37, s[50:51]
	s_waitcnt vmcnt(6)
	s_waitcnt lgkmcnt(0)
	s_barrier
	s_barrier
	ds_read_b128 v[64:67], v41
	ds_read_b128 v[72:75], v41 offset:1024
	ds_read_b128 v[80:83], v41 offset:2048
	ds_read_b128 v[84:87], v41 offset:3072
	ds_read_b128 v[88:91], v42
	ds_read_b128 v[92:95], v42 offset:1024
	ds_read_b128 v[96:99], v42 offset:2048
	ds_read_b128 v[100:103], v42 offset:3072
	ds_read_b128 v[104:107], v40 offset:32768
	ds_read_b128 v[108:111], v40 offset:33792
	ds_read_b128 v[112:115], v40 offset:34816
	ds_read_b128 v[116:119], v40 offset:35840
	ds_read_b128 v[120:123], v40 offset:36864
	ds_read_b128 v[124:127], v40 offset:37888
	ds_read_b128 v[128:131], v40 offset:38912
	ds_read_b128 v[132:135], v40 offset:39936
	s_waitcnt vmcnt(6)
	s_waitcnt lgkmcnt(0)
	s_barrier
	s_setprio 3
	v_mfma_f32_16x16x32_bf16 v[76:79], v[64:67], v[104:107], v[76:79]
	v_mfma_f32_16x16x32_bf16 v[68:71], v[80:83], v[104:107], v[68:71]
	v_mfma_f32_16x16x32_bf16 v[60:63], v[64:67], v[112:115], v[60:63]
	v_mfma_f32_16x16x32_bf16 v[44:47], v[80:83], v[112:115], v[44:47]
	v_mfma_f32_16x16x32_bf16 v[28:31], v[64:67], v[120:123], v[28:31]
	v_mfma_f32_16x16x32_bf16 v[20:23], v[80:83], v[120:123], v[20:23]
	v_mfma_f32_16x16x32_bf16 v[12:15], v[64:67], v[128:131], v[12:15]
	v_mfma_f32_16x16x32_bf16 v[4:7], v[80:83], v[128:131], v[4:7]
	v_mfma_f32_16x16x32_bf16 v[76:79], v[72:75], v[108:111], v[76:79]
	v_mfma_f32_16x16x32_bf16 v[68:71], v[84:87], v[108:111], v[68:71]
	v_mfma_f32_16x16x32_bf16 v[60:63], v[72:75], v[116:119], v[60:63]
	v_mfma_f32_16x16x32_bf16 v[44:47], v[84:87], v[116:119], v[44:47]
	v_mfma_f32_16x16x32_bf16 v[28:31], v[72:75], v[124:127], v[28:31]
	v_mfma_f32_16x16x32_bf16 v[20:23], v[84:87], v[124:127], v[20:23]
	v_mfma_f32_16x16x32_bf16 v[12:15], v[72:75], v[132:135], v[12:15]
	v_mfma_f32_16x16x32_bf16 v[4:7], v[84:87], v[132:135], v[4:7]
	v_mfma_f32_16x16x32_bf16 v[52:55], v[88:91], v[104:107], v[52:55]
	s_add_u32 s50, s18, 0x80
	s_addc_u32 s51, s19, 0
	v_mfma_f32_16x16x32_bf16 v[72:75], v[92:95], v[108:111], v[52:55]
	v_mfma_f32_16x16x32_bf16 v[52:55], v[96:99], v[104:107], v[56:59]
	v_mfma_f32_16x16x32_bf16 v[48:51], v[88:91], v[112:115], v[48:51]
	v_mfma_f32_16x16x32_bf16 v[32:35], v[96:99], v[112:115], v[32:35]
	v_mfma_f32_16x16x32_bf16 v[24:27], v[88:91], v[120:123], v[24:27]
	v_mfma_f32_16x16x32_bf16 v[16:19], v[96:99], v[120:123], v[16:19]
	v_mfma_f32_16x16x32_bf16 v[8:11], v[88:91], v[128:131], v[8:11]
	v_mfma_f32_16x16x32_bf16 v[0:3], v[96:99], v[128:131], v[0:3]
	v_mfma_f32_16x16x32_bf16 v[64:67], v[100:103], v[108:111], v[52:55]
	v_mfma_f32_16x16x32_bf16 v[48:51], v[92:95], v[116:119], v[48:51]
	v_mfma_f32_16x16x32_bf16 v[32:35], v[100:103], v[116:119], v[32:35]
	v_mfma_f32_16x16x32_bf16 v[24:27], v[92:95], v[124:127], v[24:27]
	v_mfma_f32_16x16x32_bf16 v[16:19], v[100:103], v[124:127], v[16:19]
	v_mfma_f32_16x16x32_bf16 v[8:11], v[92:95], v[132:135], v[8:11]
	v_mfma_f32_16x16x32_bf16 v[0:3], v[100:103], v[132:135], v[0:3]
	s_setprio 0
	s_barrier
	s_mov_b32 m0, s39
	s_nop 0
	global_load_lds_dwordx4 v36, s[50:51]
	s_add_u32 s50, s18, 0x20080
	s_addc_u32 s51, s19, 0
	s_mov_b32 m0, s40
	s_nop 0
	global_load_lds_dwordx4 v36, s[50:51]
	s_add_u32 s50, s18, 0x40080
	s_addc_u32 s51, s19, 0
	s_mov_b32 m0, s41
	s_add_u32 s18, s18, 0x60080
	global_load_lds_dwordx4 v36, s[50:51]
	s_addc_u32 s19, s19, 0
	s_mov_b32 m0, s49
	s_add_u32 s14, s14, 0x20080
	global_load_lds_dwordx4 v36, s[18:19]
	s_mov_b32 m0, s26
	s_addc_u32 s15, s15, 0
	global_load_lds_dwordx4 v37, s[16:17]
	s_mov_b32 m0, s27
	s_nop 0
	global_load_lds_dwordx4 v37, s[14:15]
	s_waitcnt vmcnt(6)
	s_waitcnt lgkmcnt(0)
	s_barrier
	s_barrier
	s_add_i32 s34, s34, 2
	s_add_u32 s28, s28, 0x100
	s_addc_u32 s29, s29, 0
	s_add_u32 s30, s30, 0x100
	s_addc_u32 s31, s31, 0
	s_cmp_gt_u32 s34, 13
	s_cbranch_scc0 .LBB0_333
	s_cmpk_lt_u32 s1, 0x100
	s_cbranch_scc0 .LBB0_336
	s_barrier

.LBB0_711:
	v_readlane_b32 s40, v249, 51
	s_cmp_lt_i32 s40, 5
	s_cselect_b64 s[8:9], -1, 0
	s_cmp_gt_i32 s40, 4
	s_cselect_b64 s[4:5], -1, 0
	s_and_b64 s[0:1], s[8:9], s[6:7]
	v_readlane_b32 s41, v249, 52
	s_andn2_b64 vcc, exec, s[0:1]
	v_readlane_b32 s42, v249, 53
	v_readlane_b32 s43, v249, 54
	s_cbranch_vccnz .LBB0_732
	s_getreg_b32 s0, hwreg(HW_REG_HW_ID, 0, 6)
	s_lshl_b32 s0, s0, 2
	s_and_b32 s0, s0, 0xfc
	s_add_i32 s0, s0, 0
	s_add_i32 s0, s0, 0x25c00
	v_mov_b32_e32 v0, s0
	ds_read_b32 v0, v0
	s_cmpk_gt_i32 s2, 0xff
	s_waitcnt lgkmcnt(0)
	v_readfirstlane_b32 s0, v0
	v_mbcnt_lo_u32_b32 v0, -1, 0
	v_mbcnt_hi_u32_b32 v0, -1, v0
	s_nop 1
	v_lshl_add_u32 v0, s0, 6, v0
	s_nop 0
	v_readfirstlane_b32 s1, v0
	s_cbranch_scc1 .LBB0_732
	v_bfe_i32 v3, v0, 27, 1
	v_lshlrev_b32_e32 v1, 4, v0
	v_lshrrev_b32_e32 v3, 22, v3
	v_add_u32_e32 v3, v1, v3
	v_and_b32_e32 v3, 0xfffffc00, v3
	v_ashrrev_i32_e32 v2, 31, v0
	v_sub_u32_e32 v1, v1, v3
	v_lshrrev_b32_e32 v2, 26, v2
	v_lshrrev_b32_e32 v3, 4, v1
	v_add_u32_e32 v2, v0, v2
	v_bitop3_b32 v3, v3, v1, 32 bitop3:0x6c
	v_ashrrev_i32_e32 v1, 31, v1
	s_add_u32 s3, s78, 0x15500000
	v_ashrrev_i32_e32 v2, 6, v2
	v_lshrrev_b32_e32 v1, 26, v1
	s_addc_u32 s13, s79, 0
	v_lshlrev_b32_e32 v4, 3, v2
	v_add_u32_e32 v1, v3, v1
	s_add_u32 s34, s78, 0x1700000
	v_and_b32_e32 v4, -16, v4
	v_ashrrev_i32_e32 v1, 6, v1
	s_addc_u32 s35, s79, 0
	v_add_u32_e32 v4, v1, v4
	v_mul_i32_i24_e32 v5, 64, v1
	v_and_b32_e32 v1, 3, v1
	s_mov_b32 s0, 0x1fffe0
	s_ashr_i32 s37, s2, 31
	v_and_or_b32 v1, v4, s0, v1
	s_lshr_b32 s0, s37, 29
	s_add_i32 s0, s2, s0
	s_ashr_i32 s6, s0, 3
	s_and_b32 s0, s0, -8
	s_ashr_i32 s10, s1, 6
	s_sub_i32 s0, s2, s0
	s_ashr_i32 s11, s1, 8
	s_lshl_b32 s36, s10, 10
	s_lshl_b32 s12, s0, 5
	s_mul_i32 s7, s0, 33
	s_cmp_lt_i32 s0, 0
	s_cselect_b32 s0, s7, s12
	s_add_i32 s0, s0, s6
	s_ashr_i32 s6, s0, 31
	s_lshr_b32 s6, s6, 27
	s_add_i32 s6, s0, s6
	s_ashr_i32 s7, s6, 5
	s_andn2_b32 s6, s6, 31
	s_sub_i32 s6, s0, s6
	s_bfe_i32 s0, s6, 0x80000
	s_bfe_u32 s0, s0, 0x3000c
	s_add_i32 s12, s6, s0
	s_bfe_i32 s0, s12, 0x80000
	s_and_b32 s12, s12, 0xf8
	s_sub_i32 s6, s6, s12
	s_lshl_b32 s7, s7, 3
	s_sext_i32_i8 s6, s6
	s_add_i32 s22, s7, s6
	s_sext_i32_i16 s0, s0
	s_ashr_i32 s23, s22, 31
	s_lshr_b32 s0, s0, 3
	s_lshl_b64 s[6:7], s[22:23], 19
	v_sub_u32_e32 v3, v3, v5
	v_mov_b32_e32 v5, 1
	s_add_u32 s24, s3, s6
	v_lshlrev_b32_e32 v2, 5, v2
	v_ashrrev_i16_sdwa v3, v5, sext(v3) dst_sel:DWORD dst_unused:UNUSED_PAD src0_sel:DWORD src1_sel:BYTE_0
	v_lshlrev_b32_e32 v5, 1, v4
	v_lshrrev_b32_e32 v6, 2, v4
	s_addc_u32 s25, s13, s7
	s_bfe_i64 s[6:7], s[0:1], 0x100000
	v_and_b32_e32 v2, 32, v2
	v_bfe_i32 v3, v3, 0, 16
	v_and_b32_e32 v5, 24, v5
	v_and_b32_e32 v6, 4, v6
	s_lshl_b64 s[6:7], s[6:7], 19
	v_or3_b32 v1, v1, v6, v5
	v_add_lshl_u32 v2, v2, v3, 1
	s_add_u32 s26, s34, s6
	v_lshl_add_u32 v174, v1, 11, v2
	s_addc_u32 s27, s35, s7
	s_add_i32 s23, s36, 0
	s_mov_b64 s[6:7], s[26:27]
	s_add_i32 m0, s23, 0x10000
	v_lshl_add_u32 v175, v4, 11, v2
	global_load_lds_dwordx4 v174, s[6:7]
	s_add_u32 s6, s26, 0x20000
	s_addc_u32 s7, s27, 0
	s_add_i32 m0, s23, 0x12000
	s_nop 0
	global_load_lds_dwordx4 v174, s[6:7]
	s_add_i32 m0, s23, 0x14000
	s_add_u32 s6, s26, 0x40000
	s_addc_u32 s7, s27, 0
	s_nop 0
	global_load_lds_dwordx4 v174, s[6:7]
	s_add_u32 s6, s26, 0x60000
	s_addc_u32 s7, s27, 0
	s_add_i32 m0, s23, 0x16000
	s_nop 0
	global_load_lds_dwordx4 v174, s[6:7]
	s_mov_b64 s[6:7], s[24:25]
	s_mov_b32 m0, s23
	s_nop 0
	global_load_lds_dwordx4 v175, s[6:7]
	s_add_u32 s6, s24, 0x20000
	s_addc_u32 s7, s25, 0
	s_add_i32 s38, s23, 0x2000
	s_mov_b32 m0, s38
	s_add_i32 s39, s23, 0x4000
	global_load_lds_dwordx4 v175, s[6:7]
	s_add_u32 s6, s24, 0x40000
	s_addc_u32 s7, s25, 0
	s_mov_b32 m0, s39
	s_nop 0
	global_load_lds_dwordx4 v175, s[6:7]
	s_add_u32 s6, s24, 0x60000
	s_addc_u32 s7, s25, 0
	s_add_i32 s40, s23, 0x6000
	s_mov_b32 m0, s40
	s_cmp_eq_u32 s11, 1
	global_load_lds_dwordx4 v175, s[6:7]
	s_cselect_b64 s[6:7], -1, 0
	s_cmp_lg_u32 s11, 1
	s_cbranch_scc1 .LBB0_715
	s_barrier
.LBB0_715:
	s_add_u32 s41, s78, 0x42000
	s_addc_u32 s42, s79, 0
	s_lshl_b32 s10, s10, 5
	s_and_b32 s45, s10, 0x60
	s_ashr_i32 s43, s33, 31
	s_lshl_b32 s44, s11, 6
	s_lshl_b32 s12, s11, 13
	s_lshl_b32 s14, s45, 7
	s_add_u32 s10, s26, 0x80
	s_addc_u32 s11, s27, 0
	s_waitcnt vmcnt(2)
	s_barrier
	s_add_i32 m0, s23, 0x18000
	s_sext_i32_i8 s53, s0
	global_load_lds_dwordx4 v174, s[10:11]
	s_add_u32 s10, s26, 0x20080
	s_addc_u32 s11, s27, 0
	s_add_i32 m0, s23, 0x1a000
	v_lshlrev_b32_e32 v2, 6, v0
	global_load_lds_dwordx4 v174, s[10:11]
	s_add_u32 s10, s24, 0x80
	s_addc_u32 s11, s25, 0
	s_add_i32 s48, s23, 0x8000
	s_mov_b32 m0, s48
	s_movk_i32 s0, 0x3c0
	global_load_lds_dwordx4 v175, s[10:11]
	s_add_u32 s10, s24, 0x20080
	s_addc_u32 s11, s25, 0
	s_add_i32 s49, s23, 0xa000
	s_mov_b32 m0, s49
	s_mov_b32 s50, 0
	global_load_lds_dwordx4 v175, s[10:11]
	s_add_i32 m0, s23, 0x1c000
	s_add_u32 s10, s26, 0x40080
	s_addc_u32 s11, s27, 0
	v_mov_b64_e32 v[128:129], 0x100
	global_load_lds_dwordx4 v174, s[10:11]
	s_add_u32 s10, s26, 0x60080
	s_addc_u32 s11, s27, 0
	s_add_i32 m0, s23, 0x1e000
	s_cmpk_lt_u32 s1, 0x100
	global_load_lds_dwordx4 v174, s[10:11]
	v_and_b32_e32 v1, 48, v0
	v_lshlrev_b32_e32 v0, 2, v0
	v_and_or_b32 v1, v2, s0, v1
	v_and_b32_e32 v0, 32, v0
	s_waitcnt vmcnt(6)
	v_bitop3_b32 v2, v1, s12, v0 bitop3:0xde
	v_bitop3_b32 v176, s14, v1, v0 bitop3:0xf6
	s_cselect_b64 s[10:11], -1, 0
	s_add_i32 s51, 0, 0x10000
	s_add_i32 s52, 0, 0x14000
	v_add_u32_e32 v177, s51, v176
	v_add_u32_e32 v178, s52, v176
	v_add_u32_e32 v179, 0, v2
	s_mov_b32 s12, 0x3fb504f3
	s_barrier
	s_branch .LBB0_718

.LBB0_725:
	ds_read_b128 v[130:133], v177
	ds_read_b128 v[134:137], v177 offset:1024
	ds_read_b128 v[138:141], v177 offset:2048
	ds_read_b128 v[142:145], v177 offset:3072
	ds_read_b128 v[146:149], v178
	ds_read_b128 v[150:153], v178 offset:1024
	ds_read_b128 v[154:157], v178 offset:2048
	ds_read_b128 v[158:161], v178 offset:3072
	s_add_u32 s26, s24, 0xfffa0080
	s_addc_u32 s27, s25, -1
	s_cmp_eq_u32 s60, 12
	s_cselect_b32 s26, s18, s26
	s_cselect_b32 s27, s19, s27
	s_cselect_b32 s30, s20, s15
	s_cselect_b32 s31, s21, s17
	s_add_u32 s28, s26, 0x80
	s_addc_u32 s29, s27, 0
	s_add_u32 s64, s24, 0xfffe0000
	v_mov_b32_e32 v200, v175
	s_addc_u32 s65, s25, -1
	ds_read_b128 v[162:165], v179
	ds_read_b128 v[166:169], v179 offset:1024
	ds_read_b128 v[170:173], v179 offset:2048
	ds_read_b128 v[180:183], v179 offset:3072
	ds_read_b128 v[184:187], v179 offset:4096
	ds_read_b128 v[188:191], v179 offset:5120
	ds_read_b128 v[192:195], v179 offset:6144
	ds_read_b128 v[196:199], v179 offset:7168
	s_add_i32 m0, s23, 0xc000
	s_nop 0
	global_load_lds_dwordx4 v200, s[64:65]
	s_mov_b64 s[64:65], s[24:25]
	s_add_i32 m0, s23, 0xe000
	s_nop 0
	global_load_lds_dwordx4 v175, s[64:65]
	s_waitcnt vmcnt(8)
	s_waitcnt lgkmcnt(0)
	s_barrier
	s_setprio 3
	v_mfma_f32_16x16x32_bf16 v[124:127], v[130:133], v[162:165], v[124:127]
	v_mfma_f32_16x16x32_bf16 v[120:123], v[138:141], v[162:165], v[120:123]
	v_mfma_f32_16x16x32_bf16 v[108:111], v[130:133], v[170:173], v[108:111]
	v_mfma_f32_16x16x32_bf16 v[104:107], v[138:141], v[170:173], v[104:107]
	v_mfma_f32_16x16x32_bf16 v[92:95], v[130:133], v[184:187], v[92:95]
	v_mfma_f32_16x16x32_bf16 v[88:91], v[138:141], v[184:187], v[88:91]
	v_mfma_f32_16x16x32_bf16 v[76:79], v[130:133], v[192:195], v[76:79]
	v_mfma_f32_16x16x32_bf16 v[72:75], v[138:141], v[192:195], v[72:75]
	v_mfma_f32_16x16x32_bf16 v[124:127], v[134:137], v[166:169], v[124:127]
	v_mfma_f32_16x16x32_bf16 v[120:123], v[142:145], v[166:169], v[120:123]
	v_mfma_f32_16x16x32_bf16 v[108:111], v[134:137], v[180:183], v[108:111]
	v_mfma_f32_16x16x32_bf16 v[104:107], v[142:145], v[180:183], v[104:107]
	v_mfma_f32_16x16x32_bf16 v[92:95], v[134:137], v[188:191], v[92:95]
	v_mfma_f32_16x16x32_bf16 v[88:91], v[142:145], v[188:191], v[88:91]
	v_mfma_f32_16x16x32_bf16 v[76:79], v[134:137], v[196:199], v[76:79]
	v_mfma_f32_16x16x32_bf16 v[72:75], v[142:145], v[196:199], v[72:75]
	v_mfma_f32_16x16x32_bf16 v[116:119], v[146:149], v[162:165], v[116:119]
	v_mfma_f32_16x16x32_bf16 v[112:115], v[154:157], v[162:165], v[112:115]
	v_mfma_f32_16x16x32_bf16 v[100:103], v[146:149], v[170:173], v[100:103]
	v_mfma_f32_16x16x32_bf16 v[96:99], v[154:157], v[170:173], v[96:99]
	v_mfma_f32_16x16x32_bf16 v[84:87], v[146:149], v[184:187], v[84:87]
	v_mfma_f32_16x16x32_bf16 v[80:83], v[154:157], v[184:187], v[80:83]
	v_mfma_f32_16x16x32_bf16 v[68:71], v[146:149], v[192:195], v[68:71]
	v_mfma_f32_16x16x32_bf16 v[64:67], v[154:157], v[192:195], v[64:67]
	v_mfma_f32_16x16x32_bf16 v[116:119], v[150:153], v[166:169], v[116:119]
	v_mfma_f32_16x16x32_bf16 v[112:115], v[158:161], v[166:169], v[112:115]
	v_mfma_f32_16x16x32_bf16 v[100:103], v[150:153], v[180:183], v[100:103]
	v_mfma_f32_16x16x32_bf16 v[96:99], v[158:161], v[180:183], v[96:99]
	v_mfma_f32_16x16x32_bf16 v[84:87], v[150:153], v[188:191], v[84:87]
	v_mfma_f32_16x16x32_bf16 v[80:83], v[158:161], v[188:191], v[80:83]
	v_mfma_f32_16x16x32_bf16 v[68:71], v[150:153], v[196:199], v[68:71]
	v_mfma_f32_16x16x32_bf16 v[64:67], v[158:161], v[196:199], v[64:67]
	s_setprio 0
	s_barrier
	v_mov_b32_e32 v200, v174
	s_mov_b64 s[64:65], s[30:31]
	s_add_i32 s61, s51, s36
	ds_read_b128 v[162:165], v179 offset:16384
	ds_read_b128 v[166:169], v179 offset:17408
	ds_read_b128 v[170:173], v179 offset:18432
	ds_read_b128 v[180:183], v179 offset:19456
	ds_read_b128 v[184:187], v179 offset:20480
	ds_read_b128 v[188:191], v179 offset:21504
	ds_read_b128 v[192:195], v179 offset:22528
	ds_read_b128 v[196:199], v179 offset:23552
	s_mov_b32 m0, s61
	s_nop 0
	global_load_lds_dwordx4 v200, s[64:65]
	s_add_u32 s64, s30, 0x20000
	s_addc_u32 s65, s31, 0
	s_add_i32 m0, s61, 0x2000
	s_nop 0
	global_load_lds_dwordx4 v174, s[64:65]
	s_add_u32 s64, s30, 0x40000
	s_addc_u32 s65, s31, 0
	s_add_i32 s61, s52, s36
	s_mov_b32 m0, s61
	s_nop 0
	global_load_lds_dwordx4 v174, s[64:65]
	s_add_u32 s64, s30, 0x60000
	s_addc_u32 s65, s31, 0
	s_add_i32 m0, s61, 0x2000
	s_nop 0
	global_load_lds_dwordx4 v174, s[64:65]
	s_mov_b64 s[64:65], s[26:27]
	s_mov_b32 m0, s23
	s_nop 0
	global_load_lds_dwordx4 v175, s[64:65]
	s_add_u32 s64, s26, 0x20000
	s_addc_u32 s65, s27, 0
	s_mov_b32 m0, s38
	s_nop 0
	global_load_lds_dwordx4 v175, s[64:65]
	s_waitcnt vmcnt(8)
	s_waitcnt lgkmcnt(0)
	s_barrier
	s_setprio 3
	v_mfma_f32_16x16x32_bf16 v[60:63], v[130:133], v[162:165], v[60:63]
	v_mfma_f32_16x16x32_bf16 v[56:59], v[138:141], v[162:165], v[56:59]
	v_mfma_f32_16x16x32_bf16 v[44:47], v[130:133], v[170:173], v[44:47]
	v_mfma_f32_16x16x32_bf16 v[40:43], v[138:141], v[170:173], v[40:43]
	v_mfma_f32_16x16x32_bf16 v[28:31], v[130:133], v[184:187], v[28:31]
	v_mfma_f32_16x16x32_bf16 v[24:27], v[138:141], v[184:187], v[24:27]
	v_mfma_f32_16x16x32_bf16 v[12:15], v[130:133], v[192:195], v[12:15]
	v_mfma_f32_16x16x32_bf16 v[8:11], v[138:141], v[192:195], v[8:11]
	v_mfma_f32_16x16x32_bf16 v[60:63], v[134:137], v[166:169], v[60:63]
	v_mfma_f32_16x16x32_bf16 v[56:59], v[142:145], v[166:169], v[56:59]
	v_mfma_f32_16x16x32_bf16 v[44:47], v[134:137], v[180:183], v[44:47]
	v_mfma_f32_16x16x32_bf16 v[40:43], v[142:145], v[180:183], v[40:43]
	v_mfma_f32_16x16x32_bf16 v[28:31], v[134:137], v[188:191], v[28:31]
	v_mfma_f32_16x16x32_bf16 v[24:27], v[142:145], v[188:191], v[24:27]
	v_mfma_f32_16x16x32_bf16 v[12:15], v[134:137], v[196:199], v[12:15]
	v_mfma_f32_16x16x32_bf16 v[8:11], v[142:145], v[196:199], v[8:11]
	v_mfma_f32_16x16x32_bf16 v[52:55], v[146:149], v[162:165], v[52:55]
	v_mfma_f32_16x16x32_bf16 v[48:51], v[154:157], v[162:165], v[48:51]
	v_mfma_f32_16x16x32_bf16 v[36:39], v[146:149], v[170:173], v[36:39]
	v_mfma_f32_16x16x32_bf16 v[32:35], v[154:157], v[170:173], v[32:35]
	v_mfma_f32_16x16x32_bf16 v[20:23], v[146:149], v[184:187], v[20:23]
	v_mfma_f32_16x16x32_bf16 v[16:19], v[154:157], v[184:187], v[16:19]
	v_mfma_f32_16x16x32_bf16 v[4:7], v[146:149], v[192:195], v[4:7]
	v_mfma_f32_16x16x32_bf16 v[0:3], v[154:157], v[192:195], v[0:3]
	v_mfma_f32_16x16x32_bf16 v[52:55], v[150:153], v[166:169], v[52:55]
	v_mfma_f32_16x16x32_bf16 v[48:51], v[158:161], v[166:169], v[48:51]
	v_mfma_f32_16x16x32_bf16 v[36:39], v[150:153], v[180:183], v[36:39]
	v_mfma_f32_16x16x32_bf16 v[32:35], v[158:161], v[180:183], v[32:35]
	v_mfma_f32_16x16x32_bf16 v[20:23], v[150:153], v[188:191], v[20:23]
	v_mfma_f32_16x16x32_bf16 v[16:19], v[158:161], v[188:191], v[16:19]
	v_mfma_f32_16x16x32_bf16 v[4:7], v[150:153], v[196:199], v[4:7]
	v_mfma_f32_16x16x32_bf16 v[0:3], v[158:161], v[196:199], v[0:3]
	s_setprio 0
	s_barrier
	s_add_i32 s61, 0, 0x18000
	s_add_i32 s68, 0, 0x1c000
	v_add_u32_e32 v142, s61, v176
	v_add_u32_e32 v158, s68, v176
	ds_read_b128 v[130:133], v142
	ds_read_b128 v[134:137], v142 offset:1024
	ds_read_b128 v[138:141], v142 offset:2048
	ds_read_b128 v[142:145], v142 offset:3072
	ds_read_b128 v[146:149], v158
	ds_read_b128 v[150:153], v158 offset:1024
	ds_read_b128 v[154:157], v158 offset:2048
	ds_read_b128 v[158:161], v158 offset:3072
	s_add_u32 s64, s26, 0x40000
	v_mov_b32_e32 v200, v175
	s_addc_u32 s65, s27, 0
	s_mov_b32 m0, s39
	ds_read_b128 v[162:165], v179 offset:32768
	ds_read_b128 v[166:169], v179 offset:33792
	ds_read_b128 v[170:173], v179 offset:34816
	ds_read_b128 v[180:183], v179 offset:35840
	ds_read_b128 v[184:187], v179 offset:36864
	ds_read_b128 v[188:191], v179 offset:37888
	ds_read_b128 v[192:195], v179 offset:38912
	ds_read_b128 v[196:199], v179 offset:39936
	s_nop 0
	global_load_lds_dwordx4 v200, s[64:65]
	s_add_u32 s64, s26, 0x60000
	s_addc_u32 s65, s27, 0
	s_mov_b32 m0, s40
	s_nop 0
	global_load_lds_dwordx4 v175, s[64:65]
	s_waitcnt vmcnt(8)
	s_waitcnt lgkmcnt(0)
	s_barrier
	s_setprio 3
	v_mfma_f32_16x16x32_bf16 v[124:127], v[130:133], v[162:165], v[124:127]
	v_mfma_f32_16x16x32_bf16 v[120:123], v[138:141], v[162:165], v[120:123]
	v_mfma_f32_16x16x32_bf16 v[108:111], v[130:133], v[170:173], v[108:111]
	v_mfma_f32_16x16x32_bf16 v[104:107], v[138:141], v[170:173], v[104:107]
	v_mfma_f32_16x16x32_bf16 v[92:95], v[130:133], v[184:187], v[92:95]
	v_mfma_f32_16x16x32_bf16 v[88:91], v[138:141], v[184:187], v[88:91]
	v_mfma_f32_16x16x32_bf16 v[76:79], v[130:133], v[192:195], v[76:79]
	v_mfma_f32_16x16x32_bf16 v[72:75], v[138:141], v[192:195], v[72:75]
	v_mfma_f32_16x16x32_bf16 v[124:127], v[134:137], v[166:169], v[124:127]
	v_mfma_f32_16x16x32_bf16 v[120:123], v[142:145], v[166:169], v[120:123]
	v_mfma_f32_16x16x32_bf16 v[108:111], v[134:137], v[180:183], v[108:111]
	v_mfma_f32_16x16x32_bf16 v[104:107], v[142:145], v[180:183], v[104:107]
	v_mfma_f32_16x16x32_bf16 v[92:95], v[134:137], v[188:191], v[92:95]
	v_mfma_f32_16x16x32_bf16 v[88:91], v[142:145], v[188:191], v[88:91]
	v_mfma_f32_16x16x32_bf16 v[76:79], v[134:137], v[196:199], v[76:79]
	v_mfma_f32_16x16x32_bf16 v[72:75], v[142:145], v[196:199], v[72:75]
	v_mfma_f32_16x16x32_bf16 v[116:119], v[146:149], v[162:165], v[116:119]
	v_mfma_f32_16x16x32_bf16 v[112:115], v[154:157], v[162:165], v[112:115]
	v_mfma_f32_16x16x32_bf16 v[100:103], v[146:149], v[170:173], v[100:103]
	v_mfma_f32_16x16x32_bf16 v[96:99], v[154:157], v[170:173], v[96:99]
	v_mfma_f32_16x16x32_bf16 v[84:87], v[146:149], v[184:187], v[84:87]
	v_mfma_f32_16x16x32_bf16 v[80:83], v[154:157], v[184:187], v[80:83]
	v_mfma_f32_16x16x32_bf16 v[68:71], v[146:149], v[192:195], v[68:71]
	v_mfma_f32_16x16x32_bf16 v[64:67], v[154:157], v[192:195], v[64:67]
	v_mfma_f32_16x16x32_bf16 v[116:119], v[150:153], v[166:169], v[116:119]
	v_mfma_f32_16x16x32_bf16 v[112:115], v[158:161], v[166:169], v[112:115]
	v_mfma_f32_16x16x32_bf16 v[100:103], v[150:153], v[180:183], v[100:103]
	v_mfma_f32_16x16x32_bf16 v[96:99], v[158:161], v[180:183], v[96:99]
	v_mfma_f32_16x16x32_bf16 v[84:87], v[150:153], v[188:191], v[84:87]
	v_mfma_f32_16x16x32_bf16 v[80:83], v[158:161], v[188:191], v[80:83]
	v_mfma_f32_16x16x32_bf16 v[68:71], v[150:153], v[196:199], v[68:71]
	v_mfma_f32_16x16x32_bf16 v[64:67], v[158:161], v[196:199], v[64:67]
	s_setprio 0
	s_barrier
	s_add_u32 s64, s30, 0x80
	s_addc_u32 s65, s31, 0
	v_mov_b32_e32 v200, v174
	s_add_i32 s61, s61, s36
	ds_read_b128 v[162:165], v179 offset:49152
	ds_read_b128 v[166:169], v179 offset:50176
	ds_read_b128 v[170:173], v179 offset:51200
	ds_read_b128 v[180:183], v179 offset:52224
	ds_read_b128 v[184:187], v179 offset:53248
	ds_read_b128 v[188:191], v179 offset:54272
	ds_read_b128 v[192:195], v179 offset:55296
	ds_read_b128 v[196:199], v179 offset:56320
	s_mov_b32 m0, s61
	s_nop 0
	global_load_lds_dwordx4 v200, s[64:65]
	s_add_u32 s64, s30, 0x20080
	s_addc_u32 s65, s31, 0
	s_add_i32 m0, s61, 0x2000
	s_nop 0
	global_load_lds_dwordx4 v174, s[64:65]
	s_add_u32 s64, s30, 0x40080
	s_addc_u32 s65, s31, 0
	s_add_i32 s61, s68, s36
	s_mov_b32 m0, s61
	s_add_u32 s30, s30, 0x60080
	global_load_lds_dwordx4 v174, s[64:65]
	s_addc_u32 s31, s31, 0
	s_add_i32 m0, s61, 0x2000
	s_add_u32 s26, s26, 0x20080
	global_load_lds_dwordx4 v174, s[30:31]
	s_mov_b32 m0, s48
	s_addc_u32 s27, s27, 0
	global_load_lds_dwordx4 v175, s[28:29]
	s_mov_b32 m0, s49
	s_nop 0
	global_load_lds_dwordx4 v175, s[26:27]
	s_waitcnt vmcnt(8)
	s_waitcnt lgkmcnt(0)
	s_barrier
	s_setprio 3
	v_mfma_f32_16x16x32_bf16 v[60:63], v[130:133], v[162:165], v[60:63]
	v_mfma_f32_16x16x32_bf16 v[56:59], v[138:141], v[162:165], v[56:59]
	v_mfma_f32_16x16x32_bf16 v[44:47], v[130:133], v[170:173], v[44:47]
	v_mfma_f32_16x16x32_bf16 v[40:43], v[138:141], v[170:173], v[40:43]
	v_mfma_f32_16x16x32_bf16 v[28:31], v[130:133], v[184:187], v[28:31]
	v_mfma_f32_16x16x32_bf16 v[24:27], v[138:141], v[184:187], v[24:27]
	v_mfma_f32_16x16x32_bf16 v[12:15], v[130:133], v[192:195], v[12:15]
	v_mfma_f32_16x16x32_bf16 v[8:11], v[138:141], v[192:195], v[8:11]
	v_mfma_f32_16x16x32_bf16 v[60:63], v[134:137], v[166:169], v[60:63]
	v_mfma_f32_16x16x32_bf16 v[56:59], v[142:145], v[166:169], v[56:59]
	v_mfma_f32_16x16x32_bf16 v[44:47], v[134:137], v[180:183], v[44:47]
	v_mfma_f32_16x16x32_bf16 v[40:43], v[142:145], v[180:183], v[40:43]
	v_mfma_f32_16x16x32_bf16 v[28:31], v[134:137], v[188:191], v[28:31]
	v_mfma_f32_16x16x32_bf16 v[24:27], v[142:145], v[188:191], v[24:27]
	v_mfma_f32_16x16x32_bf16 v[12:15], v[134:137], v[196:199], v[12:15]
	v_mfma_f32_16x16x32_bf16 v[8:11], v[142:145], v[196:199], v[8:11]
	v_mfma_f32_16x16x32_bf16 v[52:55], v[146:149], v[162:165], v[52:55]
	v_mfma_f32_16x16x32_bf16 v[48:51], v[154:157], v[162:165], v[48:51]
	v_mfma_f32_16x16x32_bf16 v[36:39], v[146:149], v[170:173], v[36:39]
	v_mfma_f32_16x16x32_bf16 v[32:35], v[154:157], v[170:173], v[32:35]
	v_mfma_f32_16x16x32_bf16 v[20:23], v[146:149], v[184:187], v[20:23]
	v_mfma_f32_16x16x32_bf16 v[16:19], v[154:157], v[184:187], v[16:19]
	v_mfma_f32_16x16x32_bf16 v[4:7], v[146:149], v[192:195], v[4:7]
	v_mfma_f32_16x16x32_bf16 v[0:3], v[154:157], v[192:195], v[0:3]
	v_mfma_f32_16x16x32_bf16 v[52:55], v[150:153], v[166:169], v[52:55]
	v_mfma_f32_16x16x32_bf16 v[48:51], v[158:161], v[166:169], v[48:51]
	v_mfma_f32_16x16x32_bf16 v[36:39], v[150:153], v[180:183], v[36:39]
	v_mfma_f32_16x16x32_bf16 v[32:35], v[158:161], v[180:183], v[32:35]
	v_mfma_f32_16x16x32_bf16 v[20:23], v[150:153], v[188:191], v[20:23]
	v_mfma_f32_16x16x32_bf16 v[16:19], v[158:161], v[188:191], v[16:19]
	v_mfma_f32_16x16x32_bf16 v[4:7], v[150:153], v[196:199], v[4:7]
	v_mfma_f32_16x16x32_bf16 v[0:3], v[158:161], v[196:199], v[0:3]
	s_setprio 0
	s_barrier
	s_add_i32 s60, s60, 2
	s_add_u32 s15, s15, 0x100
	s_addc_u32 s17, s17, 0
	s_add_u32 s24, s24, 0x100
	s_addc_u32 s25, s25, 0
	s_cmp_gt_u32 s60, 13
	s_cbranch_scc0 .LBB0_725
	s_and_b64 vcc, exec, s[10:11]
	s_cbranch_vccz .LBB0_728
	s_barrier

.LBB0_942:
	s_add_i32 s3, 0, 0x24808
	v_mov_b32_e32 v3, s3
	ds_read_b32 v4, v3
	s_mov_b64 s[0:1], exec
	v_mbcnt_lo_u32_b32 v2, s0, 0
	v_mbcnt_hi_u32_b32 v2, s1, v2
	v_cmp_eq_u32_e32 vcc, 0, v2
	s_waitcnt lgkmcnt(0)
	v_add_u32_e32 v4, 1, v4
	v_mov_b32_e32 v7, v4
	ds_write_b32 v3, v4
	s_and_saveexec_b64 s[14:15], vcc
	s_cbranch_execz .LBB0_944
	v_readlane_b32 s3, v249, 34
	s_lshl_b32 s3, s3, 8
	s_add_u32 s16, s94, s3
	s_addc_u32 s17, s95, 0
	s_bcnt1_i32_b64 s0, s[0:1]
	v_mov_b32_e32 v3, 0x1000
	v_mov_b32_e32 v4, s0
	global_atomic_add v3, v3, v4, s[16:17] offset:1024 sc0
.LBB0_944:
	s_or_b64 exec, exec, s[14:15]
	s_waitcnt vmcnt(0)
	v_readfirstlane_b32 s0, v3
	s_nop 1
	v_add_u32_e32 v2, s0, v2
	v_add_u32_e32 v5, 1, v2
	v_mul_lo_u32 v1, v1, v7
	v_add_u32_e32 v2, -1, v7
	v_cmp_eq_u32_e64 s[0:1], v5, v1
	v_cmp_ne_u32_e32 vcc, v5, v1
	s_nop 0
	v_cndmask_b32_e64 v1, 0, 1, s[0:1]
	s_add_i32 s0, 0, 0x2480c
	v_mov_b32_e32 v3, s0
	s_add_i32 s0, 0, 0x24810
	ds_write_b32 v3, v1
	v_mov_b32_e32 v1, s0
	ds_write_b32 v1, v2
	s_and_saveexec_b64 s[0:1], vcc
	s_xor_b64 s[0:1], exec, s[0:1]
	s_cbranch_execz .LBB0_947
	s_add_i32 s3, 0, 0x24808
	v_mov_b32_e32 v0, s3
	ds_read_b32 v0, v0
	s_waitcnt lgkmcnt(0)
	v_and_b32_e32 v0, 1, v0
	v_cmp_eq_u32_e32 vcc, 0, v0
	s_cbranch_vccnz .LBB0_947
	buffer_inv sc1
	s_waitcnt vmcnt(0)
.LBB0_947:
	s_andn2_saveexec_b64 s[0:1], s[0:1]
	s_cbranch_execz .LBB0_954
	s_mov_b64 s[0:1], exec
	buffer_wbl2 sc1
	s_waitcnt lgkmcnt(0)
	s_waitcnt vmcnt(0)
	v_mbcnt_lo_u32_b32 v1, s0, 0
	v_mbcnt_hi_u32_b32 v1, s1, v1
	v_cmp_eq_u32_e32 vcc, 0, v1
	s_and_saveexec_b64 s[14:15], vcc
	s_cbranch_execz .LBB0_950
	s_bcnt1_i32_b64 s0, s[0:1]
	v_mov_b32_e32 v2, 0x3000
	v_mov_b32_e32 v3, s0
	global_atomic_add v2, v3, s[94:95] offset:1024
.LBB0_950:
	s_or_b64 exec, exec, s[14:15]
	s_branch .LBB0_954
	v_cvt_f32_u32_e32 v3, v0
	s_waitcnt vmcnt(0)
	v_readfirstlane_b32 s0, v2
	v_sub_u32_e32 v2, 0, v0
	v_rcp_iflag_f32_e32 v3, v3
	v_add_u32_e32 v1, s0, v1
	v_mul_f32_e32 v3, 0x4f7ffffe, v3
	v_cvt_u32_f32_e32 v3, v3
	v_mul_lo_u32 v2, v2, v3
	v_mul_hi_u32 v2, v3, v2
	v_add_u32_e32 v2, v3, v2
	v_mul_hi_u32 v2, v1, v2
	v_mul_lo_u32 v3, v2, v0
	v_sub_u32_e32 v3, v1, v3
	v_add_u32_e32 v4, 1, v2
	v_cmp_ge_u32_e32 vcc, v3, v0
	v_add_u32_e32 v1, 1, v1
	s_nop 0
	v_cndmask_b32_e32 v2, v2, v4, vcc
	v_sub_u32_e32 v4, v3, v0
	v_cndmask_b32_e32 v3, v3, v4, vcc
	v_add_u32_e32 v4, 1, v2
	v_cmp_ge_u32_e32 vcc, v3, v0
	s_nop 1
	v_cndmask_b32_e32 v2, v2, v4, vcc
	v_mul_lo_u32 v2, v0, v2
	v_add_u32_e32 v0, v2, v0
	v_cmp_eq_u32_e32 vcc, v1, v0
	s_and_saveexec_b64 s[0:1], vcc
	s_cbranch_execz .LBB0_953
	s_mov_b64 s[14:15], exec
	v_mbcnt_lo_u32_b32 v0, s14, 0
	v_mbcnt_hi_u32_b32 v0, s15, v0
	v_cmp_eq_u32_e32 vcc, 0, v0
	s_and_b64 s[16:17], exec, vcc
	s_mov_b64 exec, s[16:17]
	s_cbranch_execz .LBB0_953
	s_bcnt1_i32_b64 s3, s[14:15]
	v_mov_b32_e32 v0, 0x3000
	v_mov_b32_e32 v1, s3
	global_atomic_add v0, v1, s[94:95] offset:1280

.LBB0_1106:
	s_or_b64 exec, exec, s[14:15]
	s_waitcnt vmcnt(0)
	v_ashrrev_i32_e32 v9, 1, v240
	v_lshlrev_b32_e32 v241, 15, v241
	v_and_b32_e32 v10, 0xffff0000, v241
	v_ashrrev_i32_e32 v7, 1, v242
	v_lshlrev_b32_e32 v243, 15, v243
	v_and_b32_e32 v5, 0xffff0000, v243
	v_bfe_i32 v4, v8, 27, 1
	v_lshlrev_b32_e32 v2, 4, v8
	v_lshrrev_b32_e32 v4, 22, v4
	v_add_u32_e32 v4, v2, v4
	v_and_b32_e32 v4, 0xfffffc00, v4
	v_sub_u32_e32 v2, v2, v4
	v_ashrrev_i32_e32 v3, 31, v8
	v_lshrrev_b32_e32 v4, 4, v2
	v_lshrrev_b32_e32 v3, 26, v3
	v_bitop3_b32 v4, v4, v2, 32 bitop3:0x6c
	v_ashrrev_i32_e32 v2, 31, v2
	v_add_u32_e32 v3, v8, v3
	v_lshrrev_b32_e32 v2, 26, v2
	v_ashrrev_i32_e32 v3, 6, v3
	v_add_u32_e32 v2, v4, v2
	v_lshlrev_b32_e32 v6, 3, v3
	v_ashrrev_i32_e32 v2, 6, v2
	v_or_b32_e32 v128, v10, v9
	v_and_b32_e32 v6, -16, v6
	v_mul_i32_i24_e32 v10, 64, v2
	v_add_u32_e32 v6, v2, v6
	v_sub_u32_e32 v4, v4, v10
	v_mov_b32_e32 v10, 1
	s_and_b32 s64, s16, 1
	v_lshlrev_b32_e32 v3, 5, v3
	v_ashrrev_i16_sdwa v4, v10, sext(v4) dst_sel:DWORD dst_unused:UNUSED_PAD src0_sel:DWORD src1_sel:BYTE_0
	v_lshlrev_b32_e32 v10, 1, v6
	v_lshrrev_b32_e32 v11, 2, v6
	v_and_b32_e32 v2, 3, v2
	s_mov_b32 s14, 0x3fffe0
	v_lshlrev_b64 v[0:1], 19, v[0:1]
	v_and_b32_e32 v3, 32, v3
	v_bfe_i32 v4, v4, 0, 16
	v_and_b32_e32 v10, 24, v10
	v_and_b32_e32 v11, 4, v11
	v_and_or_b32 v2, v6, s14, v2
	v_lshl_add_u64 v[0:1], s[4:5], 0, v[0:1]
	s_lshl_b32 s14, s64, 18
	s_mov_b32 s15, 0
	s_ashr_i32 s19, s18, 6
	v_or3_b32 v2, v2, v11, v10
	v_add_lshl_u32 v3, v3, v4, 1
	v_lshl_add_u64 v[0:1], v[0:1], 0, s[14:15]
	v_lshl_add_u32 v134, v2, 10, v3
	s_lshl_b32 s35, s19, 10
	v_readfirstlane_b32 s23, v1
	v_readfirstlane_b32 s22, v0
	s_add_i32 s36, s35, 0
	s_mov_b64 s[16:17], s[22:23]
	s_ashr_i32 s20, s18, 8
	s_add_i32 m0, s36, 0x10000
	v_and_b32_e32 v135, 0x7e, v3
	global_load_lds_dwordx4 v134, s[16:17]
	s_add_u32 s16, s22, 0x10000
	s_addc_u32 s17, s23, 0
	s_add_i32 m0, s36, 0x12000
	s_mov_b32 s37, 0x3fffc00
	global_load_lds_dwordx4 v134, s[16:17]
	s_add_i32 m0, s36, 0x14000
	s_add_u32 s16, s22, 0x20000
	s_addc_u32 s17, s23, 0
	v_or_b32_e32 v129, v5, v7
	global_load_lds_dwordx4 v134, s[16:17]
	s_add_u32 s16, s22, 0x30000
	s_addc_u32 s17, s23, 0
	s_add_i32 m0, s36, 0x16000
	s_add_i32 s38, s36, 0x2000
	global_load_lds_dwordx4 v134, s[16:17]
	v_lshlrev_b32_e32 v0, 10, v9
	v_and_or_b32 v0, v0, s37, v135
	s_mov_b64 s[16:17], s[8:9]
	s_mov_b32 m0, s36
	s_add_i32 s39, s36, 0x4000
	global_load_lds_dwordx4 v0, s[16:17]
	v_lshlrev_b32_e32 v1, 10, v7
	v_and_or_b32 v1, v1, s37, v135
	s_mov_b64 s[16:17], s[8:9]
	s_mov_b32 m0, s38
	s_add_i32 s40, s36, 0x6000
	global_load_lds_dwordx4 v1, s[16:17]
	v_bfe_u32 v2, v128, 16, 16
	v_lshl_or_b32 v2, v2, 10, v135
	s_mov_b64 s[16:17], s[8:9]
	s_mov_b32 m0, s39
	s_cmp_eq_u32 s20, 1
	global_load_lds_dwordx4 v2, s[16:17]
	v_bfe_u32 v2, v129, 16, 16
	v_lshl_or_b32 v2, v2, 10, v135
	s_mov_b64 s[16:17], s[8:9]
	s_mov_b32 m0, s40
	s_nop 0
	global_load_lds_dwordx4 v2, s[16:17]
	s_cselect_b64 s[16:17], -1, 0
	s_cmp_lg_u32 s20, 1
	s_cbranch_scc1 .LBB0_1108
	s_barrier
.LBB0_1108:
	s_lshl_b32 s19, s19, 5
	s_and_b32 s42, s19, 0x60
	s_lshl_b32 s41, s20, 6
	s_lshl_b32 s14, s20, 13
	s_lshl_b32 s19, s42, 7
	s_add_u32 s20, s22, 0x80
	s_addc_u32 s21, s23, 0
	s_waitcnt vmcnt(2)
	s_barrier
	s_add_i32 m0, s36, 0x18000
	v_mov_b32_e32 v140, 0
	global_load_lds_dwordx4 v134, s[20:21]
	s_add_u32 s20, s22, 0x10080
	s_addc_u32 s21, s23, 0
	s_add_i32 m0, s36, 0x1a000
	s_mov_b32 s53, 0
	global_load_lds_dwordx4 v134, s[20:21]
	s_add_u32 s20, s8, 0x80
	s_addc_u32 s21, s9, 0
	s_add_i32 s43, s36, 0x8000
	s_mov_b64 s[24:25], s[20:21]
	s_mov_b32 m0, s43
	s_add_i32 s44, s36, 0xa000
	v_mov_b32_e32 v142, v129
	global_load_lds_dwordx4 v0, s[24:25]
	s_mov_b32 m0, s44
	s_nop 0
	global_load_lds_dwordx4 v1, s[20:21]
	s_add_i32 m0, s36, 0x1c000
	s_add_u32 s20, s22, 0x20080
	s_addc_u32 s21, s23, 0
	v_lshlrev_b32_e32 v1, 6, v8
	global_load_lds_dwordx4 v134, s[20:21]
	s_add_u32 s20, s22, 0x30080
	s_addc_u32 s21, s23, 0
	s_add_i32 m0, s36, 0x1e000
	s_cmpk_lt_u32 s18, 0x100
	global_load_lds_dwordx4 v134, s[20:21]
	v_and_b32_e32 v0, 48, v8
	s_movk_i32 s20, 0x3c0
	v_and_or_b32 v0, v1, s20, v0
	v_lshlrev_b32_e32 v1, 2, v8
	v_and_b32_e32 v1, 32, v1
	v_bitop3_b32 v2, v0, s14, v1 bitop3:0xde
	v_bitop3_b32 v136, s19, v0, v1 bitop3:0xf6
	s_cselect_b64 s[18:19], -1, 0
	s_and_b32 s14, s2, 7
	s_ashr_i32 s20, s33, 3
	s_mul_i32 s14, s20, s14
	s_ashr_i32 s20, s2, 3
	s_add_i32 s14, s14, s20
	s_waitcnt vmcnt(6)
	s_and_b64 s[0:1], s[0:1], exec
	s_cselect_b32 s45, s14, s2
	s_add_i32 s52, 0, 0x10000
	s_add_i32 s48, 0, 0x14000
	v_add_u32_e32 v137, s52, v136
	v_add_u32_e32 v138, s48, v136
	v_add_u32_e32 v139, 0, v2
	s_add_i32 s49, s36, 0xc000
	s_add_i32 s51, s36, 0xe000
	s_add_i32 s52, s52, s35
	v_mov_b32_e32 v141, v128
	s_barrier
	s_branch .LBB0_1111

.LBB0_1124:
	ds_read_b128 v[144:147], v137
	ds_read_b128 v[148:151], v137 offset:1024
	ds_read_b128 v[152:155], v137 offset:2048
	ds_read_b128 v[156:159], v137 offset:3072
	ds_read_b128 v[160:163], v138
	ds_read_b128 v[164:167], v138 offset:1024
	ds_read_b128 v[168:171], v138 offset:2048
	ds_read_b128 v[172:175], v138 offset:3072
	s_cmp_eq_u32 s70, 4
	s_cselect_b64 vcc, -1, 0
	s_and_b64 s[22:23], vcc, exec
	s_cselect_b32 s26, s8, s68
	s_cselect_b32 s27, s9, s69
	s_cselect_b32 s24, s20, s14
	s_cselect_b32 s25, s21, s65
	s_add_u32 s22, s26, 0x80
	s_addc_u32 s23, s27, 0
	s_add_u32 s72, s68, 0xffffff80
	s_addc_u32 s73, s69, -1
	v_mov_b32_e32 v132, v130
	s_mov_b32 m0, s49
	ds_read_b128 v[176:179], v139
	ds_read_b128 v[180:183], v139 offset:1024
	ds_read_b128 v[184:187], v139 offset:2048
	ds_read_b128 v[188:191], v139 offset:3072
	ds_read_b128 v[192:195], v139 offset:4096
	ds_read_b128 v[196:199], v139 offset:5120
	ds_read_b128 v[200:203], v139 offset:6144
	ds_read_b128 v[204:207], v139 offset:7168
	s_mov_b64 s[74:75], s[72:73]
	s_nop 0
	global_load_lds_dwordx4 v132, s[74:75]
	s_mov_b32 m0, s51
	s_nop 0
	global_load_lds_dwordx4 v131, s[72:73]
	s_waitcnt vmcnt(8)
	s_waitcnt lgkmcnt(0)
	s_barrier
	s_setprio 3
	v_mfma_f32_16x16x128_f8f6f4 v[124:127], v[144:151], v[176:183], v[124:127]
	v_mfma_f32_16x16x128_f8f6f4 v[116:119], v[152:159], v[176:183], v[116:119]
	v_mfma_f32_16x16x128_f8f6f4 v[108:111], v[144:151], v[184:191], v[108:111]
	v_mfma_f32_16x16x128_f8f6f4 v[100:103], v[152:159], v[184:191], v[100:103]
	v_mfma_f32_16x16x128_f8f6f4 v[92:95], v[144:151], v[192:199], v[92:95]
	v_mfma_f32_16x16x128_f8f6f4 v[84:87], v[152:159], v[192:199], v[84:87]
	v_mfma_f32_16x16x128_f8f6f4 v[76:79], v[144:151], v[200:207], v[76:79]
	v_mfma_f32_16x16x128_f8f6f4 v[68:71], v[152:159], v[200:207], v[68:71]
	v_mfma_f32_16x16x128_f8f6f4 v[120:123], v[160:167], v[176:183], v[120:123]
	v_mfma_f32_16x16x128_f8f6f4 v[112:115], v[168:175], v[176:183], v[112:115]
	v_mfma_f32_16x16x128_f8f6f4 v[104:107], v[160:167], v[184:191], v[104:107]
	v_mfma_f32_16x16x128_f8f6f4 v[96:99], v[168:175], v[184:191], v[96:99]
	v_mfma_f32_16x16x128_f8f6f4 v[88:91], v[160:167], v[192:199], v[88:91]
	v_mfma_f32_16x16x128_f8f6f4 v[80:83], v[168:175], v[192:199], v[80:83]
	v_mfma_f32_16x16x128_f8f6f4 v[72:75], v[160:167], v[200:207], v[72:75]
	v_mfma_f32_16x16x128_f8f6f4 v[64:67], v[168:175], v[200:207], v[64:67]
	s_setprio 0
	s_barrier
	v_mov_b32_e32 v132, v134
	s_mov_b64 s[72:73], s[24:25]
	s_mov_b32 m0, s52
	ds_read_b128 v[176:179], v139 offset:16384
	ds_read_b128 v[180:183], v139 offset:17408
	ds_read_b128 v[184:187], v139 offset:18432
	ds_read_b128 v[188:191], v139 offset:19456
	ds_read_b128 v[192:195], v139 offset:20480
	ds_read_b128 v[196:199], v139 offset:21504
	ds_read_b128 v[200:203], v139 offset:22528
	ds_read_b128 v[204:207], v139 offset:23552
	s_nop 0
	global_load_lds_dwordx4 v132, s[72:73]
	s_add_u32 s72, s24, 0x10000
	s_addc_u32 s73, s25, 0
	s_add_i32 m0, s52, 0x2000
	s_nop 0
	global_load_lds_dwordx4 v134, s[72:73]
	s_add_u32 s72, s24, 0x20000
	s_addc_u32 s73, s25, 0
	s_add_i32 s71, s48, s35
	s_mov_b32 m0, s71
	s_nop 0
	global_load_lds_dwordx4 v134, s[72:73]
	s_add_u32 s72, s24, 0x30000
	s_addc_u32 s73, s25, 0
	s_add_i32 m0, s71, 0x2000
	s_nop 0
	global_load_lds_dwordx4 v134, s[72:73]
	v_cndmask_b32_e32 v132, v128, v141, vcc
	v_lshlrev_b32_e32 v133, 10, v132
	v_and_or_b32 v133, v133, s37, v135
	s_mov_b64 s[72:73], s[26:27]
	s_mov_b32 m0, s36
	s_nop 0
	global_load_lds_dwordx4 v133, s[72:73]
	v_cndmask_b32_e32 v143, v129, v142, vcc
	v_lshlrev_b32_e32 v208, 10, v143
	v_and_or_b32 v208, v208, s37, v135
	s_mov_b64 s[72:73], s[26:27]
	s_mov_b32 m0, s38
	s_nop 0
	global_load_lds_dwordx4 v208, s[72:73]
	s_waitcnt vmcnt(8)
	s_waitcnt lgkmcnt(0)
	s_barrier
	s_setprio 3
	v_mfma_f32_16x16x128_f8f6f4 v[60:63], v[144:151], v[176:183], v[60:63]
	v_mfma_f32_16x16x128_f8f6f4 v[52:55], v[152:159], v[176:183], v[52:55]
	v_mfma_f32_16x16x128_f8f6f4 v[44:47], v[144:151], v[184:191], v[44:47]
	v_mfma_f32_16x16x128_f8f6f4 v[36:39], v[152:159], v[184:191], v[36:39]
	v_mfma_f32_16x16x128_f8f6f4 v[28:31], v[144:151], v[192:199], v[28:31]
	v_mfma_f32_16x16x128_f8f6f4 v[20:23], v[152:159], v[192:199], v[20:23]
	v_mfma_f32_16x16x128_f8f6f4 v[12:15], v[144:151], v[200:207], v[12:15]
	v_mfma_f32_16x16x128_f8f6f4 v[4:7], v[152:159], v[200:207], v[4:7]
	v_mfma_f32_16x16x128_f8f6f4 v[56:59], v[160:167], v[176:183], v[56:59]
	v_mfma_f32_16x16x128_f8f6f4 v[48:51], v[168:175], v[176:183], v[48:51]
	v_mfma_f32_16x16x128_f8f6f4 v[40:43], v[160:167], v[184:191], v[40:43]
	v_mfma_f32_16x16x128_f8f6f4 v[32:35], v[168:175], v[184:191], v[32:35]
	v_mfma_f32_16x16x128_f8f6f4 v[24:27], v[160:167], v[192:199], v[24:27]
	v_mfma_f32_16x16x128_f8f6f4 v[16:19], v[168:175], v[192:199], v[16:19]
	v_mfma_f32_16x16x128_f8f6f4 v[8:11], v[160:167], v[200:207], v[8:11]
	v_mfma_f32_16x16x128_f8f6f4 v[0:3], v[168:175], v[200:207], v[0:3]
	s_setprio 0
	s_barrier
	s_add_i32 s71, 0, 0x18000
	s_add_i32 s74, 0, 0x1c000
	v_add_u32_e32 v156, s71, v136
	v_add_u32_e32 v172, s74, v136
	ds_read_b128 v[144:147], v156
	ds_read_b128 v[148:151], v156 offset:1024
	ds_read_b128 v[152:155], v156 offset:2048
	ds_read_b128 v[156:159], v156 offset:3072
	ds_read_b128 v[160:163], v172
	ds_read_b128 v[164:167], v172 offset:1024
	ds_read_b128 v[168:171], v172 offset:2048
	ds_read_b128 v[172:175], v172 offset:3072
	v_bfe_u32 v132, v132, 16, 16
	v_lshl_or_b32 v132, v132, 10, v135
	s_mov_b32 m0, s39
	ds_read_b128 v[176:179], v139 offset:32768
	ds_read_b128 v[180:183], v139 offset:33792
	ds_read_b128 v[184:187], v139 offset:34816
	ds_read_b128 v[188:191], v139 offset:35840
	ds_read_b128 v[192:195], v139 offset:36864
	ds_read_b128 v[196:199], v139 offset:37888
	ds_read_b128 v[200:203], v139 offset:38912
	ds_read_b128 v[204:207], v139 offset:39936
	s_mov_b64 s[72:73], s[26:27]
	s_nop 0
	global_load_lds_dwordx4 v132, s[72:73]
	v_bfe_u32 v132, v143, 16, 16
	v_lshl_or_b32 v132, v132, 10, v135
	s_mov_b32 m0, s40
	s_nop 0
	global_load_lds_dwordx4 v132, s[26:27]
	s_waitcnt vmcnt(8)
	s_waitcnt lgkmcnt(0)
	s_barrier
	s_setprio 3
	v_mfma_f32_16x16x128_f8f6f4 v[124:127], v[144:151], v[176:183], v[124:127]
	v_mfma_f32_16x16x128_f8f6f4 v[116:119], v[152:159], v[176:183], v[116:119]
	v_mfma_f32_16x16x128_f8f6f4 v[108:111], v[144:151], v[184:191], v[108:111]
	v_mfma_f32_16x16x128_f8f6f4 v[100:103], v[152:159], v[184:191], v[100:103]
	v_mfma_f32_16x16x128_f8f6f4 v[92:95], v[144:151], v[192:199], v[92:95]
	v_mfma_f32_16x16x128_f8f6f4 v[84:87], v[152:159], v[192:199], v[84:87]
	v_mfma_f32_16x16x128_f8f6f4 v[76:79], v[144:151], v[200:207], v[76:79]
	v_mfma_f32_16x16x128_f8f6f4 v[68:71], v[152:159], v[200:207], v[68:71]
	v_mfma_f32_16x16x128_f8f6f4 v[120:123], v[160:167], v[176:183], v[120:123]
	v_mfma_f32_16x16x128_f8f6f4 v[112:115], v[168:175], v[176:183], v[112:115]
	v_mfma_f32_16x16x128_f8f6f4 v[104:107], v[160:167], v[184:191], v[104:107]
	v_mfma_f32_16x16x128_f8f6f4 v[96:99], v[168:175], v[184:191], v[96:99]
	v_mfma_f32_16x16x128_f8f6f4 v[88:91], v[160:167], v[192:199], v[88:91]
	v_mfma_f32_16x16x128_f8f6f4 v[80:83], v[168:175], v[192:199], v[80:83]
	v_mfma_f32_16x16x128_f8f6f4 v[72:75], v[160:167], v[200:207], v[72:75]
	v_mfma_f32_16x16x128_f8f6f4 v[64:67], v[168:175], v[200:207], v[64:67]
	s_setprio 0
	s_barrier
	s_add_u32 s26, s24, 0x80
	s_addc_u32 s27, s25, 0
	v_mov_b32_e32 v132, v134
	s_add_i32 s71, s71, s35
	ds_read_b128 v[176:179], v139 offset:49152
	ds_read_b128 v[180:183], v139 offset:50176
	ds_read_b128 v[184:187], v139 offset:51200
	ds_read_b128 v[188:191], v139 offset:52224
	ds_read_b128 v[192:195], v139 offset:53248
	ds_read_b128 v[196:199], v139 offset:54272
	ds_read_b128 v[200:203], v139 offset:55296
	ds_read_b128 v[204:207], v139 offset:56320
	s_mov_b32 m0, s71
	s_nop 0
	global_load_lds_dwordx4 v132, s[26:27]
	s_add_u32 s26, s24, 0x10080
	s_addc_u32 s27, s25, 0
	s_add_i32 m0, s71, 0x2000
	s_nop 0
	global_load_lds_dwordx4 v134, s[26:27]
	s_add_u32 s26, s24, 0x20080
	s_addc_u32 s27, s25, 0
	s_add_i32 s71, s74, s35
	s_mov_b32 m0, s71
	s_add_u32 s24, s24, 0x30080
	s_addc_u32 s25, s25, 0
	global_load_lds_dwordx4 v134, s[26:27]
	s_add_i32 m0, s71, 0x2000
	s_nop 0
	global_load_lds_dwordx4 v134, s[24:25]
	s_mov_b64 s[24:25], s[22:23]
	s_mov_b32 m0, s43
	s_nop 0
	global_load_lds_dwordx4 v133, s[24:25]
	s_mov_b32 m0, s44
	s_nop 0
	global_load_lds_dwordx4 v208, s[22:23]
	s_waitcnt vmcnt(8)
	s_waitcnt lgkmcnt(0)
	s_barrier
	s_setprio 3
	v_mfma_f32_16x16x128_f8f6f4 v[60:63], v[144:151], v[176:183], v[60:63]
	v_mfma_f32_16x16x128_f8f6f4 v[52:55], v[152:159], v[176:183], v[52:55]
	v_mfma_f32_16x16x128_f8f6f4 v[44:47], v[144:151], v[184:191], v[44:47]
	v_mfma_f32_16x16x128_f8f6f4 v[36:39], v[152:159], v[184:191], v[36:39]
	v_mfma_f32_16x16x128_f8f6f4 v[28:31], v[144:151], v[192:199], v[28:31]
	v_mfma_f32_16x16x128_f8f6f4 v[20:23], v[152:159], v[192:199], v[20:23]
	v_mfma_f32_16x16x128_f8f6f4 v[12:15], v[144:151], v[200:207], v[12:15]
	v_mfma_f32_16x16x128_f8f6f4 v[4:7], v[152:159], v[200:207], v[4:7]
	v_mfma_f32_16x16x128_f8f6f4 v[56:59], v[160:167], v[176:183], v[56:59]
	v_mfma_f32_16x16x128_f8f6f4 v[48:51], v[168:175], v[176:183], v[48:51]
	v_mfma_f32_16x16x128_f8f6f4 v[40:43], v[160:167], v[184:191], v[40:43]
	v_mfma_f32_16x16x128_f8f6f4 v[32:35], v[168:175], v[184:191], v[32:35]
	v_mfma_f32_16x16x128_f8f6f4 v[24:27], v[160:167], v[192:199], v[24:27]
	v_mfma_f32_16x16x128_f8f6f4 v[16:19], v[168:175], v[192:199], v[16:19]
	v_mfma_f32_16x16x128_f8f6f4 v[8:11], v[160:167], v[200:207], v[8:11]
	v_mfma_f32_16x16x128_f8f6f4 v[0:3], v[168:175], v[200:207], v[0:3]
	s_setprio 0
	s_barrier
	s_add_i32 s70, s70, 2
	s_add_u32 s14, s14, 0x100
	s_addc_u32 s65, s65, 0
	s_add_u32 s68, s68, 0x100
	s_addc_u32 s69, s69, 0
	s_cmp_gt_u32 s70, 5
	s_cbranch_scc0 .LBB0_1124
	s_and_b64 vcc, exec, s[18:19]
	s_cbranch_vccz .LBB0_1127
	s_barrier

.LBB0_1283:
	s_or_b64 exec, exec, s[0:1]
	v_bfe_i32 v4, v6, 27, 1
	v_lshlrev_b32_e32 v2, 4, v6
	v_lshrrev_b32_e32 v4, 22, v4
	v_add_u32_e32 v4, v2, v4
	v_and_b32_e32 v4, 0xfffffc00, v4
	v_sub_u32_e32 v2, v2, v4
	v_ashrrev_i32_e32 v3, 31, v6
	v_lshrrev_b32_e32 v4, 4, v2
	v_lshrrev_b32_e32 v3, 26, v3
	v_bitop3_b32 v4, v4, v2, 32 bitop3:0x6c
	v_ashrrev_i32_e32 v2, 31, v2
	v_add_u32_e32 v3, v6, v3
	v_lshrrev_b32_e32 v2, 26, v2
	v_ashrrev_i32_e32 v3, 6, v3
	v_add_u32_e32 v2, v4, v2
	v_lshlrev_b32_e32 v5, 3, v3
	v_ashrrev_i32_e32 v2, 6, v2
	v_and_b32_e32 v5, -16, v5
	v_mul_i32_i24_e32 v9, 64, v2
	v_add_u32_e32 v5, v2, v5
	v_sub_u32_e32 v4, v4, v9
	v_mov_b32_e32 v9, 1
	v_lshlrev_b32_e32 v3, 5, v3
	v_ashrrev_i16_sdwa v4, v9, sext(v4) dst_sel:DWORD dst_unused:UNUSED_PAD src0_sel:DWORD src1_sel:BYTE_0
	v_lshlrev_b32_e32 v9, 1, v5
	v_lshrrev_b32_e32 v10, 2, v5
	v_and_b32_e32 v2, 3, v2
	s_mov_b32 s0, 0x3fffe0
	s_and_b32 s19, s15, 1
	v_lshlrev_b64 v[0:1], 19, v[0:1]
	v_and_b32_e32 v3, 32, v3
	v_bfe_i32 v4, v4, 0, 16
	v_and_b32_e32 v9, 24, v9
	v_and_b32_e32 v10, 4, v10
	v_and_or_b32 v2, v5, s0, v2
	v_lshl_add_u64 v[0:1], s[4:5], 0, v[0:1]
	s_lshl_b32 s0, s19, 18
	s_mov_b32 s1, 0
	s_ashr_i32 s16, s22, 6
	v_or3_b32 v2, v2, v10, v9
	v_add_lshl_u32 v3, v3, v4, 1
	v_lshl_add_u64 v[0:1], v[0:1], 0, s[0:1]
	v_lshl_add_u32 v64, v2, 10, v3
	s_lshl_b32 s14, s16, 10
	v_readfirstlane_b32 s1, v1
	v_readfirstlane_b32 s0, v0
	s_add_i32 s23, s14, 0
	s_mov_b64 s[4:5], s[0:1]
	s_ashr_i32 s17, s22, 8
	s_add_i32 m0, s23, 0x10000
	s_nop 0
	global_load_lds_dwordx4 v64, s[4:5]
	s_add_u32 s4, s0, 0x10000
	s_addc_u32 s5, s1, 0
	s_add_i32 m0, s23, 0x12000
	s_nop 0
	global_load_lds_dwordx4 v64, s[4:5]
	s_add_i32 m0, s23, 0x14000
	s_add_u32 s4, s0, 0x20000
	s_addc_u32 s5, s1, 0
	s_nop 0
	global_load_lds_dwordx4 v64, s[4:5]
	s_add_u32 s4, s0, 0x30000
	s_addc_u32 s5, s1, 0
	s_add_i32 m0, s23, 0x16000
	s_add_i32 s25, s23, 0x2000
	global_load_lds_dwordx4 v64, s[4:5]
	v_and_b32_e32 v0, 0x7e, v3
	v_or_b32_e32 v65, v8, v0
	s_mov_b64 s[4:5], s[8:9]
	s_mov_b32 m0, s23
	v_or_b32_e32 v66, v7, v0
	global_load_lds_dwordx4 v65, s[4:5]
	s_mov_b64 s[4:5], s[8:9]
	s_mov_b32 m0, s25
	s_cmp_lg_u32 s17, 1
	global_load_lds_dwordx4 v66, s[4:5]
	s_cbranch_scc1 .LBB0_1285
	s_barrier
.LBB0_1285:
	v_and_b32_e32 v0, 48, v6
	v_lshlrev_b32_e32 v1, 6, v6
	s_movk_i32 s5, 0x3c0
	v_and_or_b32 v0, v1, s5, v0
	v_lshlrev_b32_e32 v1, 2, v6
	s_lshl_b32 s4, s17, 13
	v_and_b32_e32 v1, 32, v1
	v_bitop3_b32 v2, v0, s4, v1 bitop3:0xde
	s_lshl_b32 s4, s16, 5
	s_and_b32 s21, s4, 0x60
	s_lshl_b32 s24, s17, 6
	s_lshl_b32 s4, s21, 7
	v_bitop3_b32 v1, s4, v0, v1 bitop3:0xf6
	s_add_u32 s4, s0, 0x80
	s_addc_u32 s5, s1, 0
	s_waitcnt vmcnt(0)
	s_barrier
	s_add_i32 m0, s23, 0x18000
	s_mov_b32 s37, -2
	global_load_lds_dwordx4 v64, s[4:5]
	s_add_u32 s4, s0, 0x10080
	s_addc_u32 s5, s1, 0
	s_add_i32 m0, s23, 0x1a000
	v_add_u32_e32 v69, 0, v2
	global_load_lds_dwordx4 v64, s[4:5]
	s_add_u32 s4, s8, 0x80
	s_addc_u32 s5, s9, 0
	s_add_i32 s26, s23, 0x8000
	s_mov_b64 s[16:17], s[4:5]
	s_mov_b32 m0, s26
	s_add_i32 s27, s23, 0xa000
	s_nop 0
	global_load_lds_dwordx4 v65, s[16:17]
	s_mov_b32 m0, s27
	s_nop 0
	global_load_lds_dwordx4 v66, s[4:5]
	s_add_i32 m0, s23, 0x1c000
	s_add_u32 s4, s0, 0x20080
	s_addc_u32 s5, s1, 0
	s_nop 0
	global_load_lds_dwordx4 v64, s[4:5]
	s_add_u32 s4, s0, 0x30080
	s_addc_u32 s5, s1, 0
	s_add_i32 m0, s23, 0x1e000
	s_add_u32 s31, s0, 0x100
	global_load_lds_dwordx4 v64, s[4:5]
	s_addc_u32 s34, s1, 0
	s_add_u32 s35, s8, 0x100
	s_waitcnt vmcnt(6)
	s_addc_u32 s36, s9, 0
	s_add_i32 s38, 0, 0x10000
	s_add_i32 s40, 0, 0x14000
	s_add_i32 s42, 0, 0x18000
	s_add_i32 s44, 0, 0x1c000
	v_mov_b32_e32 v0, 0
	v_add_u32_e32 v67, s38, v1
	v_add_u32_e32 v68, s40, v1
	s_add_i32 s38, s38, s14
	s_add_i32 s40, s40, s14
	v_add_u32_e32 v70, s42, v1
	v_add_u32_e32 v71, s44, v1
	s_add_i32 s42, s42, s14
	s_add_i32 s44, s44, s14
	s_add_i32 s39, s38, 0x2000
	s_add_i32 s41, s40, 0x2000
	s_add_i32 s43, s42, 0x2000
	s_add_i32 s45, s44, 0x2000
	v_mov_b32_e32 v1, v0
	v_mov_b32_e32 v2, v0
	v_mov_b32_e32 v3, v0
	v_mov_b32_e32 v8, v0
	v_mov_b32_e32 v9, v0
	v_mov_b32_e32 v10, v0
	v_mov_b32_e32 v11, v0
	v_mov_b32_e32 v16, v0
	v_mov_b32_e32 v17, v0
	v_mov_b32_e32 v18, v0
	v_mov_b32_e32 v19, v0
	v_mov_b32_e32 v24, v0
	v_mov_b32_e32 v25, v0
	v_mov_b32_e32 v26, v0
	v_mov_b32_e32 v27, v0
	s_waitcnt vmcnt(0)
	v_mov_b32_e32 v32, v0
	v_mov_b32_e32 v33, v0
	v_mov_b32_e32 v34, v0
	v_mov_b32_e32 v35, v0
	v_mov_b32_e32 v40, v0
	v_mov_b32_e32 v41, v0
	v_mov_b32_e32 v42, v0
	v_mov_b32_e32 v43, v0
	v_mov_b32_e32 v48, v0
	v_mov_b32_e32 v49, v0
	v_mov_b32_e32 v50, v0
	v_mov_b32_e32 v51, v0
	v_mov_b32_e32 v56, v0
	v_mov_b32_e32 v57, v0
	v_mov_b32_e32 v58, v0
	v_mov_b32_e32 v59, v0
	v_mov_b32_e32 v4, v0
	v_mov_b32_e32 v5, v0
	v_mov_b32_e32 v6, v0
	v_mov_b32_e32 v7, v0
	v_mov_b32_e32 v12, v0
	v_mov_b32_e32 v13, v0
	v_mov_b32_e32 v14, v0
	v_mov_b32_e32 v15, v0
	v_mov_b32_e32 v20, v0
	v_mov_b32_e32 v21, v0
	v_mov_b32_e32 v22, v0
	v_mov_b32_e32 v23, v0
	v_mov_b32_e32 v28, v0
	v_mov_b32_e32 v29, v0
	v_mov_b32_e32 v30, v0
	v_mov_b32_e32 v31, v0
	v_mov_b32_e32 v36, v0
	v_mov_b32_e32 v37, v0
	v_mov_b32_e32 v38, v0
	v_mov_b32_e32 v39, v0
	v_mov_b32_e32 v44, v0
	v_mov_b32_e32 v45, v0
	v_mov_b32_e32 v46, v0
	v_mov_b32_e32 v47, v0
	v_mov_b32_e32 v52, v0
	v_mov_b32_e32 v53, v0
	v_mov_b32_e32 v54, v0
	v_mov_b32_e32 v55, v0
	v_mov_b32_e32 v60, v0
	v_mov_b32_e32 v61, v0
	v_mov_b32_e32 v62, v0
	v_mov_b32_e32 v63, v0
	s_barrier
.LBB0_1286:
	ds_read_b128 v[72:75], v67
	ds_read_b128 v[76:79], v67 offset:1024
	ds_read_b128 v[80:83], v67 offset:2048
	ds_read_b128 v[84:87], v67 offset:3072
	ds_read_b128 v[88:91], v68
	ds_read_b128 v[92:95], v68 offset:1024
	ds_read_b128 v[96:99], v68 offset:2048
	ds_read_b128 v[100:103], v68 offset:3072
	s_cmp_eq_u32 s37, 4
	s_cselect_b32 s16, s8, s35
	s_cselect_b32 s17, s9, s36
	s_cselect_b32 s14, s0, s31
	s_cselect_b32 s15, s1, s34
	s_add_u32 s4, s16, 0x80
	s_addc_u32 s5, s17, 0
	ds_read_b128 v[104:107], v69
	ds_read_b128 v[108:111], v69 offset:1024
	ds_read_b128 v[112:115], v69 offset:2048
	ds_read_b128 v[116:119], v69 offset:3072
	ds_read_b128 v[120:123], v69 offset:4096
	ds_read_b128 v[124:127], v69 offset:5120
	ds_read_b128 v[128:131], v69 offset:6144
	ds_read_b128 v[132:135], v69 offset:7168
	s_waitcnt vmcnt(6)
	s_waitcnt lgkmcnt(0)
	s_barrier
	s_setprio 3
	v_mfma_f32_16x16x128_f8f6f4 v[60:63], v[72:79], v[104:111], v[60:63]
	v_mfma_f32_16x16x128_f8f6f4 v[52:55], v[80:87], v[104:111], v[52:55]
	v_mfma_f32_16x16x128_f8f6f4 v[44:47], v[72:79], v[112:119], v[44:47]
	v_mfma_f32_16x16x128_f8f6f4 v[36:39], v[80:87], v[112:119], v[36:39]
	v_mfma_f32_16x16x128_f8f6f4 v[28:31], v[72:79], v[120:127], v[28:31]
	v_mfma_f32_16x16x128_f8f6f4 v[20:23], v[80:87], v[120:127], v[20:23]
	v_mfma_f32_16x16x128_f8f6f4 v[12:15], v[72:79], v[128:135], v[12:15]
	v_mfma_f32_16x16x128_f8f6f4 v[136:139], v[80:87], v[128:135], v[4:7]
	v_mfma_f32_16x16x128_f8f6f4 v[56:59], v[88:95], v[104:111], v[56:59]
	v_mfma_f32_16x16x128_f8f6f4 v[48:51], v[96:103], v[104:111], v[48:51]
	v_mfma_f32_16x16x128_f8f6f4 v[40:43], v[88:95], v[112:119], v[40:43]
	v_mfma_f32_16x16x128_f8f6f4 v[32:35], v[96:103], v[112:119], v[32:35]
	v_mfma_f32_16x16x128_f8f6f4 v[24:27], v[88:95], v[120:127], v[24:27]
	v_mfma_f32_16x16x128_f8f6f4 v[16:19], v[96:103], v[120:127], v[16:19]
	v_mfma_f32_16x16x128_f8f6f4 v[8:11], v[88:95], v[128:135], v[8:11]
	v_mfma_f32_16x16x128_f8f6f4 v[128:131], v[96:103], v[128:135], v[0:3]
	s_setprio 0
	s_barrier
	s_nop 4
	s_mov_b64 s[48:49], s[14:15]
	s_mov_b32 m0, s38
	s_nop 0
	global_load_lds_dwordx4 v64, s[48:49]
	s_add_u32 s48, s14, 0x10000
	s_addc_u32 s49, s15, 0
	s_mov_b32 m0, s39
	s_nop 0
	global_load_lds_dwordx4 v64, s[48:49]
	s_add_u32 s48, s14, 0x20000
	s_addc_u32 s49, s15, 0
	s_mov_b32 m0, s40
	s_nop 0
	global_load_lds_dwordx4 v64, s[48:49]
	s_add_u32 s48, s14, 0x30000
	s_addc_u32 s49, s15, 0
	s_mov_b32 m0, s41
	s_nop 0
	global_load_lds_dwordx4 v64, s[48:49]
	s_mov_b64 s[48:49], s[16:17]
	s_mov_b32 m0, s23
	s_nop 0
	global_load_lds_dwordx4 v65, s[48:49]
	s_mov_b32 m0, s25
	s_nop 0
	global_load_lds_dwordx4 v66, s[16:17]
	s_waitcnt vmcnt(6)
	s_waitcnt lgkmcnt(0)
	s_barrier
	s_barrier
	ds_read_b128 v[0:3], v70
	ds_read_b128 v[4:7], v70 offset:1024
	ds_read_b128 v[72:75], v70 offset:2048
	ds_read_b128 v[76:79], v70 offset:3072
	ds_read_b128 v[80:83], v71
	ds_read_b128 v[84:87], v71 offset:1024
	ds_read_b128 v[88:91], v71 offset:2048
	ds_read_b128 v[92:95], v71 offset:3072
	ds_read_b128 v[96:99], v69 offset:32768
	ds_read_b128 v[100:103], v69 offset:33792
	ds_read_b128 v[104:107], v69 offset:34816
	ds_read_b128 v[108:111], v69 offset:35840
	ds_read_b128 v[112:115], v69 offset:36864
	ds_read_b128 v[116:119], v69 offset:37888
	ds_read_b128 v[120:123], v69 offset:38912
	ds_read_b128 v[124:127], v69 offset:39936
	s_waitcnt vmcnt(6)
	s_waitcnt lgkmcnt(0)
	s_barrier
	s_setprio 3
	v_mfma_f32_16x16x128_f8f6f4 v[60:63], v[0:7], v[96:103], v[60:63]
	v_mfma_f32_16x16x128_f8f6f4 v[52:55], v[72:79], v[96:103], v[52:55]
	v_mfma_f32_16x16x128_f8f6f4 v[44:47], v[0:7], v[104:111], v[44:47]
	v_mfma_f32_16x16x128_f8f6f4 v[36:39], v[72:79], v[104:111], v[36:39]
	v_mfma_f32_16x16x128_f8f6f4 v[28:31], v[0:7], v[112:119], v[28:31]
	v_mfma_f32_16x16x128_f8f6f4 v[20:23], v[72:79], v[112:119], v[20:23]
	v_mfma_f32_16x16x128_f8f6f4 v[12:15], v[0:7], v[120:127], v[12:15]
	v_mfma_f32_16x16x128_f8f6f4 v[4:7], v[72:79], v[120:127], v[136:139]
	v_mfma_f32_16x16x128_f8f6f4 v[56:59], v[80:87], v[96:103], v[56:59]
	s_add_u32 s16, s14, 0x80
	s_addc_u32 s17, s15, 0
	v_mfma_f32_16x16x128_f8f6f4 v[48:51], v[88:95], v[96:103], v[48:51]
	v_mfma_f32_16x16x128_f8f6f4 v[40:43], v[80:87], v[104:111], v[40:43]
	v_mfma_f32_16x16x128_f8f6f4 v[32:35], v[88:95], v[104:111], v[32:35]
	v_mfma_f32_16x16x128_f8f6f4 v[24:27], v[80:87], v[112:119], v[24:27]
	v_mfma_f32_16x16x128_f8f6f4 v[16:19], v[88:95], v[112:119], v[16:19]
	v_mfma_f32_16x16x128_f8f6f4 v[8:11], v[80:87], v[120:127], v[8:11]
	v_mfma_f32_16x16x128_f8f6f4 v[0:3], v[88:95], v[120:127], v[128:131]
	s_setprio 0
	s_barrier
	s_mov_b32 m0, s42
	s_nop 0
	global_load_lds_dwordx4 v64, s[16:17]
	s_add_u32 s16, s14, 0x10080
	s_addc_u32 s17, s15, 0
	s_mov_b32 m0, s43
	s_nop 0
	global_load_lds_dwordx4 v64, s[16:17]
	s_add_u32 s16, s14, 0x20080
	s_addc_u32 s17, s15, 0
	s_mov_b32 m0, s44
	s_add_u32 s14, s14, 0x30080
	global_load_lds_dwordx4 v64, s[16:17]
	s_addc_u32 s15, s15, 0
	s_mov_b32 m0, s45
	s_nop 0
	global_load_lds_dwordx4 v64, s[14:15]
	s_mov_b64 s[14:15], s[4:5]
	s_mov_b32 m0, s26
	s_nop 0
	global_load_lds_dwordx4 v65, s[14:15]
	s_mov_b32 m0, s27
	s_nop 0
	global_load_lds_dwordx4 v66, s[4:5]
	s_waitcnt vmcnt(6)
	s_waitcnt lgkmcnt(0)
	s_barrier
	s_barrier
	s_add_i32 s37, s37, 2
	s_add_u32 s31, s31, 0x100
	s_addc_u32 s34, s34, 0
	s_add_u32 s35, s35, 0x100
	s_addc_u32 s36, s36, 0
	s_cmp_gt_u32 s37, 5
	s_cbranch_scc0 .LBB0_1286
	s_cmpk_lt_u32 s22, 0x100
	s_cbranch_scc0 .LBB0_1289
	s_barrier
.LBB0_1289:
	s_lshl_b32 s0, s18, 2
	s_add_i32 s0, s3, s0
	v_mbcnt_lo_u32_b32 v72, -1, 0
	v_mbcnt_hi_u32_b32 v72, -1, v72
	v_mov_b32_e32 v64, s0
	ds_read2_b32 v[64:65], v64 offset0:64 offset1:224
	s_lshl_b32 s0, s20, 7
	v_and_b32_e32 v70, 15, v72
	s_add_i32 s0, s0, s24
	v_or_b32_e32 v71, s0, v70
	s_waitcnt lgkmcnt(0)
	v_ashrrev_i32_e32 v67, 31, v64
	v_mov_b32_e32 v66, v64
	v_lshlrev_b32_e32 v64, 2, v64
	v_add_u32_e32 v64, s3, v64
	ds_read_b32 v64, v64 offset:4
	v_lshlrev_b64 v[68:69], 16, v[66:67]
	v_add_u32_e32 v66, v65, v71
	v_mov_b32_e32 v73, 0
	v_lshl_add_u64 v[68:69], s[10:11], 0, v[68:69]
	s_waitcnt lgkmcnt(0)
	v_cmp_lt_i32_e32 vcc, v66, v64
	v_ashrrev_i32_e32 v67, 31, v66
	v_mov_b32_e32 v74, 0
	v_bfe_u32 v140, v72, 4, 2
	s_lshl_b32 s0, s19, 7
	v_lshl_add_u64 v[144:145], v[66:67], 2, v[68:69]
	v_lshl_or_b32 v141, v140, 3, s0
	global_load_dword v146, v[144:145], off
	global_load_dword v147, v[144:145], off offset:64
	global_load_dword v148, v[144:145], off offset:128
	global_load_dword v149, v[144:145], off offset:192
	s_lshl_b32 s4, s18, 8
	v_or_b32_e32 v141, s21, v141
	v_add_u32_e32 v142, s4, v71
	v_lshl_add_u32 v142, v142, 8, v141
	v_cmp_lt_i32_e32 vcc, v66, v64
	s_waitcnt vmcnt(3)
	v_mul_f32_e32 v155, 0x3c800000, v146
	v_mul_f32_e32 v156, 0xbd38aa3b, v60
	v_mul_f32_e32 v157, 0xbd38aa3b, v61
	v_mul_f32_e32 v158, 0xbd38aa3b, v62
	v_mul_f32_e32 v159, 0xbd38aa3b, v63
	v_mul_f32_e32 v160, 0xbd38aa3b, v52
	v_mul_f32_e32 v161, 0xbd38aa3b, v53
	v_mul_f32_e32 v162, 0xbd38aa3b, v54
	v_mul_f32_e32 v163, 0xbd38aa3b, v55
	v_exp_f32_e32 v156, v156
	v_exp_f32_e32 v157, v157
	v_exp_f32_e32 v158, v158
	v_exp_f32_e32 v159, v159
	v_exp_f32_e32 v160, v160
	v_exp_f32_e32 v161, v161
	v_exp_f32_e32 v162, v162
	v_exp_f32_e32 v163, v163
	v_add_f32_e32 v156, 1.0, v156
	v_add_f32_e32 v157, 1.0, v157
	v_add_f32_e32 v158, 1.0, v158
	v_add_f32_e32 v159, 1.0, v159
	v_add_f32_e32 v160, 1.0, v160
	v_add_f32_e32 v161, 1.0, v161
	v_add_f32_e32 v162, 1.0, v162
	v_add_f32_e32 v163, 1.0, v163
	v_rcp_f32_e32 v156, v156
	v_rcp_f32_e32 v157, v157
	v_rcp_f32_e32 v158, v158
	v_rcp_f32_e32 v159, v159
	v_rcp_f32_e32 v160, v160
	v_rcp_f32_e32 v161, v161
	v_rcp_f32_e32 v162, v162
	v_rcp_f32_e32 v163, v163
	v_mul_f32_e32 v156, v60, v156
	v_mul_f32_e32 v157, v61, v157
	v_mul_f32_e32 v158, v62, v158
	v_mul_f32_e32 v159, v63, v159
	v_mul_f32_e32 v160, v52, v160
	v_mul_f32_e32 v161, v53, v161
	v_mul_f32_e32 v162, v54, v162
	v_mul_f32_e32 v163, v55, v163
	v_mul_f32_e32 v156, v156, v56
	v_mul_f32_e32 v157, v157, v57
	v_mul_f32_e32 v158, v158, v58
	v_mul_f32_e32 v159, v159, v59
	v_mul_f32_e32 v160, v160, v48
	v_mul_f32_e32 v161, v161, v49
	v_mul_f32_e32 v162, v162, v50
	v_mul_f32_e32 v163, v163, v51
	v_mul_f32_e32 v156, v156, v155
	v_mul_f32_e32 v157, v157, v155
	v_mul_f32_e32 v158, v158, v155
	v_mul_f32_e32 v159, v159, v155
	v_mul_f32_e32 v160, v160, v155
	v_mul_f32_e32 v161, v161, v155
	v_mul_f32_e32 v162, v162, v155
	v_mul_f32_e32 v163, v163, v155
	v_max_f32_e32 v156, 0xc3e00000, v156
	v_max_f32_e32 v157, 0xc3e00000, v157
	v_max_f32_e32 v158, 0xc3e00000, v158
	v_max_f32_e32 v159, 0xc3e00000, v159
	v_max_f32_e32 v160, 0xc3e00000, v160
	v_max_f32_e32 v161, 0xc3e00000, v161
	v_max_f32_e32 v162, 0xc3e00000, v162
	v_max_f32_e32 v163, 0xc3e00000, v163
	v_min_f32_e32 v156, 0x43e00000, v156
	v_min_f32_e32 v157, 0x43e00000, v157
	v_min_f32_e32 v158, 0x43e00000, v158
	v_min_f32_e32 v159, 0x43e00000, v159
	v_min_f32_e32 v160, 0x43e00000, v160
	v_min_f32_e32 v161, 0x43e00000, v161
	v_min_f32_e32 v162, 0x43e00000, v162
	v_min_f32_e32 v163, 0x43e00000, v163
	v_cndmask_b32_e32 v156, 0, v156, vcc
	v_cndmask_b32_e32 v157, 0, v157, vcc
	v_cndmask_b32_e32 v158, 0, v158, vcc
	v_cndmask_b32_e32 v159, 0, v159, vcc
	v_cndmask_b32_e32 v160, 0, v160, vcc
	v_cndmask_b32_e32 v161, 0, v161, vcc
	v_cndmask_b32_e32 v162, 0, v162, vcc
	v_cndmask_b32_e32 v163, 0, v163, vcc
	v_mov_b32_e32 v180, 0
	v_mov_b32_e32 v181, 0
	v_cvt_pk_fp8_f32 v180, v156, v157
	v_cvt_pk_fp8_f32 v181, v160, v161
	v_mov_b32_e32 v184, v142
	v_cvt_pk_fp8_f32 v180, v158, v159 op_sel:[0,0,1]
	v_cvt_pk_fp8_f32 v181, v162, v163 op_sel:[0,0,1]
	s_nop 1
	global_store_dwordx2 v184, v[180:181], s[12:13] sc1
	v_add_u32_e32 v154, 0x10, v66
	v_cmp_lt_i32_e32 vcc, v154, v64
	s_waitcnt vmcnt(3)
	v_mul_f32_e32 v155, 0x3c800000, v147
	v_mul_f32_e32 v156, 0xbd38aa3b, v44
	v_mul_f32_e32 v157, 0xbd38aa3b, v45
	v_mul_f32_e32 v158, 0xbd38aa3b, v46
	v_mul_f32_e32 v159, 0xbd38aa3b, v47
	v_mul_f32_e32 v160, 0xbd38aa3b, v36
	v_mul_f32_e32 v161, 0xbd38aa3b, v37
	v_mul_f32_e32 v162, 0xbd38aa3b, v38
	v_mul_f32_e32 v163, 0xbd38aa3b, v39
	v_exp_f32_e32 v156, v156
	v_exp_f32_e32 v157, v157
	v_exp_f32_e32 v158, v158
	v_exp_f32_e32 v159, v159
	v_exp_f32_e32 v160, v160
	v_exp_f32_e32 v161, v161
	v_exp_f32_e32 v162, v162
	v_exp_f32_e32 v163, v163
	v_add_f32_e32 v156, 1.0, v156
	v_add_f32_e32 v157, 1.0, v157
	v_add_f32_e32 v158, 1.0, v158
	v_add_f32_e32 v159, 1.0, v159
	v_add_f32_e32 v160, 1.0, v160
	v_add_f32_e32 v161, 1.0, v161
	v_add_f32_e32 v162, 1.0, v162
	v_add_f32_e32 v163, 1.0, v163
	v_rcp_f32_e32 v156, v156
	v_rcp_f32_e32 v157, v157
	v_rcp_f32_e32 v158, v158
	v_rcp_f32_e32 v159, v159
	v_rcp_f32_e32 v160, v160
	v_rcp_f32_e32 v161, v161
	v_rcp_f32_e32 v162, v162
	v_rcp_f32_e32 v163, v163
	v_mul_f32_e32 v156, v44, v156
	v_mul_f32_e32 v157, v45, v157
	v_mul_f32_e32 v158, v46, v158
	v_mul_f32_e32 v159, v47, v159
	v_mul_f32_e32 v160, v36, v160
	v_mul_f32_e32 v161, v37, v161
	v_mul_f32_e32 v162, v38, v162
	v_mul_f32_e32 v163, v39, v163
	v_mul_f32_e32 v156, v156, v40
	v_mul_f32_e32 v157, v157, v41
	v_mul_f32_e32 v158, v158, v42
	v_mul_f32_e32 v159, v159, v43
	v_mul_f32_e32 v160, v160, v32
	v_mul_f32_e32 v161, v161, v33
	v_mul_f32_e32 v162, v162, v34
	v_mul_f32_e32 v163, v163, v35
	v_mul_f32_e32 v156, v156, v155
	v_mul_f32_e32 v157, v157, v155
	v_mul_f32_e32 v158, v158, v155
	v_mul_f32_e32 v159, v159, v155
	v_mul_f32_e32 v160, v160, v155
	v_mul_f32_e32 v161, v161, v155
	v_mul_f32_e32 v162, v162, v155
	v_mul_f32_e32 v163, v163, v155
	v_max_f32_e32 v156, 0xc3e00000, v156
	v_max_f32_e32 v157, 0xc3e00000, v157
	v_max_f32_e32 v158, 0xc3e00000, v158
	v_max_f32_e32 v159, 0xc3e00000, v159
	v_max_f32_e32 v160, 0xc3e00000, v160
	v_max_f32_e32 v161, 0xc3e00000, v161
	v_max_f32_e32 v162, 0xc3e00000, v162
	v_max_f32_e32 v163, 0xc3e00000, v163
	v_min_f32_e32 v156, 0x43e00000, v156
	v_min_f32_e32 v157, 0x43e00000, v157
	v_min_f32_e32 v158, 0x43e00000, v158
	v_min_f32_e32 v159, 0x43e00000, v159
	v_min_f32_e32 v160, 0x43e00000, v160
	v_min_f32_e32 v161, 0x43e00000, v161
	v_min_f32_e32 v162, 0x43e00000, v162
	v_min_f32_e32 v163, 0x43e00000, v163
	v_cndmask_b32_e32 v156, 0, v156, vcc
	v_cndmask_b32_e32 v157, 0, v157, vcc
	v_cndmask_b32_e32 v158, 0, v158, vcc
	v_cndmask_b32_e32 v159, 0, v159, vcc
	v_cndmask_b32_e32 v160, 0, v160, vcc
	v_cndmask_b32_e32 v161, 0, v161, vcc
	v_cndmask_b32_e32 v162, 0, v162, vcc
	v_cndmask_b32_e32 v163, 0, v163, vcc
	v_mov_b32_e32 v182, 0
	v_mov_b32_e32 v183, 0
	v_cvt_pk_fp8_f32 v182, v156, v157
	v_cvt_pk_fp8_f32 v183, v160, v161
	v_add_u32_e32 v184, 0x1000, v142
	v_cvt_pk_fp8_f32 v182, v158, v159 op_sel:[0,0,1]
	v_cvt_pk_fp8_f32 v183, v162, v163 op_sel:[0,0,1]
	s_nop 1
	global_store_dwordx2 v184, v[182:183], s[12:13] sc1
	v_add_u32_e32 v154, 0x20, v66
	v_cmp_lt_i32_e32 vcc, v154, v64
	s_waitcnt vmcnt(3)
	v_mul_f32_e32 v155, 0x3c800000, v148
	v_mul_f32_e32 v156, 0xbd38aa3b, v28
	v_mul_f32_e32 v157, 0xbd38aa3b, v29
	v_mul_f32_e32 v158, 0xbd38aa3b, v30
	v_mul_f32_e32 v159, 0xbd38aa3b, v31
	v_mul_f32_e32 v160, 0xbd38aa3b, v20
	v_mul_f32_e32 v161, 0xbd38aa3b, v21
	v_mul_f32_e32 v162, 0xbd38aa3b, v22
	v_mul_f32_e32 v163, 0xbd38aa3b, v23
	v_exp_f32_e32 v156, v156
	v_exp_f32_e32 v157, v157
	v_exp_f32_e32 v158, v158
	v_exp_f32_e32 v159, v159
	v_exp_f32_e32 v160, v160
	v_exp_f32_e32 v161, v161
	v_exp_f32_e32 v162, v162
	v_exp_f32_e32 v163, v163
	v_add_f32_e32 v156, 1.0, v156
	v_add_f32_e32 v157, 1.0, v157
	v_add_f32_e32 v158, 1.0, v158
	v_add_f32_e32 v159, 1.0, v159
	v_add_f32_e32 v160, 1.0, v160
	v_add_f32_e32 v161, 1.0, v161
	v_add_f32_e32 v162, 1.0, v162
	v_add_f32_e32 v163, 1.0, v163
	v_rcp_f32_e32 v156, v156
	v_rcp_f32_e32 v157, v157
	v_rcp_f32_e32 v158, v158
	v_rcp_f32_e32 v159, v159
	v_rcp_f32_e32 v160, v160
	v_rcp_f32_e32 v161, v161
	v_rcp_f32_e32 v162, v162
	v_rcp_f32_e32 v163, v163
	v_mul_f32_e32 v156, v28, v156
	v_mul_f32_e32 v157, v29, v157
	v_mul_f32_e32 v158, v30, v158
	v_mul_f32_e32 v159, v31, v159
	v_mul_f32_e32 v160, v20, v160
	v_mul_f32_e32 v161, v21, v161
	v_mul_f32_e32 v162, v22, v162
	v_mul_f32_e32 v163, v23, v163
	v_mul_f32_e32 v156, v156, v24
	v_mul_f32_e32 v157, v157, v25
	v_mul_f32_e32 v158, v158, v26
	v_mul_f32_e32 v159, v159, v27
	v_mul_f32_e32 v160, v160, v16
	v_mul_f32_e32 v161, v161, v17
	v_mul_f32_e32 v162, v162, v18
	v_mul_f32_e32 v163, v163, v19
	v_mul_f32_e32 v156, v156, v155
	v_mul_f32_e32 v157, v157, v155
	v_mul_f32_e32 v158, v158, v155
	v_mul_f32_e32 v159, v159, v155
	v_mul_f32_e32 v160, v160, v155
	v_mul_f32_e32 v161, v161, v155
	v_mul_f32_e32 v162, v162, v155
	v_mul_f32_e32 v163, v163, v155
	v_max_f32_e32 v156, 0xc3e00000, v156
	v_max_f32_e32 v157, 0xc3e00000, v157
	v_max_f32_e32 v158, 0xc3e00000, v158
	v_max_f32_e32 v159, 0xc3e00000, v159
	v_max_f32_e32 v160, 0xc3e00000, v160
	v_max_f32_e32 v161, 0xc3e00000, v161
	v_max_f32_e32 v162, 0xc3e00000, v162
	v_max_f32_e32 v163, 0xc3e00000, v163
	v_min_f32_e32 v156, 0x43e00000, v156
	v_min_f32_e32 v157, 0x43e00000, v157
	v_min_f32_e32 v158, 0x43e00000, v158
	v_min_f32_e32 v159, 0x43e00000, v159
	v_min_f32_e32 v160, 0x43e00000, v160
	v_min_f32_e32 v161, 0x43e00000, v161
	v_min_f32_e32 v162, 0x43e00000, v162
	v_min_f32_e32 v163, 0x43e00000, v163
	v_cndmask_b32_e32 v156, 0, v156, vcc
	v_cndmask_b32_e32 v157, 0, v157, vcc
	v_cndmask_b32_e32 v158, 0, v158, vcc
	v_cndmask_b32_e32 v159, 0, v159, vcc
	v_cndmask_b32_e32 v160, 0, v160, vcc
	v_cndmask_b32_e32 v161, 0, v161, vcc
	v_cndmask_b32_e32 v162, 0, v162, vcc
	v_cndmask_b32_e32 v163, 0, v163, vcc
	v_mov_b32_e32 v180, 0
	v_mov_b32_e32 v181, 0
	v_cvt_pk_fp8_f32 v180, v156, v157
	v_cvt_pk_fp8_f32 v181, v160, v161
	v_add_u32_e32 v184, 0x2000, v142
	v_cvt_pk_fp8_f32 v180, v158, v159 op_sel:[0,0,1]
	v_cvt_pk_fp8_f32 v181, v162, v163 op_sel:[0,0,1]
	s_nop 1
	global_store_dwordx2 v184, v[180:181], s[12:13] sc1
	v_add_u32_e32 v154, 0x30, v66
	v_cmp_lt_i32_e32 vcc, v154, v64
	s_waitcnt vmcnt(3)
	v_mul_f32_e32 v155, 0x3c800000, v149
	v_mul_f32_e32 v156, 0xbd38aa3b, v12
	v_mul_f32_e32 v157, 0xbd38aa3b, v13
	v_mul_f32_e32 v158, 0xbd38aa3b, v14
	v_mul_f32_e32 v159, 0xbd38aa3b, v15
	v_mul_f32_e32 v160, 0xbd38aa3b, v4
	v_mul_f32_e32 v161, 0xbd38aa3b, v5
	v_mul_f32_e32 v162, 0xbd38aa3b, v6
	v_mul_f32_e32 v163, 0xbd38aa3b, v7
	v_exp_f32_e32 v156, v156
	v_exp_f32_e32 v157, v157
	v_exp_f32_e32 v158, v158
	v_exp_f32_e32 v159, v159
	v_exp_f32_e32 v160, v160
	v_exp_f32_e32 v161, v161
	v_exp_f32_e32 v162, v162
	v_exp_f32_e32 v163, v163
	v_add_f32_e32 v156, 1.0, v156
	v_add_f32_e32 v157, 1.0, v157
	v_add_f32_e32 v158, 1.0, v158
	v_add_f32_e32 v159, 1.0, v159
	v_add_f32_e32 v160, 1.0, v160
	v_add_f32_e32 v161, 1.0, v161
	v_add_f32_e32 v162, 1.0, v162
	v_add_f32_e32 v163, 1.0, v163
	v_rcp_f32_e32 v156, v156
	v_rcp_f32_e32 v157, v157
	v_rcp_f32_e32 v158, v158
	v_rcp_f32_e32 v159, v159
	v_rcp_f32_e32 v160, v160
	v_rcp_f32_e32 v161, v161
	v_rcp_f32_e32 v162, v162
	v_rcp_f32_e32 v163, v163
	v_mul_f32_e32 v156, v12, v156
	v_mul_f32_e32 v157, v13, v157
	v_mul_f32_e32 v158, v14, v158
	v_mul_f32_e32 v159, v15, v159
	v_mul_f32_e32 v160, v4, v160
	v_mul_f32_e32 v161, v5, v161
	v_mul_f32_e32 v162, v6, v162
	v_mul_f32_e32 v163, v7, v163
	v_mul_f32_e32 v156, v156, v8
	v_mul_f32_e32 v157, v157, v9
	v_mul_f32_e32 v158, v158, v10
	v_mul_f32_e32 v159, v159, v11
	v_mul_f32_e32 v160, v160, v0
	v_mul_f32_e32 v161, v161, v1
	v_mul_f32_e32 v162, v162, v2
	v_mul_f32_e32 v163, v163, v3
	v_mul_f32_e32 v156, v156, v155
	v_mul_f32_e32 v157, v157, v155
	v_mul_f32_e32 v158, v158, v155
	v_mul_f32_e32 v159, v159, v155
	v_mul_f32_e32 v160, v160, v155
	v_mul_f32_e32 v161, v161, v155
	v_mul_f32_e32 v162, v162, v155
	v_mul_f32_e32 v163, v163, v155
	v_max_f32_e32 v156, 0xc3e00000, v156
	v_max_f32_e32 v157, 0xc3e00000, v157
	v_max_f32_e32 v158, 0xc3e00000, v158
	v_max_f32_e32 v159, 0xc3e00000, v159
	v_max_f32_e32 v160, 0xc3e00000, v160
	v_max_f32_e32 v161, 0xc3e00000, v161
	v_max_f32_e32 v162, 0xc3e00000, v162
	v_max_f32_e32 v163, 0xc3e00000, v163
	v_min_f32_e32 v156, 0x43e00000, v156
	v_min_f32_e32 v157, 0x43e00000, v157
	v_min_f32_e32 v158, 0x43e00000, v158
	v_min_f32_e32 v159, 0x43e00000, v159
	v_min_f32_e32 v160, 0x43e00000, v160
	v_min_f32_e32 v161, 0x43e00000, v161
	v_min_f32_e32 v162, 0x43e00000, v162
	v_min_f32_e32 v163, 0x43e00000, v163
	v_cndmask_b32_e32 v156, 0, v156, vcc
	v_cndmask_b32_e32 v157, 0, v157, vcc
	v_cndmask_b32_e32 v158, 0, v158, vcc
	v_cndmask_b32_e32 v159, 0, v159, vcc
	v_cndmask_b32_e32 v160, 0, v160, vcc
	v_cndmask_b32_e32 v161, 0, v161, vcc
	v_cndmask_b32_e32 v162, 0, v162, vcc
	v_cndmask_b32_e32 v163, 0, v163, vcc
	v_mov_b32_e32 v182, 0
	v_mov_b32_e32 v183, 0
	v_cvt_pk_fp8_f32 v182, v156, v157
	v_cvt_pk_fp8_f32 v183, v160, v161
	v_add_u32_e32 v184, 0x3000, v142
	v_cvt_pk_fp8_f32 v182, v158, v159 op_sel:[0,0,1]
	v_cvt_pk_fp8_f32 v183, v162, v163 op_sel:[0,0,1]
	s_nop 1
	global_store_dwordx2 v184, v[182:183], s[12:13] sc1
	v_bfe_u32 v50, v72, 4, 2
	s_waitcnt vmcnt(0)
	v_or_b32_e32 v0, v50, v70
	v_cmp_eq_u32_e32 vcc, 0, v0
	s_and_saveexec_b64 s[0:1], vcc
	s_cbranch_execz .LBB0_1364
	s_mov_b64 s[4:5], exec
	v_mbcnt_lo_u32_b32 v0, s4, 0
	v_mbcnt_hi_u32_b32 v0, s5, v0
	v_cmp_eq_u32_e32 vcc, 0, v0
	s_and_b64 s[10:11], exec, vcc
	s_mov_b64 exec, s[10:11]
	s_cbranch_execz .LBB0_1364
	s_lshl_b32 s10, s18, 5
	s_ashr_i32 s11, s10, 31
	s_lshl_b64 s[10:11], s[10:11], 2
	s_add_u32 s10, s29, s10
	s_addc_u32 s11, s50, s11
	s_bcnt1_i32_b64 s4, s[4:5]
	v_mov_b32_e32 v0, 0
	v_mov_b32_e32 v1, s4
	global_atomic_add v0, v1, s[10:11]

.LBB0_1381:
	v_bfe_i32 v3, v0, 27, 1
	v_lshlrev_b32_e32 v1, 4, v0
	v_lshrrev_b32_e32 v3, 22, v3
	v_add_u32_e32 v3, v1, v3
	v_and_b32_e32 v3, 0xfffffc00, v3
	v_ashrrev_i32_e32 v2, 31, v0
	v_sub_u32_e32 v1, v1, v3
	v_lshrrev_b32_e32 v2, 26, v2
	v_lshrrev_b32_e32 v3, 4, v1
	v_add_u32_e32 v2, v0, v2
	v_bitop3_b32 v3, v3, v1, 32 bitop3:0x6c
	v_ashrrev_i32_e32 v1, 31, v1
	v_ashrrev_i32_e32 v2, 6, v2
	v_lshrrev_b32_e32 v1, 26, v1
	v_lshlrev_b32_e32 v4, 3, v2
	v_add_u32_e32 v1, v3, v1
	s_add_u32 s14, s78, 0x6500000
	v_and_b32_e32 v4, -16, v4
	v_ashrrev_i32_e32 v1, 6, v1
	v_lshlrev_b32_e32 v2, 5, v2
	s_addc_u32 s15, s79, 0
	s_ashr_i32 s4, s21, 6
	v_add_u32_e32 v4, v1, v4
	v_and_b32_e32 v5, 32, v2
	v_mul_i32_i24_e32 v2, 64, v1
	v_and_b32_e32 v1, 3, v1
	s_mov_b32 s16, 0xffffe0
	s_ashr_i32 s41, s40, 31
	s_ashr_i32 s5, s21, 8
	v_and_or_b32 v1, v4, s16, v1
	s_lshl_b32 s51, s4, 10
	s_lshl_b64 s[16:17], s[40:41], 16
	v_sub_u32_e32 v2, v3, v2
	v_mov_b32_e32 v3, 1
	s_add_u32 s42, s12, s16
	v_ashrrev_i16_sdwa v2, v3, sext(v2) dst_sel:DWORD dst_unused:UNUSED_PAD src0_sel:DWORD src1_sel:BYTE_0
	s_addc_u32 s43, s13, s17
	s_lshl_b32 s16, s40, 2
	v_bfe_i32 v3, v2, 0, 16
	v_lshlrev_b32_e32 v2, 1, v4
	s_add_i32 s16, s16, 0
	v_and_b32_e32 v6, 24, v2
	v_lshrrev_b32_e32 v2, 2, v4
	s_add_i32 s16, s16, 0x24100
	v_and_b32_e32 v7, 4, v2
	s_barrier
	v_mov_b32_e32 v2, s16
	ds_read_b32 v2, v2
	v_or3_b32 v1, v1, v7, v6
	v_add_lshl_u32 v3, v5, v3, 1
	v_lshl_add_u32 v194, v1, 8, v3
	v_lshl_add_u32 v195, v4, 8, v3
	s_waitcnt lgkmcnt(0)
	v_ashrrev_i32_e32 v3, 31, v2
	v_lshlrev_b64 v[2:3], 18, v[2:3]
	s_ashr_i32 s39, s38, 31
	v_lshl_add_u64 v[2:3], s[14:15], 0, v[2:3]
	s_lshl_b64 s[16:17], s[38:39], 16
	v_lshl_add_u64 v[2:3], v[2:3], 0, s[16:17]
	s_add_i32 s52, s51, 0
	v_readfirstlane_b32 s17, v3
	v_readfirstlane_b32 s16, v2
	s_mov_b64 s[18:19], s[16:17]
	s_add_i32 m0, s52, 0x10000
	s_mov_b32 s64, 0
	global_load_lds_dwordx4 v194, s[18:19]
	s_add_u32 s18, s16, 0x4000
	s_addc_u32 s19, s17, 0
	s_add_i32 m0, s52, 0x12000
	s_nop 0
	global_load_lds_dwordx4 v194, s[18:19]
	s_add_i32 m0, s52, 0x14000
	s_add_u32 s18, s16, 0x8000
	s_addc_u32 s19, s17, 0
	s_nop 0
	global_load_lds_dwordx4 v194, s[18:19]
	s_add_u32 s18, s16, 0xc000
	s_addc_u32 s19, s17, 0
	s_add_i32 m0, s52, 0x16000
	s_nop 0
	global_load_lds_dwordx4 v194, s[18:19]
	v_mov_b32_e32 v1, v195
	s_mov_b64 s[18:19], s[42:43]
	s_mov_b32 m0, s52
	s_nop 0
	global_load_lds_dwordx4 v1, s[18:19] sc1
	s_add_u32 s18, s42, 0x4000
	v_mov_b32_e32 v1, v195
	s_addc_u32 s19, s43, 0
	s_add_i32 s53, s52, 0x2000
	s_mov_b32 m0, s53
	s_add_i32 s60, s52, 0x4000
	global_load_lds_dwordx4 v1, s[18:19] sc1
	s_add_u32 s18, s42, 0x8000
	v_mov_b32_e32 v1, v195
	s_addc_u32 s19, s43, 0
	s_mov_b32 m0, s60
	s_nop 0
	global_load_lds_dwordx4 v1, s[18:19] sc1
	s_add_u32 s18, s42, 0xc000
	s_addc_u32 s19, s43, 0
	s_add_i32 s61, s52, 0x6000
	v_mov_b32_e32 v1, v195
	s_mov_b32 m0, s61
	s_cmp_eq_u32 s5, 1
	global_load_lds_dwordx4 v1, s[18:19] sc1
	s_cselect_b64 s[18:19], -1, 0
	s_cmp_lg_u32 s5, 1
	s_cbranch_scc1 .LBB0_1383
	s_barrier
.LBB0_1383:
	s_lshl_b32 s4, s4, 5
	s_and_b32 s65, s4, 0x60
	s_lshl_b32 s20, s5, 6
	s_lshl_b32 s24, s5, 13
	s_lshl_b32 s25, s65, 7
	s_add_u32 s22, s78, 0x12500000
	s_addc_u32 s23, s79, 0
	s_add_u32 s4, s16, 0x80
	s_addc_u32 s5, s17, 0
	s_waitcnt vmcnt(2)
	s_barrier
	s_add_i32 m0, s52, 0x18000
	v_lshlrev_b32_e32 v2, 6, v0
	global_load_lds_dwordx4 v194, s[4:5]
	s_add_u32 s4, s16, 0x4080
	s_addc_u32 s5, s17, 0
	s_add_i32 m0, s52, 0x1a000
	v_mov_b32_e32 v193, 0
	global_load_lds_dwordx4 v194, s[4:5]
	s_add_u32 s4, s42, 0x80
	s_addc_u32 s5, s43, 0
	v_mov_b32_e32 v1, v195
	s_add_i32 s68, s52, 0x8000
	s_mov_b32 m0, s68
	s_mov_b32 s28, 0x3e000000
	global_load_lds_dwordx4 v1, s[4:5] sc1
	s_add_u32 s4, s42, 0x4080
	s_addc_u32 s5, s43, 0
	s_add_i32 s69, s52, 0xa000
	v_mov_b32_e32 v1, v195
	s_mov_b32 m0, s69
	s_nop 0
	global_load_lds_dwordx4 v1, s[4:5] sc1
	s_add_i32 m0, s52, 0x1c000
	s_add_u32 s4, s16, 0x8080
	s_addc_u32 s5, s17, 0
	s_nop 0
	global_load_lds_dwordx4 v194, s[4:5]
	s_add_u32 s4, s16, 0xc080
	s_addc_u32 s5, s17, 0
	s_add_i32 m0, s52, 0x1e000
	s_cmpk_lt_u32 s21, 0x100
	global_load_lds_dwordx4 v194, s[4:5]
	v_and_b32_e32 v1, 48, v0
	s_movk_i32 s4, 0x3c0
	v_lshlrev_b32_e32 v0, 2, v0
	v_and_or_b32 v1, v2, s4, v1
	v_and_b32_e32 v0, 32, v0
	s_waitcnt vmcnt(6)
	v_bitop3_b32 v2, v1, s24, v0 bitop3:0xde
	v_bitop3_b32 v196, s25, v1, v0 bitop3:0xf6
	s_cselect_b64 s[24:25], -1, 0
	s_ashr_i32 s21, s20, 31
	v_cndmask_b32_e64 v0, 0, 1, s[0:1]
	s_add_i32 s73, 0, 0x10000
	s_add_i32 s74, 0, 0x14000
	s_sub_i32 s70, s33, s27
	s_sub_i32 s71, s2, s27
	s_lshl_b32 s72, s26, 2
	v_cmp_ne_u32_e64 s[0:1], 1, v0
	v_add_u32_e32 v197, s73, v196
	v_add_u32_e32 v198, s74, v196
	v_add_u32_e32 v199, 0, v2
	s_lshl_b64 s[26:27], s[20:21], 2
	s_barrier
	s_branch .LBB0_1386

.LBB0_1402:
	s_waitcnt vmcnt(0)
	ds_read_b128 v[56:59], v197
	ds_read_b128 v[60:63], v197 offset:1024
	ds_read_b128 v[80:83], v197 offset:2048
	ds_read_b128 v[84:87], v197 offset:3072
	ds_read_b128 v[0:3], v198
	ds_read_b128 v[4:7], v198 offset:1024
	ds_read_b128 v[8:11], v198 offset:2048
	ds_read_b128 v[12:15], v198 offset:3072
	s_add_u32 s44, s36, 0x80
	s_addc_u32 s45, s37, 0
	s_add_u32 s48, s16, 0x80
	s_addc_u32 s49, s17, 0
	s_add_u32 s78, s42, 0x8080
	v_mov_b32_e32 v16, v195
	s_addc_u32 s79, s43, 0
	s_add_i32 m0, s52, 0xc000
	ds_read_b128 v[64:67], v199
	ds_read_b128 v[68:71], v199 offset:1024
	ds_read_b128 v[72:75], v199 offset:2048
	ds_read_b128 v[76:79], v199 offset:3072
	ds_read_b128 v[88:91], v199 offset:4096
	ds_read_b128 v[92:95], v199 offset:5120
	ds_read_b128 v[96:99], v199 offset:6144
	ds_read_b128 v[100:103], v199 offset:7168
	s_add_u32 s42, s42, 0xc080
	s_addc_u32 s43, s43, 0
	global_load_lds_dwordx4 v16, s[78:79] sc1
	v_mov_b32_e32 v16, v195
	s_add_i32 m0, s52, 0xe000
	s_nop 0
	global_load_lds_dwordx4 v16, s[42:43] sc1
	s_waitcnt vmcnt(8)
	s_waitcnt lgkmcnt(0)
	s_barrier
	s_setprio 3
	v_mfma_f32_16x16x128_f8f6f4 v[16:19], v[56:63], v[64:71], 0
	v_mfma_f32_16x16x128_f8f6f4 v[20:23], v[80:87], v[64:71], 0
	v_mfma_f32_16x16x128_f8f6f4 v[24:27], v[56:63], v[72:79], 0
	v_mfma_f32_16x16x128_f8f6f4 v[28:31], v[80:87], v[72:79], 0
	v_mfma_f32_16x16x128_f8f6f4 v[32:35], v[56:63], v[88:95], 0
	v_mfma_f32_16x16x128_f8f6f4 v[36:39], v[80:87], v[88:95], 0
	v_mfma_f32_16x16x128_f8f6f4 v[40:43], v[56:63], v[96:103], 0
	v_mfma_f32_16x16x128_f8f6f4 v[44:47], v[80:87], v[96:103], 0
	v_mfma_f32_16x16x128_f8f6f4 v[48:51], v[0:7], v[64:71], 0
	v_mfma_f32_16x16x128_f8f6f4 v[52:55], v[8:15], v[64:71], 0
	v_mfma_f32_16x16x128_f8f6f4 v[64:67], v[0:7], v[72:79], 0
	v_mfma_f32_16x16x128_f8f6f4 v[68:71], v[8:15], v[72:79], 0
	v_mfma_f32_16x16x128_f8f6f4 v[72:75], v[0:7], v[88:95], 0
	v_mfma_f32_16x16x128_f8f6f4 v[76:79], v[8:15], v[88:95], 0
	v_mfma_f32_16x16x128_f8f6f4 v[128:131], v[0:7], v[96:103], 0
	v_mfma_f32_16x16x128_f8f6f4 v[132:135], v[8:15], v[96:103], 0
	s_setprio 0
	s_barrier
	v_mov_b32_e32 v120, v194
	s_mov_b64 s[42:43], s[16:17]
	s_add_i32 s21, s73, s51
	ds_read_b128 v[88:91], v199 offset:16384
	ds_read_b128 v[92:95], v199 offset:17408
	ds_read_b128 v[96:99], v199 offset:18432
	ds_read_b128 v[100:103], v199 offset:19456
	ds_read_b128 v[104:107], v199 offset:20480
	ds_read_b128 v[108:111], v199 offset:21504
	ds_read_b128 v[112:115], v199 offset:22528
	ds_read_b128 v[116:119], v199 offset:23552
	s_mov_b32 m0, s21
	s_nop 0
	global_load_lds_dwordx4 v120, s[42:43]
	s_add_u32 s42, s16, 0x4000
	s_addc_u32 s43, s17, 0
	s_add_i32 m0, s21, 0x2000
	s_nop 0
	global_load_lds_dwordx4 v194, s[42:43]
	s_add_u32 s42, s16, 0x8000
	s_addc_u32 s43, s17, 0
	s_add_i32 s21, s74, s51
	s_mov_b32 m0, s21
	s_nop 0
	global_load_lds_dwordx4 v194, s[42:43]
	s_add_u32 s42, s16, 0xc000
	s_addc_u32 s43, s17, 0
	s_add_i32 m0, s21, 0x2000
	s_nop 0
	global_load_lds_dwordx4 v194, s[42:43]
	v_mov_b32_e32 v120, v195
	s_mov_b64 s[42:43], s[36:37]
	s_mov_b32 m0, s52
	s_nop 0
	global_load_lds_dwordx4 v120, s[42:43] sc1
	s_add_u32 s42, s36, 0x4000
	v_mov_b32_e32 v120, v195
	s_addc_u32 s43, s37, 0
	s_mov_b32 m0, s53
	s_nop 0
	global_load_lds_dwordx4 v120, s[42:43] sc1
	s_waitcnt vmcnt(8)
	s_waitcnt lgkmcnt(0)
	s_barrier
	s_setprio 3
	v_mfma_f32_16x16x128_f8f6f4 v[136:139], v[56:63], v[88:95], 0
	v_mfma_f32_16x16x128_f8f6f4 v[140:143], v[80:87], v[88:95], 0
	v_mfma_f32_16x16x128_f8f6f4 v[144:147], v[56:63], v[96:103], 0
	v_mfma_f32_16x16x128_f8f6f4 v[148:151], v[80:87], v[96:103], 0
	v_mfma_f32_16x16x128_f8f6f4 v[152:155], v[56:63], v[104:111], 0
	v_mfma_f32_16x16x128_f8f6f4 v[156:159], v[80:87], v[104:111], 0
	v_mfma_f32_16x16x128_f8f6f4 v[160:163], v[56:63], v[112:119], 0
	v_mfma_f32_16x16x128_f8f6f4 v[164:167], v[80:87], v[112:119], 0
	v_mfma_f32_16x16x128_f8f6f4 v[168:171], v[0:7], v[88:95], 0
	v_mfma_f32_16x16x128_f8f6f4 v[176:179], v[0:7], v[96:103], 0
	v_mfma_f32_16x16x128_f8f6f4 v[184:187], v[0:7], v[104:111], 0
	v_mfma_f32_16x16x128_f8f6f4 v[0:3], v[0:7], v[112:119], 0
	v_mfma_f32_16x16x128_f8f6f4 v[4:7], v[8:15], v[112:119], 0
	v_mfma_f32_16x16x128_f8f6f4 v[172:175], v[8:15], v[88:95], 0
	v_mfma_f32_16x16x128_f8f6f4 v[180:183], v[8:15], v[96:103], 0
	v_mfma_f32_16x16x128_f8f6f4 v[188:191], v[8:15], v[104:111], 0
	s_setprio 0
	s_barrier
	s_add_i32 s21, 0, 0x18000
	v_add_u32_e32 v56, s21, v196
	s_add_i32 s31, 0, 0x1c000
	ds_read_b128 v[8:11], v56
	ds_read_b128 v[12:15], v56 offset:1024
	ds_read_b128 v[200:203], v56 offset:2048
	ds_read_b128 v[204:207], v56 offset:3072
	v_add_u32_e32 v56, s31, v196
	ds_read_b128 v[208:211], v56
	ds_read_b128 v[212:215], v56 offset:1024
	ds_read_b128 v[216:219], v56 offset:2048
	ds_read_b128 v[220:223], v56 offset:3072
	s_add_u32 s42, s36, 0x8000
	v_mov_b32_e32 v56, v195
	s_addc_u32 s43, s37, 0
	s_mov_b32 m0, s60
	ds_read_b128 v[88:91], v199 offset:32768
	ds_read_b128 v[92:95], v199 offset:33792
	ds_read_b128 v[224:227], v199 offset:34816
	ds_read_b128 v[228:231], v199 offset:35840
	ds_read_b128 v[232:235], v199 offset:36864
	ds_read_b128 v[236:239], v199 offset:37888
	ds_read_b128 v[240:243], v199 offset:38912
	ds_read_b128 v[244:247], v199 offset:39936
	s_nop 0
	global_load_lds_dwordx4 v56, s[42:43] sc1
	s_add_u32 s42, s36, 0xc000
	v_mov_b32_e32 v56, v195
	s_addc_u32 s43, s37, 0
	s_mov_b32 m0, s61
	s_nop 0
	global_load_lds_dwordx4 v56, s[42:43] sc1
	s_waitcnt vmcnt(8)
	s_waitcnt lgkmcnt(0)
	s_barrier
	s_setprio 3
	v_mfma_f32_16x16x128_f8f6f4 v[112:115], v[8:15], v[88:95], v[16:19]
	v_mfma_f32_16x16x128_f8f6f4 v[116:119], v[200:207], v[88:95], v[20:23]
	v_mfma_f32_16x16x128_f8f6f4 v[96:99], v[8:15], v[224:231], v[24:27]
	v_mfma_f32_16x16x128_f8f6f4 v[100:103], v[200:207], v[224:231], v[28:31]
	v_mfma_f32_16x16x128_f8f6f4 v[80:83], v[8:15], v[232:239], v[32:35]
	v_mfma_f32_16x16x128_f8f6f4 v[84:87], v[200:207], v[232:239], v[36:39]
	v_mfma_f32_16x16x128_f8f6f4 v[56:59], v[8:15], v[240:247], v[40:43]
	v_mfma_f32_16x16x128_f8f6f4 v[60:63], v[200:207], v[240:247], v[44:47]
	v_mfma_f32_16x16x128_f8f6f4 v[120:123], v[208:215], v[88:95], v[48:51]
	v_mfma_f32_16x16x128_f8f6f4 v[124:127], v[216:223], v[88:95], v[52:55]
	v_mfma_f32_16x16x128_f8f6f4 v[104:107], v[208:215], v[224:231], v[64:67]
	v_mfma_f32_16x16x128_f8f6f4 v[108:111], v[216:223], v[224:231], v[68:71]
	v_mfma_f32_16x16x128_f8f6f4 v[88:91], v[208:215], v[232:239], v[72:75]
	v_mfma_f32_16x16x128_f8f6f4 v[92:95], v[216:223], v[232:239], v[76:79]
	v_mfma_f32_16x16x128_f8f6f4 v[64:67], v[208:215], v[240:247], v[128:131]
	v_mfma_f32_16x16x128_f8f6f4 v[68:71], v[216:223], v[240:247], v[132:135]
	s_setprio 0
	s_barrier
	v_mov_b32_e32 v24, v194
	s_add_i32 s21, s21, s51
	ds_read_b128 v[16:19], v199 offset:49152
	ds_read_b128 v[20:23], v199 offset:50176
	ds_read_b128 v[128:131], v199 offset:51200
	ds_read_b128 v[132:135], v199 offset:52224
	ds_read_b128 v[224:227], v199 offset:53248
	ds_read_b128 v[228:231], v199 offset:54272
	ds_read_b128 v[232:235], v199 offset:55296
	ds_read_b128 v[236:239], v199 offset:56320
	s_mov_b32 m0, s21
	s_add_u32 s42, s16, 0x4080
	s_addc_u32 s43, s17, 0
	global_load_lds_dwordx4 v24, s[48:49]
	s_add_i32 m0, s21, 0x2000
	s_nop 0
	global_load_lds_dwordx4 v194, s[42:43]
	s_add_u32 s42, s16, 0x8080
	s_addc_u32 s43, s17, 0
	s_add_i32 s21, s31, s51
	s_mov_b32 m0, s21
	s_nop 0
	global_load_lds_dwordx4 v194, s[42:43]
	s_add_u32 s42, s16, 0xc080
	s_addc_u32 s43, s17, 0
	s_add_i32 m0, s21, 0x2000
	s_nop 0
	global_load_lds_dwordx4 v194, s[42:43]
	v_mov_b32_e32 v24, v195
	s_mov_b32 m0, s68
	s_add_u32 s42, s36, 0x4080
	s_addc_u32 s43, s37, 0
	global_load_lds_dwordx4 v24, s[44:45] sc1
	v_mov_b32_e32 v24, v195
	s_mov_b32 m0, s69
	s_nop 0
	global_load_lds_dwordx4 v24, s[42:43] sc1
	s_waitcnt vmcnt(8)
	s_waitcnt lgkmcnt(0)
	s_barrier
	s_setprio 3
	v_mfma_f32_16x16x128_f8f6f4 v[48:51], v[8:15], v[16:23], v[136:139]
	v_mfma_f32_16x16x128_f8f6f4 v[52:55], v[200:207], v[16:23], v[140:143]
	v_mfma_f32_16x16x128_f8f6f4 v[32:35], v[8:15], v[128:135], v[144:147]
	v_mfma_f32_16x16x128_f8f6f4 v[36:39], v[200:207], v[128:135], v[148:151]
	v_mfma_f32_16x16x128_f8f6f4 v[24:27], v[8:15], v[224:231], v[152:155]
	v_mfma_f32_16x16x128_f8f6f4 v[28:31], v[200:207], v[224:231], v[156:159]
	v_mfma_f32_16x16x128_f8f6f4 v[8:11], v[8:15], v[232:239], v[160:163]
	v_mfma_f32_16x16x128_f8f6f4 v[12:15], v[200:207], v[232:239], v[164:167]
	v_mfma_f32_16x16x128_f8f6f4 v[72:75], v[208:215], v[16:23], v[168:171]
	v_mfma_f32_16x16x128_f8f6f4 v[76:79], v[216:223], v[16:23], v[172:175]
	v_mfma_f32_16x16x128_f8f6f4 v[40:43], v[208:215], v[128:135], v[176:179]
	v_mfma_f32_16x16x128_f8f6f4 v[44:47], v[216:223], v[128:135], v[180:183]
	v_mfma_f32_16x16x128_f8f6f4 v[16:19], v[208:215], v[224:231], v[184:187]
	v_mfma_f32_16x16x128_f8f6f4 v[20:23], v[216:223], v[224:231], v[188:191]
	v_mfma_f32_16x16x128_f8f6f4 v[0:3], v[208:215], v[232:239], v[0:3]
	v_mfma_f32_16x16x128_f8f6f4 v[4:7], v[216:223], v[232:239], v[4:7]
	s_setprio 0
	s_barrier
	s_andn2_b64 vcc, exec, s[24:25]
	s_cbranch_vccnz .LBB0_1404
	s_barrier

.LBB0_1457:
	s_add_i32 s3, 0, 0x24808
	v_mov_b32_e32 v3, s3
	ds_read_b32 v4, v3
	s_mov_b64 s[0:1], exec
	v_mbcnt_lo_u32_b32 v2, s0, 0
	v_mbcnt_hi_u32_b32 v2, s1, v2
	v_cmp_eq_u32_e32 vcc, 0, v2
	s_waitcnt lgkmcnt(0)
	v_add_u32_e32 v4, 1, v4
	v_mov_b32_e32 v7, v4
	ds_write_b32 v3, v4
	s_and_saveexec_b64 s[10:11], vcc
	s_cbranch_execz .LBB0_1459
	v_readlane_b32 s3, v249, 34
	s_lshl_b32 s3, s3, 8
	s_add_u32 s12, s94, s3
	s_addc_u32 s13, s95, 0
	s_bcnt1_i32_b64 s0, s[0:1]
	v_mov_b32_e32 v3, 0x1000
	v_mov_b32_e32 v4, s0
	global_atomic_add v3, v3, v4, s[12:13] offset:1024 sc0
.LBB0_1459:
	s_or_b64 exec, exec, s[10:11]
	s_waitcnt vmcnt(0)
	v_readfirstlane_b32 s0, v3
	s_nop 1
	v_add_u32_e32 v2, s0, v2
	v_add_u32_e32 v5, 1, v2
	v_mul_lo_u32 v1, v1, v7
	v_add_u32_e32 v2, -1, v7
	v_cmp_eq_u32_e64 s[0:1], v5, v1
	v_cmp_ne_u32_e32 vcc, v5, v1
	s_nop 0
	v_cndmask_b32_e64 v1, 0, 1, s[0:1]
	s_add_i32 s0, 0, 0x2480c
	v_mov_b32_e32 v3, s0
	s_add_i32 s0, 0, 0x24810
	ds_write_b32 v3, v1
	v_mov_b32_e32 v1, s0
	ds_write_b32 v1, v2
	s_and_saveexec_b64 s[0:1], vcc
	s_xor_b64 s[0:1], exec, s[0:1]
	s_cbranch_execz .LBB0_1462
	s_add_i32 s3, 0, 0x24808
	v_mov_b32_e32 v0, s3
	ds_read_b32 v0, v0
	s_waitcnt lgkmcnt(0)
	v_and_b32_e32 v0, 1, v0
	v_cmp_eq_u32_e32 vcc, 0, v0
	s_cbranch_vccnz .LBB0_1462
	buffer_inv sc1
	s_waitcnt vmcnt(0)
.LBB0_1462:
	s_andn2_saveexec_b64 s[0:1], s[0:1]
	s_cbranch_execz .LBB0_1469
	s_mov_b64 s[0:1], exec
	buffer_wbl2 sc1
	s_waitcnt lgkmcnt(0)
	s_waitcnt vmcnt(0)
	v_mbcnt_lo_u32_b32 v1, s0, 0
	v_mbcnt_hi_u32_b32 v1, s1, v1
	v_cmp_eq_u32_e32 vcc, 0, v1
	s_and_saveexec_b64 s[10:11], vcc
	s_cbranch_execz .LBB0_1465
	s_bcnt1_i32_b64 s0, s[0:1]
	v_mov_b32_e32 v2, 0x3000
	v_mov_b32_e32 v3, s0
	global_atomic_add v2, v3, s[94:95] offset:1024
.LBB0_1465:
	s_or_b64 exec, exec, s[10:11]
	s_branch .LBB0_1469
	v_cvt_f32_u32_e32 v3, v0
	s_waitcnt vmcnt(0)
	v_readfirstlane_b32 s0, v2
	v_sub_u32_e32 v2, 0, v0
	v_rcp_iflag_f32_e32 v3, v3
	v_add_u32_e32 v1, s0, v1
	v_mul_f32_e32 v3, 0x4f7ffffe, v3
	v_cvt_u32_f32_e32 v3, v3
	v_mul_lo_u32 v2, v2, v3
	v_mul_hi_u32 v2, v3, v2
	v_add_u32_e32 v2, v3, v2
	v_mul_hi_u32 v2, v1, v2
	v_mul_lo_u32 v3, v2, v0
	v_sub_u32_e32 v3, v1, v3
	v_add_u32_e32 v4, 1, v2
	v_cmp_ge_u32_e32 vcc, v3, v0
	v_add_u32_e32 v1, 1, v1
	s_nop 0
	v_cndmask_b32_e32 v2, v2, v4, vcc
	v_sub_u32_e32 v4, v3, v0
	v_cndmask_b32_e32 v3, v3, v4, vcc
	v_add_u32_e32 v4, 1, v2
	v_cmp_ge_u32_e32 vcc, v3, v0
	s_nop 1
	v_cndmask_b32_e32 v2, v2, v4, vcc
	v_mul_lo_u32 v2, v0, v2
	v_add_u32_e32 v0, v2, v0
	v_cmp_eq_u32_e32 vcc, v1, v0
	s_and_saveexec_b64 s[0:1], vcc
	s_cbranch_execz .LBB0_1468
	s_mov_b64 s[10:11], exec
	v_mbcnt_lo_u32_b32 v0, s10, 0
	v_mbcnt_hi_u32_b32 v0, s11, v0
	v_cmp_eq_u32_e32 vcc, 0, v0
	s_and_b64 s[12:13], exec, vcc
	s_mov_b64 exec, s[12:13]
	s_cbranch_execz .LBB0_1468
	s_bcnt1_i32_b64 s3, s[10:11]
	v_mov_b32_e32 v0, 0x3000
	v_mov_b32_e32 v1, s3
	global_atomic_add v0, v1, s[94:95] offset:1280

.LBB0_1756:
	s_andn2_b64 vcc, exec, s[0:1]
	s_cbranch_vccnz .LBB0_1808
	v_bfe_i32 v3, v0, 27, 1
	v_lshlrev_b32_e32 v1, 4, v0
	v_lshrrev_b32_e32 v3, 22, v3
	v_add_u32_e32 v3, v1, v3
	v_and_b32_e32 v3, 0xfffffc00, v3
	v_sub_u32_e32 v1, v1, v3
	v_ashrrev_i32_e32 v2, 31, v0
	v_lshrrev_b32_e32 v3, 4, v1
	v_lshrrev_b32_e32 v2, 26, v2
	v_bitop3_b32 v3, v3, v1, 32 bitop3:0x6c
	v_ashrrev_i32_e32 v1, 31, v1
	v_add_u32_e32 v2, v0, v2
	v_lshrrev_b32_e32 v1, 26, v1
	s_add_u32 s3, s78, 0x1900000
	v_ashrrev_i32_e32 v2, 6, v2
	v_add_u32_e32 v1, v3, v1
	s_addc_u32 s21, s79, 0
	s_ashr_i32 s1, s18, 6
	v_lshlrev_b32_e32 v4, 3, v2
	v_ashrrev_i32_e32 v1, 6, v1
	s_ashr_i32 s69, s68, 31
	s_ashr_i32 s0, s18, 8
	v_and_b32_e32 v4, -16, v4
	v_mul_i32_i24_e32 v5, 64, v1
	s_lshl_b32 s23, s1, 10
	s_lshl_b64 s[6:7], s[68:69], 19
	v_add_u32_e32 v4, v1, v4
	v_sub_u32_e32 v3, v3, v5
	v_mov_b32_e32 v5, 1
	v_and_b32_e32 v1, 3, v1
	s_mov_b32 s5, 0x1fffe0
	s_add_u32 s6, s90, s6
	v_lshlrev_b32_e32 v2, 5, v2
	v_ashrrev_i16_sdwa v3, v5, sext(v3) dst_sel:DWORD dst_unused:UNUSED_PAD src0_sel:DWORD src1_sel:BYTE_0
	v_lshlrev_b32_e32 v5, 1, v4
	v_lshrrev_b32_e32 v6, 2, v4
	v_and_or_b32 v1, v4, s5, v1
	s_addc_u32 s7, s91, s7
	s_ashr_i32 s5, s4, 31
	v_and_b32_e32 v2, 32, v2
	v_bfe_i32 v3, v3, 0, 16
	v_and_b32_e32 v5, 24, v5
	v_and_b32_e32 v6, 4, v6
	s_lshl_b64 s[12:13], s[4:5], 19
	v_or3_b32 v1, v1, v6, v5
	v_add_lshl_u32 v2, v2, v3, 1
	s_add_u32 s70, s3, s12
	v_lshl_add_u32 v152, v1, 11, v2
	s_addc_u32 s71, s21, s13
	s_add_i32 s25, s23, 0
	s_mov_b64 s[12:13], s[70:71]
	s_add_i32 m0, s25, 0x10000
	v_lshl_add_u32 v153, v4, 11, v2
	global_load_lds_dwordx4 v152, s[12:13]
	s_add_u32 s12, s70, 0x20000
	s_addc_u32 s13, s71, 0
	s_add_i32 m0, s25, 0x12000
	s_mov_b32 s15, 0
	global_load_lds_dwordx4 v152, s[12:13]
	s_add_i32 m0, s25, 0x14000
	s_add_u32 s12, s70, 0x40000
	s_addc_u32 s13, s71, 0
	s_nop 0
	global_load_lds_dwordx4 v152, s[12:13]
	s_add_u32 s12, s70, 0x60000
	s_addc_u32 s13, s71, 0
	s_add_i32 m0, s25, 0x16000
	s_nop 0
	global_load_lds_dwordx4 v152, s[12:13]
	s_mov_b64 s[12:13], s[6:7]
	s_mov_b32 m0, s25
	s_nop 0
	global_load_lds_dwordx4 v153, s[12:13]
	s_add_u32 s12, s6, 0x20000
	s_addc_u32 s13, s7, 0
	s_add_i32 s27, s25, 0x2000
	s_mov_b32 m0, s27
	s_add_i32 s29, s25, 0x4000
	global_load_lds_dwordx4 v153, s[12:13]
	s_add_u32 s12, s6, 0x40000
	s_addc_u32 s13, s7, 0
	s_mov_b32 m0, s29
	s_nop 0
	global_load_lds_dwordx4 v153, s[12:13]
	s_add_u32 s12, s6, 0x60000
	s_addc_u32 s13, s7, 0
	s_add_i32 s31, s25, 0x6000
	s_mov_b32 m0, s31
	s_cmp_eq_u32 s0, 1
	global_load_lds_dwordx4 v153, s[12:13]
	s_cselect_b64 s[12:13], -1, 0
	s_cmp_lg_u32 s0, 1
	s_cbranch_scc1 .LBB0_1759
	s_barrier
.LBB0_1759:
	s_add_u32 s16, s78, 0x600000
	s_addc_u32 s17, s79, 0
	s_and_b32 s14, s1, 3
	s_ashr_i32 s35, s33, 31
	s_ashr_i32 s37, s2, 31
	s_lshl_b32 s39, s0, 6
	s_lshl_b32 s5, s0, 13
	s_lshl_b32 s41, s14, 5
	s_lshl_b32 s19, s14, 12
	s_add_u32 s0, s70, 0x80
	s_addc_u32 s1, s71, 0
	s_waitcnt vmcnt(2)
	s_barrier
	s_add_i32 m0, s25, 0x18000
	v_lshlrev_b32_e32 v2, 6, v0
	global_load_lds_dwordx4 v152, s[0:1]
	s_add_u32 s0, s70, 0x20080
	s_addc_u32 s1, s71, 0
	s_add_i32 m0, s25, 0x1a000
	v_mov_b64_e32 v[144:145], 0x400
	global_load_lds_dwordx4 v152, s[0:1]
	s_add_u32 s0, s6, 0x80
	s_addc_u32 s1, s7, 0
	s_add_i32 s43, s25, 0x8000
	s_mov_b32 m0, s43
	s_mov_b32 s78, 0xc0900000
	global_load_lds_dwordx4 v153, s[0:1]
	s_add_u32 s0, s6, 0x20080
	s_addc_u32 s1, s7, 0
	s_add_i32 s45, s25, 0xa000
	s_mov_b32 m0, s45
	s_mov_b32 s20, 0x3dca4588
	global_load_lds_dwordx4 v153, s[0:1]
	s_add_i32 m0, s25, 0x1c000
	s_add_u32 s0, s70, 0x40080
	s_addc_u32 s1, s71, 0
	s_mov_b32 s22, 0x39d06f5c
	global_load_lds_dwordx4 v152, s[0:1]
	s_add_u32 s0, s70, 0x60080
	s_addc_u32 s1, s71, 0
	s_add_i32 m0, s25, 0x1e000
	s_cmpk_lt_u32 s18, 0x100
	global_load_lds_dwordx4 v152, s[0:1]
	v_and_b32_e32 v1, 48, v0
	s_movk_i32 s0, 0x3c0
	v_lshlrev_b32_e32 v0, 2, v0
	v_and_or_b32 v1, v2, s0, v1
	v_and_b32_e32 v0, 32, v0
	s_waitcnt vmcnt(6)
	v_bitop3_b32 v2, v1, s5, v0 bitop3:0xde
	v_bitop3_b32 v154, v1, s19, v0 bitop3:0xde
	s_cselect_b64 s[18:19], -1, 0
	s_add_i32 s49, 0, 0x10000
	s_add_i32 s77, 0, 0x14000
	v_add_u32_e32 v155, s49, v154
	v_add_u32_e32 v156, s77, v154
	v_add_u32_e32 v157, 0, v2
	s_mov_b32 s24, 0x3a8114f3
	s_mov_b32 s26, 0xbaa39819
	s_mov_b32 s28, 0x3b315f86
	s_mov_b32 s30, 0xbbcfcfd8
	s_mov_b32 s34, 0x3c3b8d5d
	s_mov_b32 s36, 0xbc97eaee
	s_mov_b32 s38, 0x3ce7ae16
	s_mov_b32 s40, 0xbd24a296
	s_mov_b32 s42, 0x3d600eae
	s_mov_b32 s44, 0xbd9e1598
	s_mov_b32 s48, 0x3e20abaf
	v_mov_b32_e32 v158, 0x40900000
	s_mov_b32 s79, s15
	s_barrier
	s_branch .LBB0_1762

.LBB0_1769:
	ds_read_b128 v[56:59], v155
	ds_read_b128 v[60:63], v155 offset:1024
	ds_read_b128 v[68:71], v155 offset:2048
	ds_read_b128 v[76:79], v155 offset:3072
	ds_read_b128 v[146:149], v156
	ds_read_b128 v[160:163], v156 offset:1024
	ds_read_b128 v[164:167], v156 offset:2048
	ds_read_b128 v[168:171], v156 offset:3072
	s_add_u32 s69, s6, 0xfffa0080
	s_addc_u32 s70, s7, -1
	s_cmp_eq_u32 s53, 12
	s_cselect_b32 s71, s61, s70
	s_cselect_b32 s70, s60, s69
	s_cselect_b32 s74, s64, s5
	s_cselect_b32 s75, s65, s51
	s_add_u32 s72, s70, 0x80
	s_addc_u32 s73, s71, 0
	s_add_u32 s80, s6, 0xfffe0000
	v_mov_b32_e32 v150, v153
	s_addc_u32 s81, s7, -1
	ds_read_b128 v[172:175], v157
	ds_read_b128 v[176:179], v157 offset:1024
	ds_read_b128 v[180:183], v157 offset:2048
	ds_read_b128 v[184:187], v157 offset:3072
	ds_read_b128 v[188:191], v157 offset:4096
	ds_read_b128 v[192:195], v157 offset:5120
	ds_read_b128 v[196:199], v157 offset:6144
	ds_read_b128 v[200:203], v157 offset:7168
	s_add_i32 m0, s25, 0xc000
	s_nop 0
	global_load_lds_dwordx4 v150, s[80:81]
	s_mov_b64 s[80:81], s[6:7]
	s_add_i32 m0, s25, 0xe000
	s_nop 0
	global_load_lds_dwordx4 v153, s[80:81]
	s_waitcnt vmcnt(8)
	s_waitcnt lgkmcnt(0)
	s_barrier
	s_setprio 3
	v_mfma_f32_16x16x32_bf16 v[140:143], v[56:59], v[172:175], v[140:143]
	v_mfma_f32_16x16x32_bf16 v[136:139], v[68:71], v[172:175], v[136:139]
	v_mfma_f32_16x16x32_bf16 v[124:127], v[56:59], v[180:183], v[124:127]
	v_mfma_f32_16x16x32_bf16 v[120:123], v[68:71], v[180:183], v[120:123]
	v_mfma_f32_16x16x32_bf16 v[108:111], v[56:59], v[188:191], v[108:111]
	v_mfma_f32_16x16x32_bf16 v[104:107], v[68:71], v[188:191], v[104:107]
	v_mfma_f32_16x16x32_bf16 v[92:95], v[56:59], v[196:199], v[92:95]
	v_mfma_f32_16x16x32_bf16 v[88:91], v[68:71], v[196:199], v[88:91]
	v_mfma_f32_16x16x32_bf16 v[140:143], v[60:63], v[176:179], v[140:143]
	v_mfma_f32_16x16x32_bf16 v[136:139], v[76:79], v[176:179], v[136:139]
	v_mfma_f32_16x16x32_bf16 v[124:127], v[60:63], v[184:187], v[124:127]
	v_mfma_f32_16x16x32_bf16 v[120:123], v[76:79], v[184:187], v[120:123]
	v_mfma_f32_16x16x32_bf16 v[108:111], v[60:63], v[192:195], v[108:111]
	v_mfma_f32_16x16x32_bf16 v[104:107], v[76:79], v[192:195], v[104:107]
	v_mfma_f32_16x16x32_bf16 v[92:95], v[60:63], v[200:203], v[92:95]
	v_mfma_f32_16x16x32_bf16 v[88:91], v[76:79], v[200:203], v[88:91]
	v_mfma_f32_16x16x32_bf16 v[132:135], v[146:149], v[172:175], v[132:135]
	v_mfma_f32_16x16x32_bf16 v[128:131], v[164:167], v[172:175], v[128:131]
	v_mfma_f32_16x16x32_bf16 v[116:119], v[146:149], v[180:183], v[116:119]
	v_mfma_f32_16x16x32_bf16 v[112:115], v[164:167], v[180:183], v[112:115]
	v_mfma_f32_16x16x32_bf16 v[100:103], v[146:149], v[188:191], v[100:103]
	v_mfma_f32_16x16x32_bf16 v[96:99], v[164:167], v[188:191], v[96:99]
	v_mfma_f32_16x16x32_bf16 v[84:87], v[146:149], v[196:199], v[84:87]
	v_mfma_f32_16x16x32_bf16 v[80:83], v[164:167], v[196:199], v[80:83]
	v_mfma_f32_16x16x32_bf16 v[132:135], v[160:163], v[176:179], v[132:135]
	v_mfma_f32_16x16x32_bf16 v[128:131], v[168:171], v[176:179], v[128:131]
	v_mfma_f32_16x16x32_bf16 v[116:119], v[160:163], v[184:187], v[116:119]
	v_mfma_f32_16x16x32_bf16 v[112:115], v[168:171], v[184:187], v[112:115]
	v_mfma_f32_16x16x32_bf16 v[100:103], v[160:163], v[192:195], v[100:103]
	v_mfma_f32_16x16x32_bf16 v[96:99], v[168:171], v[192:195], v[96:99]
	v_mfma_f32_16x16x32_bf16 v[84:87], v[160:163], v[200:203], v[84:87]
	v_mfma_f32_16x16x32_bf16 v[80:83], v[168:171], v[200:203], v[80:83]
	s_setprio 0
	s_barrier
	v_mov_b32_e32 v150, v152
	s_mov_b64 s[80:81], s[74:75]
	s_add_i32 s69, s49, s23
	ds_read_b128 v[172:175], v157 offset:16384
	ds_read_b128 v[176:179], v157 offset:17408
	ds_read_b128 v[180:183], v157 offset:18432
	ds_read_b128 v[184:187], v157 offset:19456
	ds_read_b128 v[188:191], v157 offset:20480
	ds_read_b128 v[192:195], v157 offset:21504
	ds_read_b128 v[196:199], v157 offset:22528
	ds_read_b128 v[200:203], v157 offset:23552
	s_mov_b32 m0, s69
	s_nop 0
	global_load_lds_dwordx4 v150, s[80:81]
	s_add_u32 s80, s74, 0x20000
	s_addc_u32 s81, s75, 0
	s_add_i32 m0, s69, 0x2000
	s_nop 0
	global_load_lds_dwordx4 v152, s[80:81]
	s_add_u32 s80, s74, 0x40000
	s_addc_u32 s81, s75, 0
	s_add_i32 s69, s77, s23
	s_mov_b32 m0, s69
	s_nop 0
	global_load_lds_dwordx4 v152, s[80:81]
	s_add_u32 s80, s74, 0x60000
	s_addc_u32 s81, s75, 0
	s_add_i32 m0, s69, 0x2000
	s_nop 0
	global_load_lds_dwordx4 v152, s[80:81]
	s_mov_b64 s[80:81], s[70:71]
	s_mov_b32 m0, s25
	s_nop 0
	global_load_lds_dwordx4 v153, s[80:81]
	s_add_u32 s80, s70, 0x20000
	s_addc_u32 s81, s71, 0
	s_mov_b32 m0, s27
	s_nop 0
	global_load_lds_dwordx4 v153, s[80:81]
	s_waitcnt vmcnt(8)
	s_waitcnt lgkmcnt(0)
	s_barrier
	s_setprio 3
	v_mfma_f32_16x16x32_bf16 v[72:75], v[56:59], v[172:175], v[72:75]
	v_mfma_f32_16x16x32_bf16 v[64:67], v[68:71], v[172:175], v[64:67]
	v_mfma_f32_16x16x32_bf16 v[44:47], v[56:59], v[180:183], v[44:47]
	v_mfma_f32_16x16x32_bf16 v[40:43], v[68:71], v[180:183], v[40:43]
	v_mfma_f32_16x16x32_bf16 v[28:31], v[56:59], v[188:191], v[28:31]
	v_mfma_f32_16x16x32_bf16 v[24:27], v[68:71], v[188:191], v[24:27]
	v_mfma_f32_16x16x32_bf16 v[12:15], v[56:59], v[196:199], v[12:15]
	v_mfma_f32_16x16x32_bf16 v[8:11], v[68:71], v[196:199], v[8:11]
	v_mfma_f32_16x16x32_bf16 v[72:75], v[60:63], v[176:179], v[72:75]
	v_mfma_f32_16x16x32_bf16 v[64:67], v[76:79], v[176:179], v[64:67]
	v_mfma_f32_16x16x32_bf16 v[44:47], v[60:63], v[184:187], v[44:47]
	v_mfma_f32_16x16x32_bf16 v[40:43], v[76:79], v[184:187], v[40:43]
	v_mfma_f32_16x16x32_bf16 v[28:31], v[60:63], v[192:195], v[28:31]
	v_mfma_f32_16x16x32_bf16 v[24:27], v[76:79], v[192:195], v[24:27]
	v_mfma_f32_16x16x32_bf16 v[12:15], v[60:63], v[200:203], v[12:15]
	v_mfma_f32_16x16x32_bf16 v[8:11], v[76:79], v[200:203], v[8:11]
	v_mfma_f32_16x16x32_bf16 v[52:55], v[146:149], v[172:175], v[52:55]
	v_mfma_f32_16x16x32_bf16 v[48:51], v[164:167], v[172:175], v[48:51]
	v_mfma_f32_16x16x32_bf16 v[36:39], v[146:149], v[180:183], v[36:39]
	v_mfma_f32_16x16x32_bf16 v[32:35], v[164:167], v[180:183], v[32:35]
	v_mfma_f32_16x16x32_bf16 v[20:23], v[146:149], v[188:191], v[20:23]
	v_mfma_f32_16x16x32_bf16 v[16:19], v[164:167], v[188:191], v[16:19]
	v_mfma_f32_16x16x32_bf16 v[4:7], v[146:149], v[196:199], v[4:7]
	v_mfma_f32_16x16x32_bf16 v[0:3], v[164:167], v[196:199], v[0:3]
	v_mfma_f32_16x16x32_bf16 v[52:55], v[160:163], v[176:179], v[52:55]
	v_mfma_f32_16x16x32_bf16 v[48:51], v[168:171], v[176:179], v[48:51]
	v_mfma_f32_16x16x32_bf16 v[36:39], v[160:163], v[184:187], v[36:39]
	v_mfma_f32_16x16x32_bf16 v[32:35], v[168:171], v[184:187], v[32:35]
	v_mfma_f32_16x16x32_bf16 v[20:23], v[160:163], v[192:195], v[20:23]
	v_mfma_f32_16x16x32_bf16 v[16:19], v[168:171], v[192:195], v[16:19]
	v_mfma_f32_16x16x32_bf16 v[4:7], v[160:163], v[200:203], v[4:7]
	v_mfma_f32_16x16x32_bf16 v[0:3], v[168:171], v[200:203], v[0:3]
	s_setprio 0
	s_barrier
	s_add_i32 s69, 0, 0x18000
	s_add_i32 s82, 0, 0x1c000
	v_add_u32_e32 v76, s69, v154
	v_add_u32_e32 v150, s82, v154
	ds_read_b128 v[56:59], v76
	ds_read_b128 v[60:63], v76 offset:1024
	ds_read_b128 v[68:71], v76 offset:2048
	ds_read_b128 v[76:79], v76 offset:3072
	ds_read_b128 v[146:149], v150
	ds_read_b128 v[160:163], v150 offset:1024
	ds_read_b128 v[164:167], v150 offset:2048
	ds_read_b128 v[168:171], v150 offset:3072
	s_add_u32 s80, s70, 0x40000
	v_mov_b32_e32 v150, v153
	s_addc_u32 s81, s71, 0
	s_mov_b32 m0, s29
	ds_read_b128 v[172:175], v157 offset:32768
	ds_read_b128 v[176:179], v157 offset:33792
	ds_read_b128 v[180:183], v157 offset:34816
	ds_read_b128 v[184:187], v157 offset:35840
	ds_read_b128 v[188:191], v157 offset:36864
	ds_read_b128 v[192:195], v157 offset:37888
	ds_read_b128 v[196:199], v157 offset:38912
	ds_read_b128 v[200:203], v157 offset:39936
	s_nop 0
	global_load_lds_dwordx4 v150, s[80:81]
	s_add_u32 s80, s70, 0x60000
	s_addc_u32 s81, s71, 0
	s_mov_b32 m0, s31
	s_nop 0
	global_load_lds_dwordx4 v153, s[80:81]
	s_waitcnt vmcnt(8)
	s_waitcnt lgkmcnt(0)
	s_barrier
	s_setprio 3
	v_mfma_f32_16x16x32_bf16 v[140:143], v[56:59], v[172:175], v[140:143]
	v_mfma_f32_16x16x32_bf16 v[136:139], v[68:71], v[172:175], v[136:139]
	v_mfma_f32_16x16x32_bf16 v[124:127], v[56:59], v[180:183], v[124:127]
	v_mfma_f32_16x16x32_bf16 v[120:123], v[68:71], v[180:183], v[120:123]
	v_mfma_f32_16x16x32_bf16 v[108:111], v[56:59], v[188:191], v[108:111]
	v_mfma_f32_16x16x32_bf16 v[104:107], v[68:71], v[188:191], v[104:107]
	v_mfma_f32_16x16x32_bf16 v[92:95], v[56:59], v[196:199], v[92:95]
	v_mfma_f32_16x16x32_bf16 v[88:91], v[68:71], v[196:199], v[88:91]
	v_mfma_f32_16x16x32_bf16 v[140:143], v[60:63], v[176:179], v[140:143]
	v_mfma_f32_16x16x32_bf16 v[136:139], v[76:79], v[176:179], v[136:139]
	v_mfma_f32_16x16x32_bf16 v[124:127], v[60:63], v[184:187], v[124:127]
	v_mfma_f32_16x16x32_bf16 v[120:123], v[76:79], v[184:187], v[120:123]
	v_mfma_f32_16x16x32_bf16 v[108:111], v[60:63], v[192:195], v[108:111]
	v_mfma_f32_16x16x32_bf16 v[104:107], v[76:79], v[192:195], v[104:107]
	v_mfma_f32_16x16x32_bf16 v[92:95], v[60:63], v[200:203], v[92:95]
	v_mfma_f32_16x16x32_bf16 v[88:91], v[76:79], v[200:203], v[88:91]
	v_mfma_f32_16x16x32_bf16 v[132:135], v[146:149], v[172:175], v[132:135]
	v_mfma_f32_16x16x32_bf16 v[128:131], v[164:167], v[172:175], v[128:131]
	v_mfma_f32_16x16x32_bf16 v[116:119], v[146:149], v[180:183], v[116:119]
	v_mfma_f32_16x16x32_bf16 v[112:115], v[164:167], v[180:183], v[112:115]
	v_mfma_f32_16x16x32_bf16 v[100:103], v[146:149], v[188:191], v[100:103]
	v_mfma_f32_16x16x32_bf16 v[96:99], v[164:167], v[188:191], v[96:99]
	v_mfma_f32_16x16x32_bf16 v[84:87], v[146:149], v[196:199], v[84:87]
	v_mfma_f32_16x16x32_bf16 v[80:83], v[164:167], v[196:199], v[80:83]
	v_mfma_f32_16x16x32_bf16 v[132:135], v[160:163], v[176:179], v[132:135]
	v_mfma_f32_16x16x32_bf16 v[128:131], v[168:171], v[176:179], v[128:131]
	v_mfma_f32_16x16x32_bf16 v[116:119], v[160:163], v[184:187], v[116:119]
	v_mfma_f32_16x16x32_bf16 v[112:115], v[168:171], v[184:187], v[112:115]
	v_mfma_f32_16x16x32_bf16 v[100:103], v[160:163], v[192:195], v[100:103]
	v_mfma_f32_16x16x32_bf16 v[96:99], v[168:171], v[192:195], v[96:99]
	v_mfma_f32_16x16x32_bf16 v[84:87], v[160:163], v[200:203], v[84:87]
	v_mfma_f32_16x16x32_bf16 v[80:83], v[168:171], v[200:203], v[80:83]
	s_setprio 0
	s_barrier
	s_add_u32 s80, s74, 0x80
	s_addc_u32 s81, s75, 0
	v_mov_b32_e32 v150, v152
	s_add_i32 s69, s69, s23
	ds_read_b128 v[172:175], v157 offset:49152
	ds_read_b128 v[176:179], v157 offset:50176
	ds_read_b128 v[180:183], v157 offset:51200
	ds_read_b128 v[184:187], v157 offset:52224
	ds_read_b128 v[188:191], v157 offset:53248
	ds_read_b128 v[192:195], v157 offset:54272
	ds_read_b128 v[196:199], v157 offset:55296
	ds_read_b128 v[200:203], v157 offset:56320
	s_mov_b32 m0, s69
	s_nop 0
	global_load_lds_dwordx4 v150, s[80:81]
	s_add_u32 s80, s74, 0x20080
	s_addc_u32 s81, s75, 0
	s_add_i32 m0, s69, 0x2000
	s_nop 0
	global_load_lds_dwordx4 v152, s[80:81]
	s_add_u32 s80, s74, 0x40080
	s_addc_u32 s81, s75, 0
	s_add_i32 s69, s82, s23
	s_mov_b32 m0, s69
	s_add_u32 s74, s74, 0x60080
	global_load_lds_dwordx4 v152, s[80:81]
	s_addc_u32 s75, s75, 0
	s_add_i32 m0, s69, 0x2000
	s_add_u32 s70, s70, 0x20080
	global_load_lds_dwordx4 v152, s[74:75]
	s_mov_b32 m0, s43
	s_addc_u32 s71, s71, 0
	global_load_lds_dwordx4 v153, s[72:73]
	s_mov_b32 m0, s45
	s_nop 0
	global_load_lds_dwordx4 v153, s[70:71]
	s_waitcnt vmcnt(8)
	s_waitcnt lgkmcnt(0)
	s_barrier
	s_setprio 3
	v_mfma_f32_16x16x32_bf16 v[72:75], v[56:59], v[172:175], v[72:75]
	v_mfma_f32_16x16x32_bf16 v[64:67], v[68:71], v[172:175], v[64:67]
	v_mfma_f32_16x16x32_bf16 v[44:47], v[56:59], v[180:183], v[44:47]
	v_mfma_f32_16x16x32_bf16 v[40:43], v[68:71], v[180:183], v[40:43]
	v_mfma_f32_16x16x32_bf16 v[28:31], v[56:59], v[188:191], v[28:31]
	v_mfma_f32_16x16x32_bf16 v[24:27], v[68:71], v[188:191], v[24:27]
	v_mfma_f32_16x16x32_bf16 v[12:15], v[56:59], v[196:199], v[12:15]
	v_mfma_f32_16x16x32_bf16 v[8:11], v[68:71], v[196:199], v[8:11]
	v_mfma_f32_16x16x32_bf16 v[72:75], v[60:63], v[176:179], v[72:75]
	v_mfma_f32_16x16x32_bf16 v[64:67], v[76:79], v[176:179], v[64:67]
	v_mfma_f32_16x16x32_bf16 v[44:47], v[60:63], v[184:187], v[44:47]
	v_mfma_f32_16x16x32_bf16 v[40:43], v[76:79], v[184:187], v[40:43]
	v_mfma_f32_16x16x32_bf16 v[28:31], v[60:63], v[192:195], v[28:31]
	v_mfma_f32_16x16x32_bf16 v[24:27], v[76:79], v[192:195], v[24:27]
	v_mfma_f32_16x16x32_bf16 v[12:15], v[60:63], v[200:203], v[12:15]
	v_mfma_f32_16x16x32_bf16 v[8:11], v[76:79], v[200:203], v[8:11]
	v_mfma_f32_16x16x32_bf16 v[52:55], v[146:149], v[172:175], v[52:55]
	v_mfma_f32_16x16x32_bf16 v[48:51], v[164:167], v[172:175], v[48:51]
	v_mfma_f32_16x16x32_bf16 v[36:39], v[146:149], v[180:183], v[36:39]
	v_mfma_f32_16x16x32_bf16 v[32:35], v[164:167], v[180:183], v[32:35]
	v_mfma_f32_16x16x32_bf16 v[20:23], v[146:149], v[188:191], v[20:23]
	v_mfma_f32_16x16x32_bf16 v[16:19], v[164:167], v[188:191], v[16:19]
	v_mfma_f32_16x16x32_bf16 v[4:7], v[146:149], v[196:199], v[4:7]
	v_mfma_f32_16x16x32_bf16 v[0:3], v[164:167], v[196:199], v[0:3]
	v_mfma_f32_16x16x32_bf16 v[52:55], v[160:163], v[176:179], v[52:55]
	v_mfma_f32_16x16x32_bf16 v[48:51], v[168:171], v[176:179], v[48:51]
	v_mfma_f32_16x16x32_bf16 v[36:39], v[160:163], v[184:187], v[36:39]
	v_mfma_f32_16x16x32_bf16 v[32:35], v[168:171], v[184:187], v[32:35]
	v_mfma_f32_16x16x32_bf16 v[20:23], v[160:163], v[192:195], v[20:23]
	v_mfma_f32_16x16x32_bf16 v[16:19], v[168:171], v[192:195], v[16:19]
	v_mfma_f32_16x16x32_bf16 v[4:7], v[160:163], v[200:203], v[4:7]
	v_mfma_f32_16x16x32_bf16 v[0:3], v[168:171], v[200:203], v[0:3]
	s_setprio 0
	s_barrier
	s_add_i32 s53, s53, 2
	s_add_u32 s5, s5, 0x100
	s_addc_u32 s51, s51, 0
	s_add_u32 s6, s6, 0x100
	s_addc_u32 s7, s7, 0
	s_cmp_gt_u32 s53, 13
	s_cbranch_scc0 .LBB0_1769
	s_mov_b64 s[46:47], s[94:95]
	s_and_b64 vcc, exec, s[18:19]
	s_cbranch_vccz .LBB0_1772
	s_barrier

.LBB0_2123:
	s_cmp_lt_i32 s48, 12
	s_cselect_b64 s[10:11], -1, 0
	s_cmp_gt_i32 s48, 11
	s_cselect_b64 s[4:5], -1, 0
	s_and_b64 s[0:1], s[10:11], s[6:7]
	s_andn2_b64 vcc, exec, s[0:1]
	s_cbranch_vccnz .LBB0_2144
	s_getreg_b32 s0, hwreg(HW_REG_HW_ID, 0, 6)
	s_lshl_b32 s0, s0, 2
	s_and_b32 s0, s0, 0xfc
	s_add_i32 s0, s0, 0
	s_add_i32 s0, s0, 0x25c00
	v_mov_b32_e32 v0, s0
	ds_read_b32 v0, v0
	s_cmpk_gt_i32 s2, 0xff
	s_waitcnt lgkmcnt(0)
	v_readfirstlane_b32 s0, v0
	v_mbcnt_lo_u32_b32 v0, -1, 0
	v_mbcnt_hi_u32_b32 v0, -1, v0
	s_nop 1
	v_lshl_add_u32 v0, s0, 6, v0
	s_nop 0
	v_readfirstlane_b32 s1, v0
	s_cbranch_scc1 .LBB0_2144
	v_bfe_i32 v3, v0, 27, 1
	v_lshlrev_b32_e32 v1, 4, v0
	v_lshrrev_b32_e32 v3, 22, v3
	v_add_u32_e32 v3, v1, v3
	v_and_b32_e32 v3, 0xfffffc00, v3
	v_ashrrev_i32_e32 v2, 31, v0
	v_sub_u32_e32 v1, v1, v3
	v_lshrrev_b32_e32 v2, 26, v2
	v_lshrrev_b32_e32 v3, 4, v1
	v_add_u32_e32 v2, v0, v2
	v_bitop3_b32 v3, v3, v1, 32 bitop3:0x6c
	v_ashrrev_i32_e32 v1, 31, v1
	s_add_u32 s3, s78, 0x1a500000
	v_ashrrev_i32_e32 v2, 6, v2
	v_lshrrev_b32_e32 v1, 26, v1
	s_addc_u32 s15, s79, 0
	v_lshlrev_b32_e32 v4, 3, v2
	v_add_u32_e32 v1, v3, v1
	s_add_u32 s17, s78, 0x2100000
	v_and_b32_e32 v4, -16, v4
	v_ashrrev_i32_e32 v1, 6, v1
	s_addc_u32 s38, s79, 0
	v_add_u32_e32 v4, v1, v4
	v_mul_i32_i24_e32 v5, 64, v1
	v_and_b32_e32 v1, 3, v1
	s_mov_b32 s0, 0x1fffe0
	s_ashr_i32 s40, s2, 31
	v_and_or_b32 v1, v4, s0, v1
	s_lshr_b32 s0, s40, 29
	s_add_i32 s0, s2, s0
	s_ashr_i32 s6, s0, 3
	s_and_b32 s0, s0, -8
	s_ashr_i32 s12, s1, 6
	s_sub_i32 s0, s2, s0
	s_ashr_i32 s13, s1, 8
	s_lshl_b32 s39, s12, 10
	s_lshl_b32 s14, s0, 5
	s_mul_i32 s7, s0, 33
	s_cmp_lt_i32 s0, 0
	s_cselect_b32 s0, s7, s14
	s_add_i32 s0, s0, s6
	s_ashr_i32 s6, s0, 31
	s_lshr_b32 s6, s6, 27
	s_add_i32 s6, s0, s6
	s_ashr_i32 s7, s6, 5
	s_and_b32 s6, s6, 0xffe0
	s_sub_i32 s6, s0, s6
	s_bfe_i32 s0, s6, 0x80000
	s_bfe_u32 s0, s0, 0x3000c
	s_add_i32 s14, s6, s0
	s_bfe_i32 s0, s14, 0x80000
	s_and_b32 s14, s14, 0xf8
	s_sub_i32 s6, s6, s14
	s_lshl_b32 s7, s7, 3
	s_sext_i32_i8 s6, s6
	s_add_i32 s26, s7, s6
	s_sext_i32_i16 s0, s0
	s_ashr_i32 s27, s26, 31
	s_lshr_b32 s0, s0, 3
	s_lshl_b64 s[6:7], s[26:27], 19
	v_sub_u32_e32 v3, v3, v5
	v_mov_b32_e32 v5, 1
	s_add_u32 s28, s3, s6
	v_lshlrev_b32_e32 v2, 5, v2
	v_ashrrev_i16_sdwa v3, v5, sext(v3) dst_sel:DWORD dst_unused:UNUSED_PAD src0_sel:DWORD src1_sel:BYTE_0
	v_lshlrev_b32_e32 v5, 1, v4
	v_lshrrev_b32_e32 v6, 2, v4
	s_addc_u32 s29, s15, s7
	s_bfe_i64 s[6:7], s[0:1], 0x100000
	v_and_b32_e32 v2, 32, v2
	v_bfe_i32 v3, v3, 0, 16
	v_and_b32_e32 v5, 24, v5
	v_and_b32_e32 v6, 4, v6
	s_lshl_b64 s[6:7], s[6:7], 19
	v_or3_b32 v1, v1, v6, v5
	v_add_lshl_u32 v2, v2, v3, 1
	s_add_u32 s30, s17, s6
	v_lshl_add_u32 v174, v1, 11, v2
	s_addc_u32 s31, s38, s7
	s_add_i32 s27, s39, 0
	s_mov_b64 s[6:7], s[30:31]
	s_add_i32 m0, s27, 0x10000
	v_lshl_add_u32 v175, v4, 11, v2
	global_load_lds_dwordx4 v174, s[6:7]
	s_add_u32 s6, s30, 0x20000
	s_addc_u32 s7, s31, 0
	s_add_i32 m0, s27, 0x12000
	s_nop 0
	global_load_lds_dwordx4 v174, s[6:7]
	s_add_i32 m0, s27, 0x14000
	s_add_u32 s6, s30, 0x40000
	s_addc_u32 s7, s31, 0
	s_nop 0
	global_load_lds_dwordx4 v174, s[6:7]
	s_add_u32 s6, s30, 0x60000
	s_addc_u32 s7, s31, 0
	s_add_i32 m0, s27, 0x16000
	s_nop 0
	global_load_lds_dwordx4 v174, s[6:7]
	s_mov_b64 s[6:7], s[28:29]
	s_mov_b32 m0, s27
	s_nop 0
	global_load_lds_dwordx4 v175, s[6:7]
	s_add_u32 s6, s28, 0x20000
	s_addc_u32 s7, s29, 0
	s_add_i32 s41, s27, 0x2000
	s_mov_b32 m0, s41
	s_add_i32 s42, s27, 0x4000
	global_load_lds_dwordx4 v175, s[6:7]
	s_add_u32 s6, s28, 0x40000
	s_addc_u32 s7, s29, 0
	s_mov_b32 m0, s42
	s_nop 0
	global_load_lds_dwordx4 v175, s[6:7]
	s_add_u32 s6, s28, 0x60000
	s_addc_u32 s7, s29, 0
	s_add_i32 s43, s27, 0x6000
	s_mov_b32 m0, s43
	s_cmp_eq_u32 s13, 1
	global_load_lds_dwordx4 v175, s[6:7]
	s_cselect_b64 s[6:7], -1, 0
	s_cmp_lg_u32 s13, 1
	s_cbranch_scc1 .LBB0_2127
	s_barrier
.LBB0_2127:
	s_add_u32 s44, s78, 0x4c000
	s_addc_u32 s45, s79, 0
	s_add_u32 s48, s78, 0x4e000
	s_addc_u32 s49, s79, 0
	s_lshl_b32 s12, s12, 5
	s_and_b32 s52, s12, 0x60
	s_ashr_i32 s50, s33, 31
	s_lshl_b32 s51, s13, 6
	s_lshl_b32 s14, s13, 13
	s_lshl_b32 s16, s52, 7
	s_add_u32 s12, s30, 0x80
	s_addc_u32 s13, s31, 0
	s_waitcnt vmcnt(2)
	s_barrier
	s_add_i32 m0, s27, 0x18000
	s_sext_i32_i8 s64, s0
	global_load_lds_dwordx4 v174, s[12:13]
	s_add_u32 s12, s30, 0x20080
	s_addc_u32 s13, s31, 0
	s_add_i32 m0, s27, 0x1a000
	v_lshlrev_b32_e32 v2, 6, v0
	global_load_lds_dwordx4 v174, s[12:13]
	s_add_u32 s12, s28, 0x80
	s_addc_u32 s13, s29, 0
	s_add_i32 s53, s27, 0x8000
	s_mov_b32 m0, s53
	s_movk_i32 s0, 0x3c0
	global_load_lds_dwordx4 v175, s[12:13]
	s_add_u32 s12, s28, 0x20080
	s_addc_u32 s13, s29, 0
	s_add_i32 s54, s27, 0xa000
	s_mov_b32 m0, s54
	s_mov_b32 s55, 0
	global_load_lds_dwordx4 v175, s[12:13]
	s_add_i32 m0, s27, 0x1c000
	s_add_u32 s12, s30, 0x40080
	s_addc_u32 s13, s31, 0
	v_mov_b64_e32 v[144:145], 0x100
	global_load_lds_dwordx4 v174, s[12:13]
	s_add_u32 s12, s30, 0x60080
	s_addc_u32 s13, s31, 0
	s_add_i32 m0, s27, 0x1e000
	s_cmpk_lt_u32 s1, 0x100
	global_load_lds_dwordx4 v174, s[12:13]
	v_and_b32_e32 v1, 48, v0
	v_lshlrev_b32_e32 v0, 2, v0
	v_and_or_b32 v1, v2, s0, v1
	v_and_b32_e32 v0, 32, v0
	s_waitcnt vmcnt(6)
	v_bitop3_b32 v2, v1, s14, v0 bitop3:0xde
	v_bitop3_b32 v176, s16, v1, v0 bitop3:0xf6
	s_cselect_b64 s[12:13], -1, 0
	s_add_i32 s60, 0, 0x10000
	s_add_i32 s61, 0, 0x14000
	v_add_u32_e32 v177, s60, v176
	v_add_u32_e32 v178, s61, v176
	v_add_u32_e32 v179, 0, v2
	s_mov_b32 s14, 0x3fb504f3
	s_mov_b32 s16, 0x3b000000
	s_barrier
	s_branch .LBB0_2130

.LBB0_2137:
	ds_read_b128 v[8:11], v177
	ds_read_b128 v[12:15], v177 offset:1024
	ds_read_b128 v[136:139], v177 offset:2048
	ds_read_b128 v[140:143], v177 offset:3072
	ds_read_b128 v[146:149], v178
	ds_read_b128 v[150:153], v178 offset:1024
	ds_read_b128 v[154:157], v178 offset:2048
	ds_read_b128 v[158:161], v178 offset:3072
	s_add_u32 s30, s28, 0xfffa0080
	s_addc_u32 s31, s29, -1
	s_cmp_eq_u32 s65, 12
	s_cselect_b32 s30, s22, s30
	s_cselect_b32 s31, s23, s31
	s_cselect_b32 s36, s24, s19
	s_cselect_b32 s37, s25, s21
	s_add_u32 s34, s30, 0x80
	s_addc_u32 s35, s31, 0
	s_add_u32 s68, s28, 0xfffe0000
	v_mov_b32_e32 v170, v175
	s_addc_u32 s69, s29, -1
	ds_read_b128 v[162:165], v179
	ds_read_b128 v[166:169], v179 offset:1024
	ds_read_b128 v[180:183], v179 offset:2048
	ds_read_b128 v[184:187], v179 offset:3072
	ds_read_b128 v[188:191], v179 offset:4096
	ds_read_b128 v[192:195], v179 offset:5120
	ds_read_b128 v[196:199], v179 offset:6144
	ds_read_b128 v[200:203], v179 offset:7168
	s_add_i32 m0, s27, 0xc000
	s_nop 0
	global_load_lds_dwordx4 v170, s[68:69]
	s_mov_b64 s[68:69], s[28:29]
	s_add_i32 m0, s27, 0xe000
	s_nop 0
	global_load_lds_dwordx4 v175, s[68:69]
	s_waitcnt vmcnt(8)
	s_waitcnt lgkmcnt(0)
	s_barrier
	s_setprio 3
	v_mfma_f32_16x16x128_f8f6f4 v[132:135], v[8:15], v[162:169], v[132:135]
	v_mfma_f32_16x16x128_f8f6f4 v[128:131], v[136:143], v[162:169], v[128:131]
	v_mfma_f32_16x16x128_f8f6f4 v[116:119], v[8:15], v[180:187], v[116:119]
	v_mfma_f32_16x16x128_f8f6f4 v[112:115], v[136:143], v[180:187], v[112:115]
	v_mfma_f32_16x16x128_f8f6f4 v[100:103], v[8:15], v[188:195], v[100:103]
	v_mfma_f32_16x16x128_f8f6f4 v[96:99], v[136:143], v[188:195], v[96:99]
	v_mfma_f32_16x16x128_f8f6f4 v[84:87], v[8:15], v[196:203], v[84:87]
	v_mfma_f32_16x16x128_f8f6f4 v[80:83], v[136:143], v[196:203], v[80:83]
	v_mfma_f32_16x16x128_f8f6f4 v[124:127], v[146:153], v[162:169], v[124:127]
	v_mfma_f32_16x16x128_f8f6f4 v[120:123], v[154:161], v[162:169], v[120:123]
	v_mfma_f32_16x16x128_f8f6f4 v[108:111], v[146:153], v[180:187], v[108:111]
	v_mfma_f32_16x16x128_f8f6f4 v[104:107], v[154:161], v[180:187], v[104:107]
	v_mfma_f32_16x16x128_f8f6f4 v[92:95], v[146:153], v[188:195], v[92:95]
	v_mfma_f32_16x16x128_f8f6f4 v[88:91], v[154:161], v[188:195], v[88:91]
	v_mfma_f32_16x16x128_f8f6f4 v[76:79], v[146:153], v[196:203], v[76:79]
	v_mfma_f32_16x16x128_f8f6f4 v[72:75], v[154:161], v[196:203], v[72:75]
	s_setprio 0
	s_barrier
	v_mov_b32_e32 v170, v174
	s_mov_b64 s[68:69], s[36:37]
	s_add_i32 s70, s60, s39
	ds_read_b128 v[162:165], v179 offset:16384
	ds_read_b128 v[166:169], v179 offset:17408
	ds_read_b128 v[180:183], v179 offset:18432
	ds_read_b128 v[184:187], v179 offset:19456
	ds_read_b128 v[188:191], v179 offset:20480
	ds_read_b128 v[192:195], v179 offset:21504
	ds_read_b128 v[196:199], v179 offset:22528
	ds_read_b128 v[200:203], v179 offset:23552
	s_mov_b32 m0, s70
	s_nop 0
	global_load_lds_dwordx4 v170, s[68:69]
	s_add_u32 s68, s36, 0x20000
	s_addc_u32 s69, s37, 0
	s_add_i32 m0, s70, 0x2000
	s_nop 0
	global_load_lds_dwordx4 v174, s[68:69]
	s_add_u32 s68, s36, 0x40000
	s_addc_u32 s69, s37, 0
	s_add_i32 s70, s61, s39
	s_mov_b32 m0, s70
	s_nop 0
	global_load_lds_dwordx4 v174, s[68:69]
	s_add_u32 s68, s36, 0x60000
	s_addc_u32 s69, s37, 0
	s_add_i32 m0, s70, 0x2000
	s_nop 0
	global_load_lds_dwordx4 v174, s[68:69]
	s_mov_b64 s[68:69], s[30:31]
	s_mov_b32 m0, s27
	s_nop 0
	global_load_lds_dwordx4 v175, s[68:69]
	s_add_u32 s68, s30, 0x20000
	s_addc_u32 s69, s31, 0
	s_mov_b32 m0, s41
	s_nop 0
	global_load_lds_dwordx4 v175, s[68:69]
	s_waitcnt vmcnt(8)
	s_waitcnt lgkmcnt(0)
	s_barrier
	s_setprio 3
	v_mfma_f32_16x16x128_f8f6f4 v[68:71], v[8:15], v[162:169], v[68:71]
	v_mfma_f32_16x16x128_f8f6f4 v[64:67], v[136:143], v[162:169], v[64:67]
	v_mfma_f32_16x16x128_f8f6f4 v[52:55], v[8:15], v[180:187], v[52:55]
	v_mfma_f32_16x16x128_f8f6f4 v[48:51], v[136:143], v[180:187], v[48:51]
	v_mfma_f32_16x16x128_f8f6f4 v[36:39], v[8:15], v[188:195], v[36:39]
	v_mfma_f32_16x16x128_f8f6f4 v[32:35], v[136:143], v[188:195], v[32:35]
	v_mfma_f32_16x16x128_f8f6f4 v[20:23], v[8:15], v[196:203], v[20:23]
	v_mfma_f32_16x16x128_f8f6f4 v[16:19], v[136:143], v[196:203], v[16:19]
	v_mfma_f32_16x16x128_f8f6f4 v[60:63], v[146:153], v[162:169], v[60:63]
	v_mfma_f32_16x16x128_f8f6f4 v[56:59], v[154:161], v[162:169], v[56:59]
	v_mfma_f32_16x16x128_f8f6f4 v[44:47], v[146:153], v[180:187], v[44:47]
	v_mfma_f32_16x16x128_f8f6f4 v[40:43], v[154:161], v[180:187], v[40:43]
	v_mfma_f32_16x16x128_f8f6f4 v[28:31], v[146:153], v[188:195], v[28:31]
	v_mfma_f32_16x16x128_f8f6f4 v[24:27], v[154:161], v[188:195], v[24:27]
	v_mfma_f32_16x16x128_f8f6f4 v[136:139], v[146:153], v[196:203], v[4:7]
	v_mfma_f32_16x16x128_f8f6f4 v[140:143], v[154:161], v[196:203], v[0:3]
	s_setprio 0
	s_barrier
	s_add_i32 s70, 0, 0x18000
	s_add_i32 s71, 0, 0x1c000
	s_nop 2
	v_add_u32_e32 v0, s70, v176
	v_add_u32_e32 v12, s71, v176
	ds_read_b128 v[146:149], v0
	ds_read_b128 v[150:153], v0 offset:1024
	ds_read_b128 v[154:157], v0 offset:2048
	ds_read_b128 v[158:161], v0 offset:3072
	ds_read_b128 v[0:3], v12
	ds_read_b128 v[4:7], v12 offset:1024
	ds_read_b128 v[8:11], v12 offset:2048
	ds_read_b128 v[12:15], v12 offset:3072
	s_add_u32 s68, s30, 0x40000
	v_mov_b32_e32 v170, v175
	s_addc_u32 s69, s31, 0
	s_mov_b32 m0, s42
	ds_read_b128 v[162:165], v179 offset:32768
	ds_read_b128 v[166:169], v179 offset:33792
	ds_read_b128 v[180:183], v179 offset:34816
	ds_read_b128 v[184:187], v179 offset:35840
	ds_read_b128 v[188:191], v179 offset:36864
	ds_read_b128 v[192:195], v179 offset:37888
	ds_read_b128 v[196:199], v179 offset:38912
	ds_read_b128 v[200:203], v179 offset:39936
	s_nop 0
	global_load_lds_dwordx4 v170, s[68:69]
	s_add_u32 s68, s30, 0x60000
	s_addc_u32 s69, s31, 0
	s_mov_b32 m0, s43
	s_nop 0
	global_load_lds_dwordx4 v175, s[68:69]
	s_waitcnt vmcnt(8)
	s_waitcnt lgkmcnt(0)
	s_barrier
	s_setprio 3
	v_mfma_f32_16x16x128_f8f6f4 v[132:135], v[146:153], v[162:169], v[132:135]
	v_mfma_f32_16x16x128_f8f6f4 v[128:131], v[154:161], v[162:169], v[128:131]
	v_mfma_f32_16x16x128_f8f6f4 v[116:119], v[146:153], v[180:187], v[116:119]
	v_mfma_f32_16x16x128_f8f6f4 v[112:115], v[154:161], v[180:187], v[112:115]
	v_mfma_f32_16x16x128_f8f6f4 v[100:103], v[146:153], v[188:195], v[100:103]
	v_mfma_f32_16x16x128_f8f6f4 v[96:99], v[154:161], v[188:195], v[96:99]
	v_mfma_f32_16x16x128_f8f6f4 v[84:87], v[146:153], v[196:203], v[84:87]
	v_mfma_f32_16x16x128_f8f6f4 v[80:83], v[154:161], v[196:203], v[80:83]
	v_mfma_f32_16x16x128_f8f6f4 v[124:127], v[0:7], v[162:169], v[124:127]
	v_mfma_f32_16x16x128_f8f6f4 v[120:123], v[8:15], v[162:169], v[120:123]
	v_mfma_f32_16x16x128_f8f6f4 v[108:111], v[0:7], v[180:187], v[108:111]
	v_mfma_f32_16x16x128_f8f6f4 v[104:107], v[8:15], v[180:187], v[104:107]
	v_mfma_f32_16x16x128_f8f6f4 v[92:95], v[0:7], v[188:195], v[92:95]
	v_mfma_f32_16x16x128_f8f6f4 v[88:91], v[8:15], v[188:195], v[88:91]
	v_mfma_f32_16x16x128_f8f6f4 v[76:79], v[0:7], v[196:203], v[76:79]
	v_mfma_f32_16x16x128_f8f6f4 v[72:75], v[8:15], v[196:203], v[72:75]
	s_setprio 0
	s_barrier
	s_add_u32 s68, s36, 0x80
	s_addc_u32 s69, s37, 0
	v_mov_b32_e32 v170, v174
	s_add_i32 s70, s70, s39
	ds_read_b128 v[162:165], v179 offset:49152
	ds_read_b128 v[166:169], v179 offset:50176
	ds_read_b128 v[180:183], v179 offset:51200
	ds_read_b128 v[184:187], v179 offset:52224
	ds_read_b128 v[188:191], v179 offset:53248
	ds_read_b128 v[192:195], v179 offset:54272
	ds_read_b128 v[196:199], v179 offset:55296
	ds_read_b128 v[200:203], v179 offset:56320
	s_mov_b32 m0, s70
	s_nop 0
	global_load_lds_dwordx4 v170, s[68:69]
	s_add_u32 s68, s36, 0x20080
	s_addc_u32 s69, s37, 0
	s_add_i32 m0, s70, 0x2000
	s_nop 0
	global_load_lds_dwordx4 v174, s[68:69]
	s_add_u32 s68, s36, 0x40080
	s_addc_u32 s69, s37, 0
	s_add_i32 s70, s71, s39
	s_mov_b32 m0, s70
	s_add_u32 s36, s36, 0x60080
	global_load_lds_dwordx4 v174, s[68:69]
	s_addc_u32 s37, s37, 0
	s_add_i32 m0, s70, 0x2000
	s_add_u32 s30, s30, 0x20080
	global_load_lds_dwordx4 v174, s[36:37]
	s_mov_b32 m0, s53
	s_addc_u32 s31, s31, 0
	global_load_lds_dwordx4 v175, s[34:35]
	s_mov_b32 m0, s54
	s_nop 0
	global_load_lds_dwordx4 v175, s[30:31]
	s_waitcnt vmcnt(8)
	s_waitcnt lgkmcnt(0)
	s_barrier
	s_setprio 3
	v_mfma_f32_16x16x128_f8f6f4 v[68:71], v[146:153], v[162:169], v[68:71]
	v_mfma_f32_16x16x128_f8f6f4 v[64:67], v[154:161], v[162:169], v[64:67]
	v_mfma_f32_16x16x128_f8f6f4 v[52:55], v[146:153], v[180:187], v[52:55]
	v_mfma_f32_16x16x128_f8f6f4 v[48:51], v[154:161], v[180:187], v[48:51]
	v_mfma_f32_16x16x128_f8f6f4 v[36:39], v[146:153], v[188:195], v[36:39]
	v_mfma_f32_16x16x128_f8f6f4 v[32:35], v[154:161], v[188:195], v[32:35]
	v_mfma_f32_16x16x128_f8f6f4 v[20:23], v[146:153], v[196:203], v[20:23]
	v_mfma_f32_16x16x128_f8f6f4 v[16:19], v[154:161], v[196:203], v[16:19]
	v_mfma_f32_16x16x128_f8f6f4 v[60:63], v[0:7], v[162:169], v[60:63]
	v_mfma_f32_16x16x128_f8f6f4 v[56:59], v[8:15], v[162:169], v[56:59]
	v_mfma_f32_16x16x128_f8f6f4 v[44:47], v[0:7], v[180:187], v[44:47]
	v_mfma_f32_16x16x128_f8f6f4 v[40:43], v[8:15], v[180:187], v[40:43]
	v_mfma_f32_16x16x128_f8f6f4 v[28:31], v[0:7], v[188:195], v[28:31]
	v_mfma_f32_16x16x128_f8f6f4 v[24:27], v[8:15], v[188:195], v[24:27]
	v_mfma_f32_16x16x128_f8f6f4 v[4:7], v[0:7], v[196:203], v[136:139]
	v_mfma_f32_16x16x128_f8f6f4 v[0:3], v[8:15], v[196:203], v[140:143]
	s_setprio 0
	s_barrier
	s_add_i32 s65, s65, 2
	s_add_u32 s19, s19, 0x100
	s_addc_u32 s21, s21, 0
	s_add_u32 s28, s28, 0x100
	s_addc_u32 s29, s29, 0
	s_cmp_gt_u32 s65, 13
	s_cbranch_scc0 .LBB0_2137
	s_and_b64 vcc, exec, s[12:13]
	s_cbranch_vccz .LBB0_2140
	s_barrier

.LBB0_2161:
	s_add_i32 s3, 0, 0x24808
	v_mov_b32_e32 v3, s3
	ds_read_b32 v4, v3
	s_mov_b64 s[0:1], exec
	v_mbcnt_lo_u32_b32 v2, s0, 0
	v_mbcnt_hi_u32_b32 v2, s1, v2
	v_cmp_eq_u32_e32 vcc, 0, v2
	s_waitcnt lgkmcnt(0)
	v_add_u32_e32 v4, 1, v4
	v_mov_b32_e32 v7, v4
	ds_write_b32 v3, v4
	s_and_saveexec_b64 s[10:11], vcc
	s_cbranch_execz .LBB0_2163
	v_readlane_b32 s3, v249, 34
	s_lshl_b32 s3, s3, 8
	s_add_u32 s14, s94, s3
	s_addc_u32 s15, s95, 0
	s_bcnt1_i32_b64 s0, s[0:1]
	v_mov_b32_e32 v3, 0x1000
	v_mov_b32_e32 v4, s0
	global_atomic_add v3, v3, v4, s[14:15] offset:1024 sc0

.LBB0_2169:
	s_or_b64 exec, exec, s[10:11]
	s_branch .LBB0_2173
	v_cvt_f32_u32_e32 v3, v0
	s_waitcnt vmcnt(0)
	v_readfirstlane_b32 s0, v2
	v_sub_u32_e32 v2, 0, v0
	v_rcp_iflag_f32_e32 v3, v3
	v_add_u32_e32 v1, s0, v1
	v_mul_f32_e32 v3, 0x4f7ffffe, v3
	v_cvt_u32_f32_e32 v3, v3
	v_mul_lo_u32 v2, v2, v3
	v_mul_hi_u32 v2, v3, v2
	v_add_u32_e32 v2, v3, v2
	v_mul_hi_u32 v2, v1, v2
	v_mul_lo_u32 v3, v2, v0
	v_sub_u32_e32 v3, v1, v3
	v_add_u32_e32 v4, 1, v2
	v_cmp_ge_u32_e32 vcc, v3, v0
	v_add_u32_e32 v1, 1, v1
	s_nop 0
	v_cndmask_b32_e32 v2, v2, v4, vcc
	v_sub_u32_e32 v4, v3, v0
	v_cndmask_b32_e32 v3, v3, v4, vcc
	v_add_u32_e32 v4, 1, v2
	v_cmp_ge_u32_e32 vcc, v3, v0
	s_nop 1
	v_cndmask_b32_e32 v2, v2, v4, vcc
	v_mul_lo_u32 v2, v0, v2
	v_add_u32_e32 v0, v2, v0
	v_cmp_eq_u32_e32 vcc, v1, v0
	s_and_saveexec_b64 s[0:1], vcc
	s_cbranch_execz .LBB0_2172
	s_mov_b64 s[10:11], exec
	v_mbcnt_lo_u32_b32 v0, s10, 0
	v_mbcnt_hi_u32_b32 v0, s11, v0
	v_cmp_eq_u32_e32 vcc, 0, v0
	s_and_b64 s[14:15], exec, vcc
	s_mov_b64 exec, s[14:15]
	s_cbranch_execz .LBB0_2172
	s_bcnt1_i32_b64 s3, s[10:11]
	v_mov_b32_e32 v0, 0x3000
	v_mov_b32_e32 v1, s3
	global_atomic_add v0, v1, s[94:95] offset:1280

.LBB0_2428:
	s_or_b64 exec, exec, s[14:15]
	s_waitcnt vmcnt(0)
	v_ashrrev_i32_e32 v9, 1, v240
	v_lshlrev_b32_e32 v241, 15, v241
	v_and_b32_e32 v10, 0xffff0000, v241
	v_ashrrev_i32_e32 v7, 1, v242
	v_lshlrev_b32_e32 v243, 15, v243
	v_and_b32_e32 v5, 0xffff0000, v243
	v_bfe_i32 v4, v8, 27, 1
	v_lshlrev_b32_e32 v2, 4, v8
	v_lshrrev_b32_e32 v4, 22, v4
	v_add_u32_e32 v4, v2, v4
	v_and_b32_e32 v4, 0xfffffc00, v4
	v_sub_u32_e32 v2, v2, v4
	v_ashrrev_i32_e32 v3, 31, v8
	v_lshrrev_b32_e32 v4, 4, v2
	v_lshrrev_b32_e32 v3, 26, v3
	v_bitop3_b32 v4, v4, v2, 32 bitop3:0x6c
	v_ashrrev_i32_e32 v2, 31, v2
	v_add_u32_e32 v3, v8, v3
	v_lshrrev_b32_e32 v2, 26, v2
	v_ashrrev_i32_e32 v3, 6, v3
	v_add_u32_e32 v2, v4, v2
	v_lshlrev_b32_e32 v6, 3, v3
	v_ashrrev_i32_e32 v2, 6, v2
	v_or_b32_e32 v128, v10, v9
	v_and_b32_e32 v6, -16, v6
	v_mul_i32_i24_e32 v10, 64, v2
	v_add_u32_e32 v6, v2, v6
	v_sub_u32_e32 v4, v4, v10
	v_mov_b32_e32 v10, 1
	s_and_b32 s56, s16, 1
	v_lshlrev_b32_e32 v3, 5, v3
	v_ashrrev_i16_sdwa v4, v10, sext(v4) dst_sel:DWORD dst_unused:UNUSED_PAD src0_sel:DWORD src1_sel:BYTE_0
	v_lshlrev_b32_e32 v10, 1, v6
	v_lshrrev_b32_e32 v11, 2, v6
	v_and_b32_e32 v2, 3, v2
	s_mov_b32 s14, 0x3fffe0
	v_lshlrev_b64 v[0:1], 19, v[0:1]
	v_and_b32_e32 v3, 32, v3
	v_bfe_i32 v4, v4, 0, 16
	v_and_b32_e32 v10, 24, v10
	v_and_b32_e32 v11, 4, v11
	v_and_or_b32 v2, v6, s14, v2
	v_lshl_add_u64 v[0:1], s[4:5], 0, v[0:1]
	s_lshl_b32 s14, s56, 18
	s_mov_b32 s15, 0
	s_ashr_i32 s19, s18, 6
	v_or3_b32 v2, v2, v11, v10
	v_add_lshl_u32 v3, v3, v4, 1
	v_lshl_add_u64 v[0:1], v[0:1], 0, s[14:15]
	v_lshl_add_u32 v134, v2, 10, v3
	s_lshl_b32 s34, s19, 10
	v_readfirstlane_b32 s23, v1
	v_readfirstlane_b32 s22, v0
	s_add_i32 s35, s34, 0
	s_mov_b64 s[16:17], s[22:23]
	s_ashr_i32 s20, s18, 8
	s_add_i32 m0, s35, 0x10000
	v_and_b32_e32 v135, 0x7e, v3
	global_load_lds_dwordx4 v134, s[16:17]
	s_add_u32 s16, s22, 0x10000
	s_addc_u32 s17, s23, 0
	s_add_i32 m0, s35, 0x12000
	s_mov_b32 s36, 0x3fffc00
	global_load_lds_dwordx4 v134, s[16:17]
	s_add_i32 m0, s35, 0x14000
	s_add_u32 s16, s22, 0x20000
	s_addc_u32 s17, s23, 0
	v_or_b32_e32 v129, v5, v7
	global_load_lds_dwordx4 v134, s[16:17]
	s_add_u32 s16, s22, 0x30000
	s_addc_u32 s17, s23, 0
	s_add_i32 m0, s35, 0x16000
	s_add_i32 s37, s35, 0x2000
	global_load_lds_dwordx4 v134, s[16:17]
	v_lshlrev_b32_e32 v0, 10, v9
	v_and_or_b32 v0, v0, s36, v135
	s_mov_b64 s[16:17], s[8:9]
	s_mov_b32 m0, s35
	s_add_i32 s38, s35, 0x4000
	global_load_lds_dwordx4 v0, s[16:17]
	v_lshlrev_b32_e32 v1, 10, v7
	v_and_or_b32 v1, v1, s36, v135
	s_mov_b64 s[16:17], s[8:9]
	s_mov_b32 m0, s37
	s_add_i32 s39, s35, 0x6000
	global_load_lds_dwordx4 v1, s[16:17]
	v_bfe_u32 v2, v128, 16, 16
	v_lshl_or_b32 v2, v2, 10, v135
	s_mov_b64 s[16:17], s[8:9]
	s_mov_b32 m0, s38
	s_cmp_eq_u32 s20, 1
	global_load_lds_dwordx4 v2, s[16:17]
	v_bfe_u32 v2, v129, 16, 16
	v_lshl_or_b32 v2, v2, 10, v135
	s_mov_b64 s[16:17], s[8:9]
	s_mov_b32 m0, s39
	s_nop 0
	global_load_lds_dwordx4 v2, s[16:17]
	s_cselect_b64 s[16:17], -1, 0
	s_cmp_lg_u32 s20, 1
	s_cbranch_scc1 .LBB0_2430
	s_barrier
.LBB0_2430:
	s_lshl_b32 s19, s19, 5
	s_and_b32 s41, s19, 0x60
	s_lshl_b32 s40, s20, 6
	s_lshl_b32 s14, s20, 13
	s_lshl_b32 s19, s41, 7
	s_add_u32 s20, s22, 0x80
	s_addc_u32 s21, s23, 0
	s_waitcnt vmcnt(2)
	s_barrier
	s_add_i32 m0, s35, 0x18000
	v_mov_b32_e32 v140, 0
	global_load_lds_dwordx4 v134, s[20:21]
	s_add_u32 s20, s22, 0x10080
	s_addc_u32 s21, s23, 0
	s_add_i32 m0, s35, 0x1a000
	s_mov_b32 s53, 0
	global_load_lds_dwordx4 v134, s[20:21]
	s_add_u32 s20, s8, 0x80
	s_addc_u32 s21, s9, 0
	s_add_i32 s42, s35, 0x8000
	s_mov_b64 s[24:25], s[20:21]
	s_mov_b32 m0, s42
	s_add_i32 s43, s35, 0xa000
	v_mov_b32_e32 v142, v129
	global_load_lds_dwordx4 v0, s[24:25]
	s_mov_b32 m0, s43
	s_nop 0
	global_load_lds_dwordx4 v1, s[20:21]
	s_add_i32 m0, s35, 0x1c000
	s_add_u32 s20, s22, 0x20080
	s_addc_u32 s21, s23, 0
	v_lshlrev_b32_e32 v1, 6, v8
	global_load_lds_dwordx4 v134, s[20:21]
	s_add_u32 s20, s22, 0x30080
	s_addc_u32 s21, s23, 0
	s_add_i32 m0, s35, 0x1e000
	s_cmpk_lt_u32 s18, 0x100
	global_load_lds_dwordx4 v134, s[20:21]
	v_and_b32_e32 v0, 48, v8
	s_movk_i32 s20, 0x3c0
	v_and_or_b32 v0, v1, s20, v0
	v_lshlrev_b32_e32 v1, 2, v8
	v_and_b32_e32 v1, 32, v1
	v_bitop3_b32 v2, v0, s14, v1 bitop3:0xde
	v_bitop3_b32 v136, s19, v0, v1 bitop3:0xf6
	s_cselect_b64 s[18:19], -1, 0
	s_and_b32 s14, s2, 7
	s_ashr_i32 s20, s33, 3
	s_mul_i32 s14, s20, s14
	s_ashr_i32 s20, s2, 3
	s_add_i32 s14, s14, s20
	s_waitcnt vmcnt(6)
	s_and_b64 s[0:1], s[0:1], exec
	s_cselect_b32 s44, s14, s2
	s_add_i32 s52, 0, 0x10000
	s_add_i32 s45, 0, 0x14000
	v_add_u32_e32 v137, s52, v136
	v_add_u32_e32 v138, s45, v136
	v_add_u32_e32 v139, 0, v2
	s_add_i32 s50, s35, 0xc000
	s_add_i32 s51, s35, 0xe000
	s_add_i32 s52, s52, s34
	v_mov_b32_e32 v141, v128
	s_barrier
	s_branch .LBB0_2433

.LBB0_2446:
	ds_read_b128 v[144:147], v137
	ds_read_b128 v[148:151], v137 offset:1024
	ds_read_b128 v[152:155], v137 offset:2048
	ds_read_b128 v[156:159], v137 offset:3072
	ds_read_b128 v[160:163], v138
	ds_read_b128 v[164:167], v138 offset:1024
	ds_read_b128 v[168:171], v138 offset:2048
	ds_read_b128 v[172:175], v138 offset:3072
	s_cmp_eq_u32 s60, 4
	s_cselect_b64 vcc, -1, 0
	s_and_b64 s[22:23], vcc, exec
	s_cselect_b32 s26, s8, s58
	s_cselect_b32 s27, s9, s59
	s_cselect_b32 s24, s20, s14
	s_cselect_b32 s25, s21, s57
	s_add_u32 s22, s26, 0x80
	s_addc_u32 s23, s27, 0
	s_add_u32 s62, s58, 0xffffff80
	s_addc_u32 s63, s59, -1
	v_mov_b32_e32 v132, v130
	s_mov_b32 m0, s50
	ds_read_b128 v[176:179], v139
	ds_read_b128 v[180:183], v139 offset:1024
	ds_read_b128 v[184:187], v139 offset:2048
	ds_read_b128 v[188:191], v139 offset:3072
	ds_read_b128 v[192:195], v139 offset:4096
	ds_read_b128 v[196:199], v139 offset:5120
	ds_read_b128 v[200:203], v139 offset:6144
	ds_read_b128 v[204:207], v139 offset:7168
	s_mov_b64 s[64:65], s[62:63]
	s_nop 0
	global_load_lds_dwordx4 v132, s[64:65]
	s_mov_b32 m0, s51
	s_nop 0
	global_load_lds_dwordx4 v131, s[62:63]
	s_waitcnt vmcnt(8)
	s_waitcnt lgkmcnt(0)
	s_barrier
	s_setprio 3
	v_mfma_f32_16x16x128_f8f6f4 v[124:127], v[144:151], v[176:183], v[124:127]
	v_mfma_f32_16x16x128_f8f6f4 v[116:119], v[152:159], v[176:183], v[116:119]
	v_mfma_f32_16x16x128_f8f6f4 v[108:111], v[144:151], v[184:191], v[108:111]
	v_mfma_f32_16x16x128_f8f6f4 v[100:103], v[152:159], v[184:191], v[100:103]
	v_mfma_f32_16x16x128_f8f6f4 v[92:95], v[144:151], v[192:199], v[92:95]
	v_mfma_f32_16x16x128_f8f6f4 v[84:87], v[152:159], v[192:199], v[84:87]
	v_mfma_f32_16x16x128_f8f6f4 v[76:79], v[144:151], v[200:207], v[76:79]
	v_mfma_f32_16x16x128_f8f6f4 v[68:71], v[152:159], v[200:207], v[68:71]
	v_mfma_f32_16x16x128_f8f6f4 v[120:123], v[160:167], v[176:183], v[120:123]
	v_mfma_f32_16x16x128_f8f6f4 v[112:115], v[168:175], v[176:183], v[112:115]
	v_mfma_f32_16x16x128_f8f6f4 v[104:107], v[160:167], v[184:191], v[104:107]
	v_mfma_f32_16x16x128_f8f6f4 v[96:99], v[168:175], v[184:191], v[96:99]
	v_mfma_f32_16x16x128_f8f6f4 v[88:91], v[160:167], v[192:199], v[88:91]
	v_mfma_f32_16x16x128_f8f6f4 v[80:83], v[168:175], v[192:199], v[80:83]
	v_mfma_f32_16x16x128_f8f6f4 v[72:75], v[160:167], v[200:207], v[72:75]
	v_mfma_f32_16x16x128_f8f6f4 v[64:67], v[168:175], v[200:207], v[64:67]
	s_setprio 0
	s_barrier
	v_mov_b32_e32 v132, v134
	s_mov_b64 s[62:63], s[24:25]
	s_mov_b32 m0, s52
	ds_read_b128 v[176:179], v139 offset:16384
	ds_read_b128 v[180:183], v139 offset:17408
	ds_read_b128 v[184:187], v139 offset:18432
	ds_read_b128 v[188:191], v139 offset:19456
	ds_read_b128 v[192:195], v139 offset:20480
	ds_read_b128 v[196:199], v139 offset:21504
	ds_read_b128 v[200:203], v139 offset:22528
	ds_read_b128 v[204:207], v139 offset:23552
	s_nop 0
	global_load_lds_dwordx4 v132, s[62:63]
	s_add_u32 s62, s24, 0x10000
	s_addc_u32 s63, s25, 0
	s_add_i32 m0, s52, 0x2000
	s_nop 0
	global_load_lds_dwordx4 v134, s[62:63]
	s_add_u32 s62, s24, 0x20000
	s_addc_u32 s63, s25, 0
	s_add_i32 s61, s45, s34
	s_mov_b32 m0, s61
	s_nop 0
	global_load_lds_dwordx4 v134, s[62:63]
	s_add_u32 s62, s24, 0x30000
	s_addc_u32 s63, s25, 0
	s_add_i32 m0, s61, 0x2000
	s_nop 0
	global_load_lds_dwordx4 v134, s[62:63]
	v_cndmask_b32_e32 v132, v128, v141, vcc
	v_lshlrev_b32_e32 v133, 10, v132
	v_and_or_b32 v133, v133, s36, v135
	s_mov_b64 s[62:63], s[26:27]
	s_mov_b32 m0, s35
	s_nop 0
	global_load_lds_dwordx4 v133, s[62:63]
	v_cndmask_b32_e32 v143, v129, v142, vcc
	v_lshlrev_b32_e32 v208, 10, v143
	v_and_or_b32 v208, v208, s36, v135
	s_mov_b64 s[62:63], s[26:27]
	s_mov_b32 m0, s37
	s_nop 0
	global_load_lds_dwordx4 v208, s[62:63]
	s_waitcnt vmcnt(8)
	s_waitcnt lgkmcnt(0)
	s_barrier
	s_setprio 3
	v_mfma_f32_16x16x128_f8f6f4 v[60:63], v[144:151], v[176:183], v[60:63]
	v_mfma_f32_16x16x128_f8f6f4 v[52:55], v[152:159], v[176:183], v[52:55]
	v_mfma_f32_16x16x128_f8f6f4 v[44:47], v[144:151], v[184:191], v[44:47]
	v_mfma_f32_16x16x128_f8f6f4 v[36:39], v[152:159], v[184:191], v[36:39]
	v_mfma_f32_16x16x128_f8f6f4 v[28:31], v[144:151], v[192:199], v[28:31]
	v_mfma_f32_16x16x128_f8f6f4 v[20:23], v[152:159], v[192:199], v[20:23]
	v_mfma_f32_16x16x128_f8f6f4 v[12:15], v[144:151], v[200:207], v[12:15]
	v_mfma_f32_16x16x128_f8f6f4 v[4:7], v[152:159], v[200:207], v[4:7]
	v_mfma_f32_16x16x128_f8f6f4 v[56:59], v[160:167], v[176:183], v[56:59]
	v_mfma_f32_16x16x128_f8f6f4 v[48:51], v[168:175], v[176:183], v[48:51]
	v_mfma_f32_16x16x128_f8f6f4 v[40:43], v[160:167], v[184:191], v[40:43]
	v_mfma_f32_16x16x128_f8f6f4 v[32:35], v[168:175], v[184:191], v[32:35]
	v_mfma_f32_16x16x128_f8f6f4 v[24:27], v[160:167], v[192:199], v[24:27]
	v_mfma_f32_16x16x128_f8f6f4 v[16:19], v[168:175], v[192:199], v[16:19]
	v_mfma_f32_16x16x128_f8f6f4 v[8:11], v[160:167], v[200:207], v[8:11]
	v_mfma_f32_16x16x128_f8f6f4 v[0:3], v[168:175], v[200:207], v[0:3]
	s_setprio 0
	s_barrier
	s_add_i32 s61, 0, 0x18000
	s_add_i32 s64, 0, 0x1c000
	v_add_u32_e32 v156, s61, v136
	v_add_u32_e32 v172, s64, v136
	ds_read_b128 v[144:147], v156
	ds_read_b128 v[148:151], v156 offset:1024
	ds_read_b128 v[152:155], v156 offset:2048
	ds_read_b128 v[156:159], v156 offset:3072
	ds_read_b128 v[160:163], v172
	ds_read_b128 v[164:167], v172 offset:1024
	ds_read_b128 v[168:171], v172 offset:2048
	ds_read_b128 v[172:175], v172 offset:3072
	v_bfe_u32 v132, v132, 16, 16
	v_lshl_or_b32 v132, v132, 10, v135
	s_mov_b32 m0, s38
	ds_read_b128 v[176:179], v139 offset:32768
	ds_read_b128 v[180:183], v139 offset:33792
	ds_read_b128 v[184:187], v139 offset:34816
	ds_read_b128 v[188:191], v139 offset:35840
	ds_read_b128 v[192:195], v139 offset:36864
	ds_read_b128 v[196:199], v139 offset:37888
	ds_read_b128 v[200:203], v139 offset:38912
	ds_read_b128 v[204:207], v139 offset:39936
	s_mov_b64 s[62:63], s[26:27]
	s_nop 0
	global_load_lds_dwordx4 v132, s[62:63]
	v_bfe_u32 v132, v143, 16, 16
	v_lshl_or_b32 v132, v132, 10, v135
	s_mov_b32 m0, s39
	s_nop 0
	global_load_lds_dwordx4 v132, s[26:27]
	s_waitcnt vmcnt(8)
	s_waitcnt lgkmcnt(0)
	s_barrier
	s_setprio 3
	v_mfma_f32_16x16x128_f8f6f4 v[124:127], v[144:151], v[176:183], v[124:127]
	v_mfma_f32_16x16x128_f8f6f4 v[116:119], v[152:159], v[176:183], v[116:119]
	v_mfma_f32_16x16x128_f8f6f4 v[108:111], v[144:151], v[184:191], v[108:111]
	v_mfma_f32_16x16x128_f8f6f4 v[100:103], v[152:159], v[184:191], v[100:103]
	v_mfma_f32_16x16x128_f8f6f4 v[92:95], v[144:151], v[192:199], v[92:95]
	v_mfma_f32_16x16x128_f8f6f4 v[84:87], v[152:159], v[192:199], v[84:87]
	v_mfma_f32_16x16x128_f8f6f4 v[76:79], v[144:151], v[200:207], v[76:79]
	v_mfma_f32_16x16x128_f8f6f4 v[68:71], v[152:159], v[200:207], v[68:71]
	v_mfma_f32_16x16x128_f8f6f4 v[120:123], v[160:167], v[176:183], v[120:123]
	v_mfma_f32_16x16x128_f8f6f4 v[112:115], v[168:175], v[176:183], v[112:115]
	v_mfma_f32_16x16x128_f8f6f4 v[104:107], v[160:167], v[184:191], v[104:107]
	v_mfma_f32_16x16x128_f8f6f4 v[96:99], v[168:175], v[184:191], v[96:99]
	v_mfma_f32_16x16x128_f8f6f4 v[88:91], v[160:167], v[192:199], v[88:91]
	v_mfma_f32_16x16x128_f8f6f4 v[80:83], v[168:175], v[192:199], v[80:83]
	v_mfma_f32_16x16x128_f8f6f4 v[72:75], v[160:167], v[200:207], v[72:75]
	v_mfma_f32_16x16x128_f8f6f4 v[64:67], v[168:175], v[200:207], v[64:67]
	s_setprio 0
	s_barrier
	s_add_u32 s26, s24, 0x80
	s_addc_u32 s27, s25, 0
	v_mov_b32_e32 v132, v134
	s_add_i32 s61, s61, s34
	ds_read_b128 v[176:179], v139 offset:49152
	ds_read_b128 v[180:183], v139 offset:50176
	ds_read_b128 v[184:187], v139 offset:51200
	ds_read_b128 v[188:191], v139 offset:52224
	ds_read_b128 v[192:195], v139 offset:53248
	ds_read_b128 v[196:199], v139 offset:54272
	ds_read_b128 v[200:203], v139 offset:55296
	ds_read_b128 v[204:207], v139 offset:56320
	s_mov_b32 m0, s61
	s_nop 0
	global_load_lds_dwordx4 v132, s[26:27]
	s_add_u32 s26, s24, 0x10080
	s_addc_u32 s27, s25, 0
	s_add_i32 m0, s61, 0x2000
	s_nop 0
	global_load_lds_dwordx4 v134, s[26:27]
	s_add_u32 s26, s24, 0x20080
	s_addc_u32 s27, s25, 0
	s_add_i32 s61, s64, s34
	s_mov_b32 m0, s61
	s_add_u32 s24, s24, 0x30080
	s_addc_u32 s25, s25, 0
	global_load_lds_dwordx4 v134, s[26:27]
	s_add_i32 m0, s61, 0x2000
	s_nop 0
	global_load_lds_dwordx4 v134, s[24:25]
	s_mov_b64 s[24:25], s[22:23]
	s_mov_b32 m0, s42
	s_nop 0
	global_load_lds_dwordx4 v133, s[24:25]
	s_mov_b32 m0, s43
	s_nop 0
	global_load_lds_dwordx4 v208, s[22:23]
	s_waitcnt vmcnt(8)
	s_waitcnt lgkmcnt(0)
	s_barrier
	s_setprio 3
	v_mfma_f32_16x16x128_f8f6f4 v[60:63], v[144:151], v[176:183], v[60:63]
	v_mfma_f32_16x16x128_f8f6f4 v[52:55], v[152:159], v[176:183], v[52:55]
	v_mfma_f32_16x16x128_f8f6f4 v[44:47], v[144:151], v[184:191], v[44:47]
	v_mfma_f32_16x16x128_f8f6f4 v[36:39], v[152:159], v[184:191], v[36:39]
	v_mfma_f32_16x16x128_f8f6f4 v[28:31], v[144:151], v[192:199], v[28:31]
	v_mfma_f32_16x16x128_f8f6f4 v[20:23], v[152:159], v[192:199], v[20:23]
	v_mfma_f32_16x16x128_f8f6f4 v[12:15], v[144:151], v[200:207], v[12:15]
	v_mfma_f32_16x16x128_f8f6f4 v[4:7], v[152:159], v[200:207], v[4:7]
	v_mfma_f32_16x16x128_f8f6f4 v[56:59], v[160:167], v[176:183], v[56:59]
	v_mfma_f32_16x16x128_f8f6f4 v[48:51], v[168:175], v[176:183], v[48:51]
	v_mfma_f32_16x16x128_f8f6f4 v[40:43], v[160:167], v[184:191], v[40:43]
	v_mfma_f32_16x16x128_f8f6f4 v[32:35], v[168:175], v[184:191], v[32:35]
	v_mfma_f32_16x16x128_f8f6f4 v[24:27], v[160:167], v[192:199], v[24:27]
	v_mfma_f32_16x16x128_f8f6f4 v[16:19], v[168:175], v[192:199], v[16:19]
	v_mfma_f32_16x16x128_f8f6f4 v[8:11], v[160:167], v[200:207], v[8:11]
	v_mfma_f32_16x16x128_f8f6f4 v[0:3], v[168:175], v[200:207], v[0:3]
	s_setprio 0
	s_barrier
	s_add_i32 s60, s60, 2
	s_add_u32 s14, s14, 0x100
	s_addc_u32 s57, s57, 0
	s_add_u32 s58, s58, 0x100
	s_addc_u32 s59, s59, 0
	s_cmp_gt_u32 s60, 5
	s_cbranch_scc0 .LBB0_2446
	s_and_b64 vcc, exec, s[18:19]
	s_cbranch_vccz .LBB0_2449
	s_barrier

.LBB0_2607:
	v_and_b32_e32 v0, 48, v6
	v_lshlrev_b32_e32 v1, 6, v6
	s_movk_i32 s5, 0x3c0
	v_and_or_b32 v0, v1, s5, v0
	v_lshlrev_b32_e32 v1, 2, v6
	s_lshl_b32 s4, s17, 13
	v_and_b32_e32 v1, 32, v1
	v_bitop3_b32 v2, v0, s4, v1 bitop3:0xde
	s_lshl_b32 s4, s16, 5
	s_and_b32 s21, s4, 0x60
	s_lshl_b32 s24, s17, 6
	s_lshl_b32 s4, s21, 7
	v_bitop3_b32 v1, s4, v0, v1 bitop3:0xf6
	s_add_u32 s4, s0, 0x80
	s_addc_u32 s5, s1, 0
	s_waitcnt vmcnt(0)
	s_barrier
	s_add_i32 m0, s23, 0x18000
	s_mov_b32 s36, -2
	global_load_lds_dwordx4 v64, s[4:5]
	s_add_u32 s4, s0, 0x10080
	s_addc_u32 s5, s1, 0
	s_add_i32 m0, s23, 0x1a000
	v_add_u32_e32 v69, 0, v2
	global_load_lds_dwordx4 v64, s[4:5]
	s_add_u32 s4, s8, 0x80
	s_addc_u32 s5, s9, 0
	s_add_i32 s26, s23, 0x8000
	s_mov_b64 s[16:17], s[4:5]
	s_mov_b32 m0, s26
	s_add_i32 s27, s23, 0xa000
	s_nop 0
	global_load_lds_dwordx4 v65, s[16:17]
	s_mov_b32 m0, s27
	s_nop 0
	global_load_lds_dwordx4 v66, s[4:5]
	s_add_i32 m0, s23, 0x1c000
	s_add_u32 s4, s0, 0x20080
	s_addc_u32 s5, s1, 0
	s_nop 0
	global_load_lds_dwordx4 v64, s[4:5]
	s_add_u32 s4, s0, 0x30080
	s_addc_u32 s5, s1, 0
	s_add_i32 m0, s23, 0x1e000
	s_add_u32 s30, s0, 0x100
	global_load_lds_dwordx4 v64, s[4:5]
	s_addc_u32 s31, s1, 0
	s_add_u32 s34, s8, 0x100
	s_waitcnt vmcnt(6)
	s_addc_u32 s35, s9, 0
	s_add_i32 s37, 0, 0x10000
	s_add_i32 s39, 0, 0x14000
	s_add_i32 s41, 0, 0x18000
	s_add_i32 s43, 0, 0x1c000
	v_mov_b32_e32 v0, 0
	v_add_u32_e32 v67, s37, v1
	v_add_u32_e32 v68, s39, v1
	s_add_i32 s37, s37, s14
	s_add_i32 s39, s39, s14
	v_add_u32_e32 v70, s41, v1
	v_add_u32_e32 v71, s43, v1
	s_add_i32 s41, s41, s14
	s_add_i32 s43, s43, s14
	s_add_i32 s38, s37, 0x2000
	s_add_i32 s40, s39, 0x2000
	s_add_i32 s42, s41, 0x2000
	s_add_i32 s44, s43, 0x2000
	v_mov_b32_e32 v1, v0
	v_mov_b32_e32 v2, v0
	v_mov_b32_e32 v3, v0
	v_mov_b32_e32 v8, v0
	v_mov_b32_e32 v9, v0
	v_mov_b32_e32 v10, v0
	v_mov_b32_e32 v11, v0
	v_mov_b32_e32 v16, v0
	v_mov_b32_e32 v17, v0
	v_mov_b32_e32 v18, v0
	v_mov_b32_e32 v19, v0
	v_mov_b32_e32 v24, v0
	v_mov_b32_e32 v25, v0
	v_mov_b32_e32 v26, v0
	v_mov_b32_e32 v27, v0
	v_mov_b32_e32 v32, v0
	v_mov_b32_e32 v33, v0
	v_mov_b32_e32 v34, v0
	v_mov_b32_e32 v35, v0
	v_mov_b32_e32 v40, v0
	v_mov_b32_e32 v41, v0
	v_mov_b32_e32 v42, v0
	v_mov_b32_e32 v43, v0
	v_mov_b32_e32 v48, v0
	v_mov_b32_e32 v49, v0
	v_mov_b32_e32 v50, v0
	v_mov_b32_e32 v51, v0
	v_mov_b32_e32 v56, v0
	v_mov_b32_e32 v57, v0
	v_mov_b32_e32 v58, v0
	v_mov_b32_e32 v59, v0
	v_mov_b32_e32 v4, v0
	v_mov_b32_e32 v5, v0
	v_mov_b32_e32 v6, v0
	v_mov_b32_e32 v7, v0
	v_mov_b32_e32 v12, v0
	v_mov_b32_e32 v13, v0
	v_mov_b32_e32 v14, v0
	v_mov_b32_e32 v15, v0
	v_mov_b32_e32 v20, v0
	v_mov_b32_e32 v21, v0
	v_mov_b32_e32 v22, v0
	v_mov_b32_e32 v23, v0
	v_mov_b32_e32 v28, v0
	v_mov_b32_e32 v29, v0
	v_mov_b32_e32 v30, v0
	v_mov_b32_e32 v31, v0
	v_mov_b32_e32 v36, v0
	v_mov_b32_e32 v37, v0
	v_mov_b32_e32 v38, v0
	v_mov_b32_e32 v39, v0
	v_mov_b32_e32 v44, v0
	v_mov_b32_e32 v45, v0
	v_mov_b32_e32 v46, v0
	v_mov_b32_e32 v47, v0
	v_mov_b32_e32 v52, v0
	v_mov_b32_e32 v53, v0
	v_mov_b32_e32 v54, v0
	v_mov_b32_e32 v55, v0
	v_mov_b32_e32 v60, v0
	v_mov_b32_e32 v61, v0
	v_mov_b32_e32 v62, v0
	v_mov_b32_e32 v63, v0
	s_barrier
.LBB0_2608:
	ds_read_b128 v[72:75], v67
	ds_read_b128 v[76:79], v67 offset:1024
	ds_read_b128 v[80:83], v67 offset:2048
	ds_read_b128 v[84:87], v67 offset:3072
	ds_read_b128 v[88:91], v68
	ds_read_b128 v[92:95], v68 offset:1024
	ds_read_b128 v[96:99], v68 offset:2048
	ds_read_b128 v[100:103], v68 offset:3072
	s_cmp_eq_u32 s36, 4
	s_cselect_b32 s16, s8, s34
	s_cselect_b32 s17, s9, s35
	s_cselect_b32 s14, s0, s30
	s_cselect_b32 s15, s1, s31
	s_add_u32 s4, s16, 0x80
	s_addc_u32 s5, s17, 0
	ds_read_b128 v[104:107], v69
	ds_read_b128 v[108:111], v69 offset:1024
	ds_read_b128 v[112:115], v69 offset:2048
	ds_read_b128 v[116:119], v69 offset:3072
	ds_read_b128 v[120:123], v69 offset:4096
	ds_read_b128 v[124:127], v69 offset:5120
	ds_read_b128 v[128:131], v69 offset:6144
	ds_read_b128 v[132:135], v69 offset:7168
	s_waitcnt vmcnt(6)
	s_waitcnt lgkmcnt(0)
	s_barrier
	s_setprio 3
	v_mfma_f32_16x16x128_f8f6f4 v[60:63], v[72:79], v[104:111], v[60:63]
	v_mfma_f32_16x16x128_f8f6f4 v[52:55], v[80:87], v[104:111], v[52:55]
	v_mfma_f32_16x16x128_f8f6f4 v[44:47], v[72:79], v[112:119], v[44:47]
	v_mfma_f32_16x16x128_f8f6f4 v[36:39], v[80:87], v[112:119], v[36:39]
	v_mfma_f32_16x16x128_f8f6f4 v[28:31], v[72:79], v[120:127], v[28:31]
	v_mfma_f32_16x16x128_f8f6f4 v[20:23], v[80:87], v[120:127], v[20:23]
	v_mfma_f32_16x16x128_f8f6f4 v[12:15], v[72:79], v[128:135], v[12:15]
	v_mfma_f32_16x16x128_f8f6f4 v[136:139], v[80:87], v[128:135], v[4:7]
	v_mfma_f32_16x16x128_f8f6f4 v[56:59], v[88:95], v[104:111], v[56:59]
	v_mfma_f32_16x16x128_f8f6f4 v[48:51], v[96:103], v[104:111], v[48:51]
	v_mfma_f32_16x16x128_f8f6f4 v[40:43], v[88:95], v[112:119], v[40:43]
	v_mfma_f32_16x16x128_f8f6f4 v[32:35], v[96:103], v[112:119], v[32:35]
	v_mfma_f32_16x16x128_f8f6f4 v[24:27], v[88:95], v[120:127], v[24:27]
	v_mfma_f32_16x16x128_f8f6f4 v[16:19], v[96:103], v[120:127], v[16:19]
	v_mfma_f32_16x16x128_f8f6f4 v[8:11], v[88:95], v[128:135], v[8:11]
	v_mfma_f32_16x16x128_f8f6f4 v[128:131], v[96:103], v[128:135], v[0:3]
	s_setprio 0
	s_barrier
	s_nop 4
	s_mov_b64 s[50:51], s[14:15]
	s_mov_b32 m0, s37
	s_nop 0
	global_load_lds_dwordx4 v64, s[50:51]
	s_add_u32 s50, s14, 0x10000
	s_addc_u32 s51, s15, 0
	s_mov_b32 m0, s38
	s_nop 0
	global_load_lds_dwordx4 v64, s[50:51]
	s_add_u32 s50, s14, 0x20000
	s_addc_u32 s51, s15, 0
	s_mov_b32 m0, s39
	s_nop 0
	global_load_lds_dwordx4 v64, s[50:51]
	s_add_u32 s50, s14, 0x30000
	s_addc_u32 s51, s15, 0
	s_mov_b32 m0, s40
	s_nop 0
	global_load_lds_dwordx4 v64, s[50:51]
	s_mov_b64 s[50:51], s[16:17]
	s_mov_b32 m0, s23
	s_nop 0
	global_load_lds_dwordx4 v65, s[50:51]
	s_mov_b32 m0, s25
	s_nop 0
	global_load_lds_dwordx4 v66, s[16:17]
	s_waitcnt vmcnt(6)
	s_waitcnt lgkmcnt(0)
	s_barrier
	s_barrier
	ds_read_b128 v[0:3], v70
	ds_read_b128 v[4:7], v70 offset:1024
	ds_read_b128 v[72:75], v70 offset:2048
	ds_read_b128 v[76:79], v70 offset:3072
	ds_read_b128 v[80:83], v71
	ds_read_b128 v[84:87], v71 offset:1024
	ds_read_b128 v[88:91], v71 offset:2048
	ds_read_b128 v[92:95], v71 offset:3072
	ds_read_b128 v[96:99], v69 offset:32768
	ds_read_b128 v[100:103], v69 offset:33792
	ds_read_b128 v[104:107], v69 offset:34816
	ds_read_b128 v[108:111], v69 offset:35840
	ds_read_b128 v[112:115], v69 offset:36864
	ds_read_b128 v[116:119], v69 offset:37888
	ds_read_b128 v[120:123], v69 offset:38912
	ds_read_b128 v[124:127], v69 offset:39936
	s_waitcnt vmcnt(6)
	s_waitcnt lgkmcnt(0)
	s_barrier
	s_setprio 3
	v_mfma_f32_16x16x128_f8f6f4 v[60:63], v[0:7], v[96:103], v[60:63]
	v_mfma_f32_16x16x128_f8f6f4 v[52:55], v[72:79], v[96:103], v[52:55]
	v_mfma_f32_16x16x128_f8f6f4 v[44:47], v[0:7], v[104:111], v[44:47]
	v_mfma_f32_16x16x128_f8f6f4 v[36:39], v[72:79], v[104:111], v[36:39]
	v_mfma_f32_16x16x128_f8f6f4 v[28:31], v[0:7], v[112:119], v[28:31]
	v_mfma_f32_16x16x128_f8f6f4 v[20:23], v[72:79], v[112:119], v[20:23]
	v_mfma_f32_16x16x128_f8f6f4 v[12:15], v[0:7], v[120:127], v[12:15]
	v_mfma_f32_16x16x128_f8f6f4 v[4:7], v[72:79], v[120:127], v[136:139]
	v_mfma_f32_16x16x128_f8f6f4 v[56:59], v[80:87], v[96:103], v[56:59]
	s_add_u32 s16, s14, 0x80
	s_addc_u32 s17, s15, 0
	v_mfma_f32_16x16x128_f8f6f4 v[48:51], v[88:95], v[96:103], v[48:51]
	v_mfma_f32_16x16x128_f8f6f4 v[40:43], v[80:87], v[104:111], v[40:43]
	v_mfma_f32_16x16x128_f8f6f4 v[32:35], v[88:95], v[104:111], v[32:35]
	v_mfma_f32_16x16x128_f8f6f4 v[24:27], v[80:87], v[112:119], v[24:27]
	v_mfma_f32_16x16x128_f8f6f4 v[16:19], v[88:95], v[112:119], v[16:19]
	v_mfma_f32_16x16x128_f8f6f4 v[8:11], v[80:87], v[120:127], v[8:11]
	v_mfma_f32_16x16x128_f8f6f4 v[0:3], v[88:95], v[120:127], v[128:131]
	s_setprio 0
	s_barrier
	s_mov_b32 m0, s41
	s_nop 0
	global_load_lds_dwordx4 v64, s[16:17]
	s_add_u32 s16, s14, 0x10080
	s_addc_u32 s17, s15, 0
	s_mov_b32 m0, s42
	s_nop 0
	global_load_lds_dwordx4 v64, s[16:17]
	s_add_u32 s16, s14, 0x20080
	s_addc_u32 s17, s15, 0
	s_mov_b32 m0, s43
	s_add_u32 s14, s14, 0x30080
	global_load_lds_dwordx4 v64, s[16:17]
	s_addc_u32 s15, s15, 0
	s_mov_b32 m0, s44
	s_nop 0
	global_load_lds_dwordx4 v64, s[14:15]
	s_mov_b64 s[14:15], s[4:5]
	s_mov_b32 m0, s26
	s_nop 0
	global_load_lds_dwordx4 v65, s[14:15]
	s_mov_b32 m0, s27
	s_nop 0
	global_load_lds_dwordx4 v66, s[4:5]
	s_waitcnt vmcnt(6)
	s_waitcnt lgkmcnt(0)
	s_barrier
	s_barrier
	s_add_i32 s36, s36, 2
	s_add_u32 s30, s30, 0x100
	s_addc_u32 s31, s31, 0
	s_add_u32 s34, s34, 0x100
	s_addc_u32 s35, s35, 0
	s_cmp_gt_u32 s36, 5
	s_cbranch_scc0 .LBB0_2608
	s_cmpk_lt_u32 s22, 0x100
	s_cbranch_scc0 .LBB0_2611
	s_barrier
.LBB0_2611:
	s_lshl_b32 s0, s18, 2
	s_add_i32 s0, s3, s0
	v_mbcnt_lo_u32_b32 v72, -1, 0
	v_mbcnt_hi_u32_b32 v72, -1, v72
	v_mov_b32_e32 v64, s0
	ds_read2_b32 v[64:65], v64 offset0:64 offset1:224
	s_lshl_b32 s0, s20, 7
	v_and_b32_e32 v70, 15, v72
	s_add_i32 s0, s0, s24
	v_or_b32_e32 v71, s0, v70
	s_waitcnt lgkmcnt(0)
	v_ashrrev_i32_e32 v67, 31, v64
	v_mov_b32_e32 v66, v64
	v_lshlrev_b32_e32 v64, 2, v64
	v_add_u32_e32 v64, s3, v64
	ds_read_b32 v64, v64 offset:4
	v_lshlrev_b64 v[68:69], 16, v[66:67]
	v_add_u32_e32 v66, v65, v71
	v_mov_b32_e32 v73, 0
	v_lshl_add_u64 v[68:69], s[10:11], 0, v[68:69]
	s_waitcnt lgkmcnt(0)
	v_cmp_lt_i32_e32 vcc, v66, v64
	v_ashrrev_i32_e32 v67, 31, v66
	v_mov_b32_e32 v74, 0
	v_bfe_u32 v140, v72, 4, 2
	s_lshl_b32 s0, s19, 7
	v_lshl_add_u64 v[144:145], v[66:67], 2, v[68:69]
	v_lshl_or_b32 v141, v140, 3, s0
	global_load_dword v146, v[144:145], off
	global_load_dword v147, v[144:145], off offset:64
	global_load_dword v148, v[144:145], off offset:128
	global_load_dword v149, v[144:145], off offset:192
	s_lshl_b32 s4, s18, 8
	v_or_b32_e32 v141, s21, v141
	v_add_u32_e32 v142, s4, v71
	v_lshl_add_u32 v142, v142, 8, v141
	v_cmp_lt_i32_e32 vcc, v66, v64
	s_waitcnt vmcnt(3)
	v_mul_f32_e32 v155, 0x3c800000, v146
	v_mul_f32_e32 v156, 0xbd38aa3b, v60
	v_mul_f32_e32 v157, 0xbd38aa3b, v61
	v_mul_f32_e32 v158, 0xbd38aa3b, v62
	v_mul_f32_e32 v159, 0xbd38aa3b, v63
	v_mul_f32_e32 v160, 0xbd38aa3b, v52
	v_mul_f32_e32 v161, 0xbd38aa3b, v53
	v_mul_f32_e32 v162, 0xbd38aa3b, v54
	v_mul_f32_e32 v163, 0xbd38aa3b, v55
	v_exp_f32_e32 v156, v156
	v_exp_f32_e32 v157, v157
	v_exp_f32_e32 v158, v158
	v_exp_f32_e32 v159, v159
	v_exp_f32_e32 v160, v160
	v_exp_f32_e32 v161, v161
	v_exp_f32_e32 v162, v162
	v_exp_f32_e32 v163, v163
	v_add_f32_e32 v156, 1.0, v156
	v_add_f32_e32 v157, 1.0, v157
	v_add_f32_e32 v158, 1.0, v158
	v_add_f32_e32 v159, 1.0, v159
	v_add_f32_e32 v160, 1.0, v160
	v_add_f32_e32 v161, 1.0, v161
	v_add_f32_e32 v162, 1.0, v162
	v_add_f32_e32 v163, 1.0, v163
	v_rcp_f32_e32 v156, v156
	v_rcp_f32_e32 v157, v157
	v_rcp_f32_e32 v158, v158
	v_rcp_f32_e32 v159, v159
	v_rcp_f32_e32 v160, v160
	v_rcp_f32_e32 v161, v161
	v_rcp_f32_e32 v162, v162
	v_rcp_f32_e32 v163, v163
	v_mul_f32_e32 v156, v60, v156
	v_mul_f32_e32 v157, v61, v157
	v_mul_f32_e32 v158, v62, v158
	v_mul_f32_e32 v159, v63, v159
	v_mul_f32_e32 v160, v52, v160
	v_mul_f32_e32 v161, v53, v161
	v_mul_f32_e32 v162, v54, v162
	v_mul_f32_e32 v163, v55, v163
	v_mul_f32_e32 v156, v156, v56
	v_mul_f32_e32 v157, v157, v57
	v_mul_f32_e32 v158, v158, v58
	v_mul_f32_e32 v159, v159, v59
	v_mul_f32_e32 v160, v160, v48
	v_mul_f32_e32 v161, v161, v49
	v_mul_f32_e32 v162, v162, v50
	v_mul_f32_e32 v163, v163, v51
	v_mul_f32_e32 v156, v156, v155
	v_mul_f32_e32 v157, v157, v155
	v_mul_f32_e32 v158, v158, v155
	v_mul_f32_e32 v159, v159, v155
	v_mul_f32_e32 v160, v160, v155
	v_mul_f32_e32 v161, v161, v155
	v_mul_f32_e32 v162, v162, v155
	v_mul_f32_e32 v163, v163, v155
	v_max_f32_e32 v156, 0xc3e00000, v156
	v_max_f32_e32 v157, 0xc3e00000, v157
	v_max_f32_e32 v158, 0xc3e00000, v158
	v_max_f32_e32 v159, 0xc3e00000, v159
	v_max_f32_e32 v160, 0xc3e00000, v160
	v_max_f32_e32 v161, 0xc3e00000, v161
	v_max_f32_e32 v162, 0xc3e00000, v162
	v_max_f32_e32 v163, 0xc3e00000, v163
	v_min_f32_e32 v156, 0x43e00000, v156
	v_min_f32_e32 v157, 0x43e00000, v157
	v_min_f32_e32 v158, 0x43e00000, v158
	v_min_f32_e32 v159, 0x43e00000, v159
	v_min_f32_e32 v160, 0x43e00000, v160
	v_min_f32_e32 v161, 0x43e00000, v161
	v_min_f32_e32 v162, 0x43e00000, v162
	v_min_f32_e32 v163, 0x43e00000, v163
	v_cndmask_b32_e32 v156, 0, v156, vcc
	v_cndmask_b32_e32 v157, 0, v157, vcc
	v_cndmask_b32_e32 v158, 0, v158, vcc
	v_cndmask_b32_e32 v159, 0, v159, vcc
	v_cndmask_b32_e32 v160, 0, v160, vcc
	v_cndmask_b32_e32 v161, 0, v161, vcc
	v_cndmask_b32_e32 v162, 0, v162, vcc
	v_cndmask_b32_e32 v163, 0, v163, vcc
	v_mov_b32_e32 v180, 0
	v_mov_b32_e32 v181, 0
	v_cvt_pk_fp8_f32 v180, v156, v157
	v_cvt_pk_fp8_f32 v181, v160, v161
	v_mov_b32_e32 v184, v142
	v_cvt_pk_fp8_f32 v180, v158, v159 op_sel:[0,0,1]
	v_cvt_pk_fp8_f32 v181, v162, v163 op_sel:[0,0,1]
	s_nop 1
	global_store_dwordx2 v184, v[180:181], s[12:13] sc1
	v_add_u32_e32 v154, 0x10, v66
	v_cmp_lt_i32_e32 vcc, v154, v64
	s_waitcnt vmcnt(3)
	v_mul_f32_e32 v155, 0x3c800000, v147
	v_mul_f32_e32 v156, 0xbd38aa3b, v44
	v_mul_f32_e32 v157, 0xbd38aa3b, v45
	v_mul_f32_e32 v158, 0xbd38aa3b, v46
	v_mul_f32_e32 v159, 0xbd38aa3b, v47
	v_mul_f32_e32 v160, 0xbd38aa3b, v36
	v_mul_f32_e32 v161, 0xbd38aa3b, v37
	v_mul_f32_e32 v162, 0xbd38aa3b, v38
	v_mul_f32_e32 v163, 0xbd38aa3b, v39
	v_exp_f32_e32 v156, v156
	v_exp_f32_e32 v157, v157
	v_exp_f32_e32 v158, v158
	v_exp_f32_e32 v159, v159
	v_exp_f32_e32 v160, v160
	v_exp_f32_e32 v161, v161
	v_exp_f32_e32 v162, v162
	v_exp_f32_e32 v163, v163
	v_add_f32_e32 v156, 1.0, v156
	v_add_f32_e32 v157, 1.0, v157
	v_add_f32_e32 v158, 1.0, v158
	v_add_f32_e32 v159, 1.0, v159
	v_add_f32_e32 v160, 1.0, v160
	v_add_f32_e32 v161, 1.0, v161
	v_add_f32_e32 v162, 1.0, v162
	v_add_f32_e32 v163, 1.0, v163
	v_rcp_f32_e32 v156, v156
	v_rcp_f32_e32 v157, v157
	v_rcp_f32_e32 v158, v158
	v_rcp_f32_e32 v159, v159
	v_rcp_f32_e32 v160, v160
	v_rcp_f32_e32 v161, v161
	v_rcp_f32_e32 v162, v162
	v_rcp_f32_e32 v163, v163
	v_mul_f32_e32 v156, v44, v156
	v_mul_f32_e32 v157, v45, v157
	v_mul_f32_e32 v158, v46, v158
	v_mul_f32_e32 v159, v47, v159
	v_mul_f32_e32 v160, v36, v160
	v_mul_f32_e32 v161, v37, v161
	v_mul_f32_e32 v162, v38, v162
	v_mul_f32_e32 v163, v39, v163
	v_mul_f32_e32 v156, v156, v40
	v_mul_f32_e32 v157, v157, v41
	v_mul_f32_e32 v158, v158, v42
	v_mul_f32_e32 v159, v159, v43
	v_mul_f32_e32 v160, v160, v32
	v_mul_f32_e32 v161, v161, v33
	v_mul_f32_e32 v162, v162, v34
	v_mul_f32_e32 v163, v163, v35
	v_mul_f32_e32 v156, v156, v155
	v_mul_f32_e32 v157, v157, v155
	v_mul_f32_e32 v158, v158, v155
	v_mul_f32_e32 v159, v159, v155
	v_mul_f32_e32 v160, v160, v155
	v_mul_f32_e32 v161, v161, v155
	v_mul_f32_e32 v162, v162, v155
	v_mul_f32_e32 v163, v163, v155
	v_max_f32_e32 v156, 0xc3e00000, v156
	v_max_f32_e32 v157, 0xc3e00000, v157
	v_max_f32_e32 v158, 0xc3e00000, v158
	v_max_f32_e32 v159, 0xc3e00000, v159
	v_max_f32_e32 v160, 0xc3e00000, v160
	v_max_f32_e32 v161, 0xc3e00000, v161
	v_max_f32_e32 v162, 0xc3e00000, v162
	v_max_f32_e32 v163, 0xc3e00000, v163
	v_min_f32_e32 v156, 0x43e00000, v156
	v_min_f32_e32 v157, 0x43e00000, v157
	v_min_f32_e32 v158, 0x43e00000, v158
	v_min_f32_e32 v159, 0x43e00000, v159
	v_min_f32_e32 v160, 0x43e00000, v160
	v_min_f32_e32 v161, 0x43e00000, v161
	v_min_f32_e32 v162, 0x43e00000, v162
	v_min_f32_e32 v163, 0x43e00000, v163
	v_cndmask_b32_e32 v156, 0, v156, vcc
	v_cndmask_b32_e32 v157, 0, v157, vcc
	v_cndmask_b32_e32 v158, 0, v158, vcc
	v_cndmask_b32_e32 v159, 0, v159, vcc
	v_cndmask_b32_e32 v160, 0, v160, vcc
	v_cndmask_b32_e32 v161, 0, v161, vcc
	v_cndmask_b32_e32 v162, 0, v162, vcc
	v_cndmask_b32_e32 v163, 0, v163, vcc
	v_mov_b32_e32 v182, 0
	v_mov_b32_e32 v183, 0
	v_cvt_pk_fp8_f32 v182, v156, v157
	v_cvt_pk_fp8_f32 v183, v160, v161
	v_add_u32_e32 v184, 0x1000, v142
	v_cvt_pk_fp8_f32 v182, v158, v159 op_sel:[0,0,1]
	v_cvt_pk_fp8_f32 v183, v162, v163 op_sel:[0,0,1]
	s_nop 1
	global_store_dwordx2 v184, v[182:183], s[12:13] sc1
	v_add_u32_e32 v154, 0x20, v66
	v_cmp_lt_i32_e32 vcc, v154, v64
	s_waitcnt vmcnt(3)
	v_mul_f32_e32 v155, 0x3c800000, v148
	v_mul_f32_e32 v156, 0xbd38aa3b, v28
	v_mul_f32_e32 v157, 0xbd38aa3b, v29
	v_mul_f32_e32 v158, 0xbd38aa3b, v30
	v_mul_f32_e32 v159, 0xbd38aa3b, v31
	v_mul_f32_e32 v160, 0xbd38aa3b, v20
	v_mul_f32_e32 v161, 0xbd38aa3b, v21
	v_mul_f32_e32 v162, 0xbd38aa3b, v22
	v_mul_f32_e32 v163, 0xbd38aa3b, v23
	v_exp_f32_e32 v156, v156
	v_exp_f32_e32 v157, v157
	v_exp_f32_e32 v158, v158
	v_exp_f32_e32 v159, v159
	v_exp_f32_e32 v160, v160
	v_exp_f32_e32 v161, v161
	v_exp_f32_e32 v162, v162
	v_exp_f32_e32 v163, v163
	v_add_f32_e32 v156, 1.0, v156
	v_add_f32_e32 v157, 1.0, v157
	v_add_f32_e32 v158, 1.0, v158
	v_add_f32_e32 v159, 1.0, v159
	v_add_f32_e32 v160, 1.0, v160
	v_add_f32_e32 v161, 1.0, v161
	v_add_f32_e32 v162, 1.0, v162
	v_add_f32_e32 v163, 1.0, v163
	v_rcp_f32_e32 v156, v156
	v_rcp_f32_e32 v157, v157
	v_rcp_f32_e32 v158, v158
	v_rcp_f32_e32 v159, v159
	v_rcp_f32_e32 v160, v160
	v_rcp_f32_e32 v161, v161
	v_rcp_f32_e32 v162, v162
	v_rcp_f32_e32 v163, v163
	v_mul_f32_e32 v156, v28, v156
	v_mul_f32_e32 v157, v29, v157
	v_mul_f32_e32 v158, v30, v158
	v_mul_f32_e32 v159, v31, v159
	v_mul_f32_e32 v160, v20, v160
	v_mul_f32_e32 v161, v21, v161
	v_mul_f32_e32 v162, v22, v162
	v_mul_f32_e32 v163, v23, v163
	v_mul_f32_e32 v156, v156, v24
	v_mul_f32_e32 v157, v157, v25
	v_mul_f32_e32 v158, v158, v26
	v_mul_f32_e32 v159, v159, v27
	v_mul_f32_e32 v160, v160, v16
	v_mul_f32_e32 v161, v161, v17
	v_mul_f32_e32 v162, v162, v18
	v_mul_f32_e32 v163, v163, v19
	v_mul_f32_e32 v156, v156, v155
	v_mul_f32_e32 v157, v157, v155
	v_mul_f32_e32 v158, v158, v155
	v_mul_f32_e32 v159, v159, v155
	v_mul_f32_e32 v160, v160, v155
	v_mul_f32_e32 v161, v161, v155
	v_mul_f32_e32 v162, v162, v155
	v_mul_f32_e32 v163, v163, v155
	v_max_f32_e32 v156, 0xc3e00000, v156
	v_max_f32_e32 v157, 0xc3e00000, v157
	v_max_f32_e32 v158, 0xc3e00000, v158
	v_max_f32_e32 v159, 0xc3e00000, v159
	v_max_f32_e32 v160, 0xc3e00000, v160
	v_max_f32_e32 v161, 0xc3e00000, v161
	v_max_f32_e32 v162, 0xc3e00000, v162
	v_max_f32_e32 v163, 0xc3e00000, v163
	v_min_f32_e32 v156, 0x43e00000, v156
	v_min_f32_e32 v157, 0x43e00000, v157
	v_min_f32_e32 v158, 0x43e00000, v158
	v_min_f32_e32 v159, 0x43e00000, v159
	v_min_f32_e32 v160, 0x43e00000, v160
	v_min_f32_e32 v161, 0x43e00000, v161
	v_min_f32_e32 v162, 0x43e00000, v162
	v_min_f32_e32 v163, 0x43e00000, v163
	v_cndmask_b32_e32 v156, 0, v156, vcc
	v_cndmask_b32_e32 v157, 0, v157, vcc
	v_cndmask_b32_e32 v158, 0, v158, vcc
	v_cndmask_b32_e32 v159, 0, v159, vcc
	v_cndmask_b32_e32 v160, 0, v160, vcc
	v_cndmask_b32_e32 v161, 0, v161, vcc
	v_cndmask_b32_e32 v162, 0, v162, vcc
	v_cndmask_b32_e32 v163, 0, v163, vcc
	v_mov_b32_e32 v180, 0
	v_mov_b32_e32 v181, 0
	v_cvt_pk_fp8_f32 v180, v156, v157
	v_cvt_pk_fp8_f32 v181, v160, v161
	v_add_u32_e32 v184, 0x2000, v142
	v_cvt_pk_fp8_f32 v180, v158, v159 op_sel:[0,0,1]
	v_cvt_pk_fp8_f32 v181, v162, v163 op_sel:[0,0,1]
	s_nop 1
	global_store_dwordx2 v184, v[180:181], s[12:13] sc1
	v_add_u32_e32 v154, 0x30, v66
	v_cmp_lt_i32_e32 vcc, v154, v64
	s_waitcnt vmcnt(3)
	v_mul_f32_e32 v155, 0x3c800000, v149
	v_mul_f32_e32 v156, 0xbd38aa3b, v12
	v_mul_f32_e32 v157, 0xbd38aa3b, v13
	v_mul_f32_e32 v158, 0xbd38aa3b, v14
	v_mul_f32_e32 v159, 0xbd38aa3b, v15
	v_mul_f32_e32 v160, 0xbd38aa3b, v4
	v_mul_f32_e32 v161, 0xbd38aa3b, v5
	v_mul_f32_e32 v162, 0xbd38aa3b, v6
	v_mul_f32_e32 v163, 0xbd38aa3b, v7
	v_exp_f32_e32 v156, v156
	v_exp_f32_e32 v157, v157
	v_exp_f32_e32 v158, v158
	v_exp_f32_e32 v159, v159
	v_exp_f32_e32 v160, v160
	v_exp_f32_e32 v161, v161
	v_exp_f32_e32 v162, v162
	v_exp_f32_e32 v163, v163
	v_add_f32_e32 v156, 1.0, v156
	v_add_f32_e32 v157, 1.0, v157
	v_add_f32_e32 v158, 1.0, v158
	v_add_f32_e32 v159, 1.0, v159
	v_add_f32_e32 v160, 1.0, v160
	v_add_f32_e32 v161, 1.0, v161
	v_add_f32_e32 v162, 1.0, v162
	v_add_f32_e32 v163, 1.0, v163
	v_rcp_f32_e32 v156, v156
	v_rcp_f32_e32 v157, v157
	v_rcp_f32_e32 v158, v158
	v_rcp_f32_e32 v159, v159
	v_rcp_f32_e32 v160, v160
	v_rcp_f32_e32 v161, v161
	v_rcp_f32_e32 v162, v162
	v_rcp_f32_e32 v163, v163
	v_mul_f32_e32 v156, v12, v156
	v_mul_f32_e32 v157, v13, v157
	v_mul_f32_e32 v158, v14, v158
	v_mul_f32_e32 v159, v15, v159
	v_mul_f32_e32 v160, v4, v160
	v_mul_f32_e32 v161, v5, v161
	v_mul_f32_e32 v162, v6, v162
	v_mul_f32_e32 v163, v7, v163
	v_mul_f32_e32 v156, v156, v8
	v_mul_f32_e32 v157, v157, v9
	v_mul_f32_e32 v158, v158, v10
	v_mul_f32_e32 v159, v159, v11
	v_mul_f32_e32 v160, v160, v0
	v_mul_f32_e32 v161, v161, v1
	v_mul_f32_e32 v162, v162, v2
	v_mul_f32_e32 v163, v163, v3
	v_mul_f32_e32 v156, v156, v155
	v_mul_f32_e32 v157, v157, v155
	v_mul_f32_e32 v158, v158, v155
	v_mul_f32_e32 v159, v159, v155
	v_mul_f32_e32 v160, v160, v155
	v_mul_f32_e32 v161, v161, v155
	v_mul_f32_e32 v162, v162, v155
	v_mul_f32_e32 v163, v163, v155
	v_max_f32_e32 v156, 0xc3e00000, v156
	v_max_f32_e32 v157, 0xc3e00000, v157
	v_max_f32_e32 v158, 0xc3e00000, v158
	v_max_f32_e32 v159, 0xc3e00000, v159
	v_max_f32_e32 v160, 0xc3e00000, v160
	v_max_f32_e32 v161, 0xc3e00000, v161
	v_max_f32_e32 v162, 0xc3e00000, v162
	v_max_f32_e32 v163, 0xc3e00000, v163
	v_min_f32_e32 v156, 0x43e00000, v156
	v_min_f32_e32 v157, 0x43e00000, v157
	v_min_f32_e32 v158, 0x43e00000, v158
	v_min_f32_e32 v159, 0x43e00000, v159
	v_min_f32_e32 v160, 0x43e00000, v160
	v_min_f32_e32 v161, 0x43e00000, v161
	v_min_f32_e32 v162, 0x43e00000, v162
	v_min_f32_e32 v163, 0x43e00000, v163
	v_cndmask_b32_e32 v156, 0, v156, vcc
	v_cndmask_b32_e32 v157, 0, v157, vcc
	v_cndmask_b32_e32 v158, 0, v158, vcc
	v_cndmask_b32_e32 v159, 0, v159, vcc
	v_cndmask_b32_e32 v160, 0, v160, vcc
	v_cndmask_b32_e32 v161, 0, v161, vcc
	v_cndmask_b32_e32 v162, 0, v162, vcc
	v_cndmask_b32_e32 v163, 0, v163, vcc
	v_mov_b32_e32 v182, 0
	v_mov_b32_e32 v183, 0
	v_cvt_pk_fp8_f32 v182, v156, v157
	v_cvt_pk_fp8_f32 v183, v160, v161
	v_add_u32_e32 v184, 0x3000, v142
	v_cvt_pk_fp8_f32 v182, v158, v159 op_sel:[0,0,1]
	v_cvt_pk_fp8_f32 v183, v162, v163 op_sel:[0,0,1]
	s_nop 1
	global_store_dwordx2 v184, v[182:183], s[12:13] sc1
	v_bfe_u32 v50, v72, 4, 2
	s_waitcnt vmcnt(0)
	v_or_b32_e32 v0, v50, v70
	v_cmp_eq_u32_e32 vcc, 0, v0
	s_and_saveexec_b64 s[0:1], vcc
	s_cbranch_execz .LBB0_2686
	s_mov_b64 s[4:5], exec
	v_mbcnt_lo_u32_b32 v0, s4, 0
	v_mbcnt_hi_u32_b32 v0, s5, v0
	v_cmp_eq_u32_e32 vcc, 0, v0
	s_and_b64 s[8:9], exec, vcc
	s_mov_b64 exec, s[8:9]
	s_cbranch_execz .LBB0_2686
	s_lshl_b32 s8, s18, 5
	s_ashr_i32 s9, s8, 31
	s_lshl_b64 s[8:9], s[8:9], 2
	s_add_u32 s8, s48, s8
	s_addc_u32 s9, s49, s9
	s_bcnt1_i32_b64 s4, s[4:5]
	v_mov_b32_e32 v0, 0
	v_mov_b32_e32 v1, s4
	global_atomic_add v0, v1, s[8:9]

.LBB0_2703:
	v_bfe_i32 v3, v0, 27, 1
	v_lshlrev_b32_e32 v1, 4, v0
	v_lshrrev_b32_e32 v3, 22, v3
	v_add_u32_e32 v3, v1, v3
	v_and_b32_e32 v3, 0xfffffc00, v3
	v_ashrrev_i32_e32 v2, 31, v0
	v_sub_u32_e32 v1, v1, v3
	v_lshrrev_b32_e32 v2, 26, v2
	v_lshrrev_b32_e32 v3, 4, v1
	v_add_u32_e32 v2, v0, v2
	v_bitop3_b32 v3, v3, v1, 32 bitop3:0x6c
	v_ashrrev_i32_e32 v1, 31, v1
	v_ashrrev_i32_e32 v2, 6, v2
	v_lshrrev_b32_e32 v1, 26, v1
	v_lshlrev_b32_e32 v4, 3, v2
	v_add_u32_e32 v1, v3, v1
	s_add_u32 s10, s78, 0x6d00000
	v_and_b32_e32 v4, -16, v4
	v_ashrrev_i32_e32 v1, 6, v1
	v_lshlrev_b32_e32 v2, 5, v2
	s_addc_u32 s11, s79, 0
	s_ashr_i32 s4, s19, 6
	v_add_u32_e32 v4, v1, v4
	v_and_b32_e32 v5, 32, v2
	v_mul_i32_i24_e32 v2, 64, v1
	v_and_b32_e32 v1, 3, v1
	s_mov_b32 s14, 0xffffe0
	s_ashr_i32 s39, s38, 31
	s_ashr_i32 s5, s19, 8
	v_and_or_b32 v1, v4, s14, v1
	s_lshl_b32 s27, s4, 10
	s_lshl_b64 s[14:15], s[38:39], 16
	v_sub_u32_e32 v2, v3, v2
	v_mov_b32_e32 v3, 1
	s_add_u32 s40, s12, s14
	v_ashrrev_i16_sdwa v2, v3, sext(v2) dst_sel:DWORD dst_unused:UNUSED_PAD src0_sel:DWORD src1_sel:BYTE_0
	s_addc_u32 s41, s13, s15
	s_lshl_b32 s14, s38, 2
	v_bfe_i32 v3, v2, 0, 16
	v_lshlrev_b32_e32 v2, 1, v4
	s_add_i32 s14, s14, 0
	v_and_b32_e32 v6, 24, v2
	v_lshrrev_b32_e32 v2, 2, v4
	s_add_i32 s14, s14, 0x24100
	v_and_b32_e32 v7, 4, v2
	s_barrier
	v_mov_b32_e32 v2, s14
	ds_read_b32 v2, v2
	v_or3_b32 v1, v1, v7, v6
	v_add_lshl_u32 v3, v5, v3, 1
	v_lshl_add_u32 v194, v1, 8, v3
	v_lshl_add_u32 v195, v4, 8, v3
	s_waitcnt lgkmcnt(0)
	v_ashrrev_i32_e32 v3, 31, v2
	v_lshlrev_b64 v[2:3], 18, v[2:3]
	s_ashr_i32 s37, s36, 31
	v_lshl_add_u64 v[2:3], s[10:11], 0, v[2:3]
	s_lshl_b64 s[14:15], s[36:37], 16
	v_lshl_add_u64 v[2:3], v[2:3], 0, s[14:15]
	s_add_i32 s50, s27, 0
	v_readfirstlane_b32 s15, v3
	v_readfirstlane_b32 s14, v2
	s_mov_b64 s[16:17], s[14:15]
	s_add_i32 m0, s50, 0x10000
	s_mov_b32 s54, 0
	global_load_lds_dwordx4 v194, s[16:17]
	s_add_u32 s16, s14, 0x4000
	s_addc_u32 s17, s15, 0
	s_add_i32 m0, s50, 0x12000
	s_nop 0
	global_load_lds_dwordx4 v194, s[16:17]
	s_add_i32 m0, s50, 0x14000
	s_add_u32 s16, s14, 0x8000
	s_addc_u32 s17, s15, 0
	s_nop 0
	global_load_lds_dwordx4 v194, s[16:17]
	s_add_u32 s16, s14, 0xc000
	s_addc_u32 s17, s15, 0
	s_add_i32 m0, s50, 0x16000
	s_nop 0
	global_load_lds_dwordx4 v194, s[16:17]
	v_mov_b32_e32 v1, v195
	s_mov_b64 s[16:17], s[40:41]
	s_mov_b32 m0, s50
	s_nop 0
	global_load_lds_dwordx4 v1, s[16:17] sc1
	s_add_u32 s16, s40, 0x4000
	v_mov_b32_e32 v1, v195
	s_addc_u32 s17, s41, 0
	s_add_i32 s51, s50, 0x2000
	s_mov_b32 m0, s51
	s_add_i32 s52, s50, 0x4000
	global_load_lds_dwordx4 v1, s[16:17] sc1
	s_add_u32 s16, s40, 0x8000
	v_mov_b32_e32 v1, v195
	s_addc_u32 s17, s41, 0
	s_mov_b32 m0, s52
	s_nop 0
	global_load_lds_dwordx4 v1, s[16:17] sc1
	s_add_u32 s16, s40, 0xc000
	s_addc_u32 s17, s41, 0
	s_add_i32 s53, s50, 0x6000
	v_mov_b32_e32 v1, v195
	s_mov_b32 m0, s53
	s_cmp_eq_u32 s5, 1
	global_load_lds_dwordx4 v1, s[16:17] sc1
	s_cselect_b64 s[16:17], -1, 0
	s_cmp_lg_u32 s5, 1
	s_cbranch_scc1 .LBB0_2705
	s_barrier
.LBB0_2705:
	s_lshl_b32 s4, s4, 5
	s_and_b32 s55, s4, 0x60
	s_lshl_b32 s18, s5, 6
	s_lshl_b32 s22, s5, 13
	s_lshl_b32 s23, s55, 7
	s_add_u32 s20, s78, 0x12500000
	s_addc_u32 s21, s79, 0
	s_add_u32 s4, s14, 0x80
	s_addc_u32 s5, s15, 0
	s_waitcnt vmcnt(2)
	s_barrier
	s_add_i32 m0, s50, 0x18000
	v_lshlrev_b32_e32 v2, 6, v0
	global_load_lds_dwordx4 v194, s[4:5]
	s_add_u32 s4, s14, 0x4080
	s_addc_u32 s5, s15, 0
	s_add_i32 m0, s50, 0x1a000
	v_mov_b32_e32 v193, 0
	global_load_lds_dwordx4 v194, s[4:5]
	s_add_u32 s4, s40, 0x80
	s_addc_u32 s5, s41, 0
	v_mov_b32_e32 v1, v195
	s_add_i32 s56, s50, 0x8000
	s_mov_b32 m0, s56
	s_mov_b32 s26, 0x3e000000
	global_load_lds_dwordx4 v1, s[4:5] sc1
	s_add_u32 s4, s40, 0x4080
	s_addc_u32 s5, s41, 0
	s_add_i32 s57, s50, 0xa000
	v_mov_b32_e32 v1, v195
	s_mov_b32 m0, s57
	s_nop 0
	global_load_lds_dwordx4 v1, s[4:5] sc1
	s_add_i32 m0, s50, 0x1c000
	s_add_u32 s4, s14, 0x8080
	s_addc_u32 s5, s15, 0
	s_nop 0
	global_load_lds_dwordx4 v194, s[4:5]
	s_add_u32 s4, s14, 0xc080
	s_addc_u32 s5, s15, 0
	s_add_i32 m0, s50, 0x1e000
	s_cmpk_lt_u32 s19, 0x100
	global_load_lds_dwordx4 v194, s[4:5]
	v_and_b32_e32 v1, 48, v0
	s_movk_i32 s4, 0x3c0
	v_lshlrev_b32_e32 v0, 2, v0
	v_and_or_b32 v1, v2, s4, v1
	v_and_b32_e32 v0, 32, v0
	s_waitcnt vmcnt(6)
	v_bitop3_b32 v2, v1, s22, v0 bitop3:0xde
	v_bitop3_b32 v196, s23, v1, v0 bitop3:0xf6
	s_cselect_b64 s[22:23], -1, 0
	s_ashr_i32 s19, s18, 31
	v_cndmask_b32_e64 v0, 0, 1, s[0:1]
	s_add_i32 s61, 0, 0x10000
	s_add_i32 s62, 0, 0x14000
	s_sub_i32 s58, s33, s25
	s_sub_i32 s59, s2, s25
	s_lshl_b32 s60, s24, 2
	v_cmp_ne_u32_e64 s[0:1], 1, v0
	v_add_u32_e32 v197, s61, v196
	v_add_u32_e32 v198, s62, v196
	v_add_u32_e32 v199, 0, v2
	s_lshl_b64 s[24:25], s[18:19], 2
	s_barrier
	s_branch .LBB0_2708

.LBB0_2724:
	ds_read_b128 v[56:59], v197
	ds_read_b128 v[60:63], v197 offset:1024
	ds_read_b128 v[80:83], v197 offset:2048
	ds_read_b128 v[84:87], v197 offset:3072
	ds_read_b128 v[0:3], v198
	ds_read_b128 v[4:7], v198 offset:1024
	ds_read_b128 v[8:11], v198 offset:2048
	ds_read_b128 v[12:15], v198 offset:3072
	s_add_u32 s42, s34, 0x80
	s_addc_u32 s43, s35, 0
	s_add_u32 s44, s14, 0x80
	s_addc_u32 s45, s15, 0
	s_add_u32 s64, s40, 0x8080
	v_mov_b32_e32 v16, v195
	s_addc_u32 s65, s41, 0
	s_add_i32 m0, s50, 0xc000
	ds_read_b128 v[64:67], v199
	ds_read_b128 v[68:71], v199 offset:1024
	ds_read_b128 v[72:75], v199 offset:2048
	ds_read_b128 v[76:79], v199 offset:3072
	ds_read_b128 v[88:91], v199 offset:4096
	ds_read_b128 v[92:95], v199 offset:5120
	ds_read_b128 v[96:99], v199 offset:6144
	ds_read_b128 v[100:103], v199 offset:7168
	s_add_u32 s40, s40, 0xc080
	s_addc_u32 s41, s41, 0
	global_load_lds_dwordx4 v16, s[64:65] sc1
	v_mov_b32_e32 v16, v195
	s_add_i32 m0, s50, 0xe000
	s_nop 0
	global_load_lds_dwordx4 v16, s[40:41] sc1
	s_waitcnt vmcnt(8)
	s_waitcnt lgkmcnt(0)
	s_barrier
	s_setprio 3
	v_mfma_f32_16x16x128_f8f6f4 v[16:19], v[56:63], v[64:71], 0
	v_mfma_f32_16x16x128_f8f6f4 v[20:23], v[80:87], v[64:71], 0
	v_mfma_f32_16x16x128_f8f6f4 v[24:27], v[56:63], v[72:79], 0
	v_mfma_f32_16x16x128_f8f6f4 v[28:31], v[80:87], v[72:79], 0
	v_mfma_f32_16x16x128_f8f6f4 v[32:35], v[56:63], v[88:95], 0
	v_mfma_f32_16x16x128_f8f6f4 v[36:39], v[80:87], v[88:95], 0
	v_mfma_f32_16x16x128_f8f6f4 v[40:43], v[56:63], v[96:103], 0
	v_mfma_f32_16x16x128_f8f6f4 v[44:47], v[80:87], v[96:103], 0
	v_mfma_f32_16x16x128_f8f6f4 v[48:51], v[0:7], v[64:71], 0
	v_mfma_f32_16x16x128_f8f6f4 v[52:55], v[8:15], v[64:71], 0
	v_mfma_f32_16x16x128_f8f6f4 v[64:67], v[0:7], v[72:79], 0
	v_mfma_f32_16x16x128_f8f6f4 v[68:71], v[8:15], v[72:79], 0
	v_mfma_f32_16x16x128_f8f6f4 v[72:75], v[0:7], v[88:95], 0
	v_mfma_f32_16x16x128_f8f6f4 v[76:79], v[8:15], v[88:95], 0
	v_mfma_f32_16x16x128_f8f6f4 v[128:131], v[0:7], v[96:103], 0
	v_mfma_f32_16x16x128_f8f6f4 v[132:135], v[8:15], v[96:103], 0
	s_setprio 0
	s_barrier
	v_mov_b32_e32 v120, v194
	s_mov_b64 s[40:41], s[14:15]
	s_add_i32 s19, s61, s27
	ds_read_b128 v[88:91], v199 offset:16384
	ds_read_b128 v[92:95], v199 offset:17408
	ds_read_b128 v[96:99], v199 offset:18432
	ds_read_b128 v[100:103], v199 offset:19456
	ds_read_b128 v[104:107], v199 offset:20480
	ds_read_b128 v[108:111], v199 offset:21504
	ds_read_b128 v[112:115], v199 offset:22528
	ds_read_b128 v[116:119], v199 offset:23552
	s_mov_b32 m0, s19
	s_nop 0
	global_load_lds_dwordx4 v120, s[40:41]
	s_add_u32 s40, s14, 0x4000
	s_addc_u32 s41, s15, 0
	s_add_i32 m0, s19, 0x2000
	s_nop 0
	global_load_lds_dwordx4 v194, s[40:41]
	s_add_u32 s40, s14, 0x8000
	s_addc_u32 s41, s15, 0
	s_add_i32 s19, s62, s27
	s_mov_b32 m0, s19
	s_nop 0
	global_load_lds_dwordx4 v194, s[40:41]
	s_add_u32 s40, s14, 0xc000
	s_addc_u32 s41, s15, 0
	s_add_i32 m0, s19, 0x2000
	s_nop 0
	global_load_lds_dwordx4 v194, s[40:41]
	v_mov_b32_e32 v120, v195
	s_mov_b64 s[40:41], s[34:35]
	s_mov_b32 m0, s50
	s_nop 0
	global_load_lds_dwordx4 v120, s[40:41] sc1
	s_add_u32 s40, s34, 0x4000
	v_mov_b32_e32 v120, v195
	s_addc_u32 s41, s35, 0
	s_mov_b32 m0, s51
	s_nop 0
	global_load_lds_dwordx4 v120, s[40:41] sc1
	s_waitcnt vmcnt(8)
	s_waitcnt lgkmcnt(0)
	s_barrier
	s_setprio 3
	v_mfma_f32_16x16x128_f8f6f4 v[136:139], v[56:63], v[88:95], 0
	v_mfma_f32_16x16x128_f8f6f4 v[140:143], v[80:87], v[88:95], 0
	v_mfma_f32_16x16x128_f8f6f4 v[144:147], v[56:63], v[96:103], 0
	v_mfma_f32_16x16x128_f8f6f4 v[148:151], v[80:87], v[96:103], 0
	v_mfma_f32_16x16x128_f8f6f4 v[152:155], v[56:63], v[104:111], 0
	v_mfma_f32_16x16x128_f8f6f4 v[156:159], v[80:87], v[104:111], 0
	v_mfma_f32_16x16x128_f8f6f4 v[160:163], v[56:63], v[112:119], 0
	v_mfma_f32_16x16x128_f8f6f4 v[164:167], v[80:87], v[112:119], 0
	v_mfma_f32_16x16x128_f8f6f4 v[168:171], v[0:7], v[88:95], 0
	v_mfma_f32_16x16x128_f8f6f4 v[176:179], v[0:7], v[96:103], 0
	v_mfma_f32_16x16x128_f8f6f4 v[184:187], v[0:7], v[104:111], 0
	v_mfma_f32_16x16x128_f8f6f4 v[0:3], v[0:7], v[112:119], 0
	v_mfma_f32_16x16x128_f8f6f4 v[4:7], v[8:15], v[112:119], 0
	v_mfma_f32_16x16x128_f8f6f4 v[172:175], v[8:15], v[88:95], 0
	v_mfma_f32_16x16x128_f8f6f4 v[180:183], v[8:15], v[96:103], 0
	v_mfma_f32_16x16x128_f8f6f4 v[188:191], v[8:15], v[104:111], 0
	s_setprio 0
	s_barrier
	s_add_i32 s19, 0, 0x18000
	v_add_u32_e32 v56, s19, v196
	s_add_i32 s29, 0, 0x1c000
	ds_read_b128 v[8:11], v56
	ds_read_b128 v[12:15], v56 offset:1024
	ds_read_b128 v[200:203], v56 offset:2048
	ds_read_b128 v[204:207], v56 offset:3072
	v_add_u32_e32 v56, s29, v196
	ds_read_b128 v[208:211], v56
	ds_read_b128 v[212:215], v56 offset:1024
	ds_read_b128 v[216:219], v56 offset:2048
	ds_read_b128 v[220:223], v56 offset:3072
	s_add_u32 s40, s34, 0x8000
	v_mov_b32_e32 v56, v195
	s_addc_u32 s41, s35, 0
	s_mov_b32 m0, s52
	ds_read_b128 v[88:91], v199 offset:32768
	ds_read_b128 v[92:95], v199 offset:33792
	ds_read_b128 v[224:227], v199 offset:34816
	ds_read_b128 v[228:231], v199 offset:35840
	ds_read_b128 v[232:235], v199 offset:36864
	ds_read_b128 v[236:239], v199 offset:37888
	ds_read_b128 v[240:243], v199 offset:38912
	ds_read_b128 v[244:247], v199 offset:39936
	s_nop 0
	global_load_lds_dwordx4 v56, s[40:41] sc1
	s_add_u32 s40, s34, 0xc000
	v_mov_b32_e32 v56, v195
	s_addc_u32 s41, s35, 0
	s_mov_b32 m0, s53
	s_nop 0
	global_load_lds_dwordx4 v56, s[40:41] sc1
	s_waitcnt vmcnt(8)
	s_waitcnt lgkmcnt(0)
	s_barrier
	s_setprio 3
	v_mfma_f32_16x16x128_f8f6f4 v[112:115], v[8:15], v[88:95], v[16:19]
	v_mfma_f32_16x16x128_f8f6f4 v[116:119], v[200:207], v[88:95], v[20:23]
	v_mfma_f32_16x16x128_f8f6f4 v[96:99], v[8:15], v[224:231], v[24:27]
	v_mfma_f32_16x16x128_f8f6f4 v[100:103], v[200:207], v[224:231], v[28:31]
	v_mfma_f32_16x16x128_f8f6f4 v[80:83], v[8:15], v[232:239], v[32:35]
	v_mfma_f32_16x16x128_f8f6f4 v[84:87], v[200:207], v[232:239], v[36:39]
	v_mfma_f32_16x16x128_f8f6f4 v[56:59], v[8:15], v[240:247], v[40:43]
	v_mfma_f32_16x16x128_f8f6f4 v[60:63], v[200:207], v[240:247], v[44:47]
	v_mfma_f32_16x16x128_f8f6f4 v[120:123], v[208:215], v[88:95], v[48:51]
	v_mfma_f32_16x16x128_f8f6f4 v[124:127], v[216:223], v[88:95], v[52:55]
	v_mfma_f32_16x16x128_f8f6f4 v[104:107], v[208:215], v[224:231], v[64:67]
	v_mfma_f32_16x16x128_f8f6f4 v[108:111], v[216:223], v[224:231], v[68:71]
	v_mfma_f32_16x16x128_f8f6f4 v[88:91], v[208:215], v[232:239], v[72:75]
	v_mfma_f32_16x16x128_f8f6f4 v[92:95], v[216:223], v[232:239], v[76:79]
	v_mfma_f32_16x16x128_f8f6f4 v[64:67], v[208:215], v[240:247], v[128:131]
	v_mfma_f32_16x16x128_f8f6f4 v[68:71], v[216:223], v[240:247], v[132:135]
	s_setprio 0
	s_barrier
	v_mov_b32_e32 v24, v194
	s_add_i32 s19, s19, s27
	ds_read_b128 v[16:19], v199 offset:49152
	ds_read_b128 v[20:23], v199 offset:50176
	ds_read_b128 v[128:131], v199 offset:51200
	ds_read_b128 v[132:135], v199 offset:52224
	ds_read_b128 v[224:227], v199 offset:53248
	ds_read_b128 v[228:231], v199 offset:54272
	ds_read_b128 v[232:235], v199 offset:55296
	ds_read_b128 v[236:239], v199 offset:56320
	s_mov_b32 m0, s19
	s_add_u32 s40, s14, 0x4080
	s_addc_u32 s41, s15, 0
	global_load_lds_dwordx4 v24, s[44:45]
	s_add_i32 m0, s19, 0x2000
	s_nop 0
	global_load_lds_dwordx4 v194, s[40:41]
	s_add_u32 s40, s14, 0x8080
	s_addc_u32 s41, s15, 0
	s_add_i32 s19, s29, s27
	s_mov_b32 m0, s19
	s_nop 0
	global_load_lds_dwordx4 v194, s[40:41]
	s_add_u32 s40, s14, 0xc080
	s_addc_u32 s41, s15, 0
	s_add_i32 m0, s19, 0x2000
	s_nop 0
	global_load_lds_dwordx4 v194, s[40:41]
	v_mov_b32_e32 v24, v195
	s_mov_b32 m0, s56
	s_add_u32 s40, s34, 0x4080
	s_addc_u32 s41, s35, 0
	global_load_lds_dwordx4 v24, s[42:43] sc1
	v_mov_b32_e32 v24, v195
	s_mov_b32 m0, s57
	s_nop 0
	global_load_lds_dwordx4 v24, s[40:41] sc1
	s_waitcnt vmcnt(8)
	s_waitcnt lgkmcnt(0)
	s_barrier
	s_setprio 3
	v_mfma_f32_16x16x128_f8f6f4 v[48:51], v[8:15], v[16:23], v[136:139]
	v_mfma_f32_16x16x128_f8f6f4 v[52:55], v[200:207], v[16:23], v[140:143]
	v_mfma_f32_16x16x128_f8f6f4 v[32:35], v[8:15], v[128:135], v[144:147]
	v_mfma_f32_16x16x128_f8f6f4 v[36:39], v[200:207], v[128:135], v[148:151]
	v_mfma_f32_16x16x128_f8f6f4 v[24:27], v[8:15], v[224:231], v[152:155]
	v_mfma_f32_16x16x128_f8f6f4 v[28:31], v[200:207], v[224:231], v[156:159]
	v_mfma_f32_16x16x128_f8f6f4 v[8:11], v[8:15], v[232:239], v[160:163]
	v_mfma_f32_16x16x128_f8f6f4 v[12:15], v[200:207], v[232:239], v[164:167]
	v_mfma_f32_16x16x128_f8f6f4 v[72:75], v[208:215], v[16:23], v[168:171]
	v_mfma_f32_16x16x128_f8f6f4 v[76:79], v[216:223], v[16:23], v[172:175]
	v_mfma_f32_16x16x128_f8f6f4 v[40:43], v[208:215], v[128:135], v[176:179]
	v_mfma_f32_16x16x128_f8f6f4 v[44:47], v[216:223], v[128:135], v[180:183]
	v_mfma_f32_16x16x128_f8f6f4 v[16:19], v[208:215], v[224:231], v[184:187]
	v_mfma_f32_16x16x128_f8f6f4 v[20:23], v[216:223], v[224:231], v[188:191]
	v_mfma_f32_16x16x128_f8f6f4 v[0:3], v[208:215], v[232:239], v[0:3]
	v_mfma_f32_16x16x128_f8f6f4 v[4:7], v[216:223], v[232:239], v[4:7]
	s_setprio 0
	s_barrier
	s_andn2_b64 vcc, exec, s[22:23]
	s_cbranch_vccnz .LBB0_2726
	s_barrier

.LBB0_2883:
	s_add_i32 s4, 0, 0x24808
	v_mov_b32_e32 v3, s4
	ds_read_b32 v4, v3
	s_mov_b64 s[0:1], exec
	v_mbcnt_lo_u32_b32 v2, s0, 0
	v_mbcnt_hi_u32_b32 v2, s1, v2
	v_cmp_eq_u32_e32 vcc, 0, v2
	s_waitcnt lgkmcnt(0)
	v_add_u32_e32 v4, 1, v4
	v_mov_b32_e32 v7, v4
	ds_write_b32 v3, v4
	s_and_saveexec_b64 s[4:5], vcc
	s_cbranch_execz .LBB0_2885
	v_readlane_b32 s6, v249, 34
	s_lshl_b32 s6, s6, 8
	s_add_u32 s6, s94, s6
	s_addc_u32 s7, s95, 0
	s_bcnt1_i32_b64 s0, s[0:1]
	v_mov_b32_e32 v3, 0x1000
	v_mov_b32_e32 v4, s0
	global_atomic_add v3, v3, v4, s[6:7] offset:1024 sc0
.LBB0_2885:
	s_or_b64 exec, exec, s[4:5]
	s_waitcnt vmcnt(0)
	v_readfirstlane_b32 s0, v3
	s_nop 1
	v_add_u32_e32 v2, s0, v2
	v_add_u32_e32 v5, 1, v2
	v_mul_lo_u32 v1, v1, v7
	v_add_u32_e32 v2, -1, v7
	v_cmp_eq_u32_e64 s[0:1], v5, v1
	v_cmp_ne_u32_e32 vcc, v5, v1
	s_nop 0
	v_cndmask_b32_e64 v1, 0, 1, s[0:1]
	s_add_i32 s0, 0, 0x2480c
	v_mov_b32_e32 v3, s0
	s_add_i32 s0, 0, 0x24810
	ds_write_b32 v3, v1
	v_mov_b32_e32 v1, s0
	ds_write_b32 v1, v2
	s_and_saveexec_b64 s[0:1], vcc
	s_xor_b64 s[0:1], exec, s[0:1]
	s_cbranch_execz .LBB0_2888
	s_add_i32 s4, 0, 0x24808
	v_mov_b32_e32 v0, s4
	ds_read_b32 v0, v0
	s_waitcnt lgkmcnt(0)
	v_and_b32_e32 v0, 1, v0
	v_cmp_eq_u32_e32 vcc, 0, v0
	s_cbranch_vccnz .LBB0_2888
	buffer_inv sc1
	s_waitcnt vmcnt(0)
.LBB0_2888:
	s_andn2_saveexec_b64 s[0:1], s[0:1]
	s_cbranch_execz .LBB0_2895
	s_mov_b64 s[0:1], exec
	buffer_wbl2 sc1
	s_waitcnt lgkmcnt(0)
	s_waitcnt vmcnt(0)
	v_mbcnt_lo_u32_b32 v1, s0, 0
	v_mbcnt_hi_u32_b32 v1, s1, v1
	v_cmp_eq_u32_e32 vcc, 0, v1
	s_and_saveexec_b64 s[4:5], vcc
	s_cbranch_execz .LBB0_2891
	s_bcnt1_i32_b64 s0, s[0:1]
	v_mov_b32_e32 v2, 0x3000
	v_mov_b32_e32 v3, s0
	global_atomic_add v2, v3, s[94:95] offset:1024
.LBB0_2891:
	s_or_b64 exec, exec, s[4:5]
	s_branch .LBB0_2895
	v_cvt_f32_u32_e32 v3, v0
	s_waitcnt vmcnt(0)
	v_readfirstlane_b32 s0, v2
	v_sub_u32_e32 v2, 0, v0
	v_rcp_iflag_f32_e32 v3, v3
	v_add_u32_e32 v1, s0, v1
	v_mul_f32_e32 v3, 0x4f7ffffe, v3
	v_cvt_u32_f32_e32 v3, v3
	v_mul_lo_u32 v2, v2, v3
	v_mul_hi_u32 v2, v3, v2
	v_add_u32_e32 v2, v3, v2
	v_mul_hi_u32 v2, v1, v2
	v_mul_lo_u32 v3, v2, v0
	v_sub_u32_e32 v3, v1, v3
	v_add_u32_e32 v4, 1, v2
	v_cmp_ge_u32_e32 vcc, v3, v0
	v_add_u32_e32 v1, 1, v1
	s_nop 0
	v_cndmask_b32_e32 v2, v2, v4, vcc
	v_sub_u32_e32 v4, v3, v0
	v_cndmask_b32_e32 v3, v3, v4, vcc
	v_add_u32_e32 v4, 1, v2
	v_cmp_ge_u32_e32 vcc, v3, v0
	s_nop 1
	v_cndmask_b32_e32 v2, v2, v4, vcc
	v_mul_lo_u32 v2, v0, v2
	v_add_u32_e32 v0, v2, v0
	v_cmp_eq_u32_e32 vcc, v1, v0
	s_and_saveexec_b64 s[0:1], vcc
	s_cbranch_execz .LBB0_2894
	s_mov_b64 s[4:5], exec
	v_mbcnt_lo_u32_b32 v0, s4, 0
	v_mbcnt_hi_u32_b32 v0, s5, v0
	v_cmp_eq_u32_e32 vcc, 0, v0
	s_and_b64 s[6:7], exec, vcc
	s_mov_b64 exec, s[6:7]
	s_cbranch_execz .LBB0_2894
	s_bcnt1_i32_b64 s4, s[4:5]
	v_mov_b32_e32 v0, 0x3000
	v_mov_b32_e32 v1, s4
	global_atomic_add v0, v1, s[94:95] offset:1280
